# E6 with GEMM s_setprio toggles inverted (priority 1 during the stage-load / ds_read segments, 0 during MFMA blocks) and attention toggles removed
# baseline (speedup 1.0000x reference)
.LBB0_259:
	s_waitcnt vmcnt(0)
	ds_read_b128 v[170:173], v161
	ds_read_b128 v[174:177], v161 offset:1024
	ds_read_b128 v[178:181], v161 offset:2048
	ds_read_b128 v[182:185], v161 offset:3072
	ds_read_b128 v[186:189], v165
	ds_read_b128 v[190:193], v165 offset:1024
	ds_read_b128 v[194:197], v165 offset:2048
	ds_read_b128 v[198:201], v165 offset:3072
	s_add_u32 s36, s30, 0x100
	s_addc_u32 s37, s31, 0
	s_cmp_eq_u32 s29, 12
	s_cselect_b32 s41, s25, s37
	s_cselect_b32 s40, s24, s36
	s_cselect_b32 s39, s27, s23
	s_cselect_b32 s38, s26, s21
	v_lshl_add_u64 v[150:151], s[30:31], 0, v[140:141]
	s_add_i32 m0, s53, 0xc000
	ds_read_b128 v[202:205], v169
	ds_read_b128 v[206:209], v169 offset:1024
	ds_read_b128 v[210:213], v169 offset:2048
	ds_read_b128 v[214:217], v169 offset:3072
	ds_read_b128 v[218:221], v169 offset:4096
	ds_read_b128 v[222:225], v169 offset:5120
	ds_read_b128 v[226:229], v169 offset:6144
	ds_read_b128 v[230:233], v169 offset:7168
	global_load_lds_dwordx4 v[150:151], off
	v_lshl_add_u64 v[150:151], s[30:31], 0, v[138:139]
	s_add_i32 m0, s53, 0xe000
	s_nop 0
	global_load_lds_dwordx4 v[150:151], off
	s_waitcnt vmcnt(8)
	s_waitcnt lgkmcnt(0)
	s_barrier
	s_setprio 0
	s_waitcnt lgkmcnt(0)
	v_mfma_f32_16x16x32_bf16 v[124:127], v[170:173], v[202:205], v[124:127]
	v_mfma_f32_16x16x32_bf16 v[120:123], v[178:181], v[202:205], v[120:123]
	v_mfma_f32_16x16x32_bf16 v[112:115], v[170:173], v[210:213], v[112:115]
	v_mfma_f32_16x16x32_bf16 v[104:107], v[178:181], v[210:213], v[104:107]
	v_mfma_f32_16x16x32_bf16 v[96:99], v[170:173], v[218:221], v[96:99]
	v_mfma_f32_16x16x32_bf16 v[88:91], v[178:181], v[218:221], v[88:91]
	v_mfma_f32_16x16x32_bf16 v[80:83], v[170:173], v[226:229], v[80:83]
	v_mfma_f32_16x16x32_bf16 v[72:75], v[178:181], v[226:229], v[72:75]
	v_mfma_f32_16x16x32_bf16 v[124:127], v[174:177], v[206:209], v[124:127]
	v_mfma_f32_16x16x32_bf16 v[120:123], v[182:185], v[206:209], v[120:123]
	v_mfma_f32_16x16x32_bf16 v[112:115], v[174:177], v[214:217], v[112:115]
	v_mfma_f32_16x16x32_bf16 v[104:107], v[182:185], v[214:217], v[104:107]
	v_mfma_f32_16x16x32_bf16 v[96:99], v[174:177], v[222:225], v[96:99]
	v_mfma_f32_16x16x32_bf16 v[88:91], v[182:185], v[222:225], v[88:91]
	v_mfma_f32_16x16x32_bf16 v[80:83], v[174:177], v[230:233], v[80:83]
	v_mfma_f32_16x16x32_bf16 v[72:75], v[182:185], v[230:233], v[72:75]
	s_setprio 1
	s_setprio 0
	v_mfma_f32_16x16x32_bf16 v[116:119], v[186:189], v[202:205], v[116:119]
	v_mfma_f32_16x16x32_bf16 v[108:111], v[194:197], v[202:205], v[108:111]
	v_mfma_f32_16x16x32_bf16 v[100:103], v[186:189], v[210:213], v[100:103]
	v_mfma_f32_16x16x32_bf16 v[92:95], v[194:197], v[210:213], v[92:95]
	v_mfma_f32_16x16x32_bf16 v[84:87], v[186:189], v[218:221], v[84:87]
	v_mfma_f32_16x16x32_bf16 v[76:79], v[194:197], v[218:221], v[76:79]
	v_mfma_f32_16x16x32_bf16 v[68:71], v[186:189], v[226:229], v[68:71]
	v_mfma_f32_16x16x32_bf16 v[64:67], v[194:197], v[226:229], v[64:67]
	v_mfma_f32_16x16x32_bf16 v[116:119], v[190:193], v[206:209], v[116:119]
	v_mfma_f32_16x16x32_bf16 v[108:111], v[198:201], v[206:209], v[108:111]
	v_mfma_f32_16x16x32_bf16 v[100:103], v[190:193], v[214:217], v[100:103]
	v_mfma_f32_16x16x32_bf16 v[92:95], v[198:201], v[214:217], v[92:95]
	v_mfma_f32_16x16x32_bf16 v[84:87], v[190:193], v[222:225], v[84:87]
	v_mfma_f32_16x16x32_bf16 v[76:79], v[198:201], v[222:225], v[76:79]
	v_mfma_f32_16x16x32_bf16 v[68:71], v[190:193], v[230:233], v[68:71]
	v_mfma_f32_16x16x32_bf16 v[64:67], v[198:201], v[230:233], v[64:67]
	s_setprio 1
	s_barrier
	s_add_i32 s30, s61, s50
	v_lshl_add_u64 v[150:151], s[38:39], 0, v[132:133]
	s_mov_b32 m0, s30
	ds_read_b128 v[202:205], v169 offset:16384
	ds_read_b128 v[206:209], v169 offset:17408
	ds_read_b128 v[210:213], v169 offset:18432
	ds_read_b128 v[214:217], v169 offset:19456
	ds_read_b128 v[218:221], v169 offset:20480
	ds_read_b128 v[222:225], v169 offset:21504
	ds_read_b128 v[226:229], v169 offset:22528
	ds_read_b128 v[230:233], v169 offset:23552
	global_load_lds_dwordx4 v[150:151], off
	s_add_i32 m0, s30, 0x2000
	s_add_u32 s30, s38, 0x40000
	v_lshl_add_u64 v[154:155], s[38:39], 0, v[128:129]
	s_addc_u32 s31, s39, 0
	s_add_i32 s64, s62, s50
	global_load_lds_dwordx4 v[154:155], off
	v_lshl_add_u64 v[158:159], s[30:31], 0, v[132:133]
	s_mov_b32 m0, s64
	v_lshl_add_u64 v[162:163], s[40:41], 0, v[130:131]
	global_load_lds_dwordx4 v[158:159], off
	v_lshl_add_u64 v[158:159], s[30:31], 0, v[128:129]
	s_add_i32 m0, s64, 0x2000
	s_nop 0
	global_load_lds_dwordx4 v[158:159], off
	v_lshl_add_u64 v[158:159], s[40:41], 0, v[134:135]
	s_mov_b32 m0, s53
	s_nop 0
	global_load_lds_dwordx4 v[158:159], off
	s_mov_b32 m0, s54
	s_nop 0
	global_load_lds_dwordx4 v[162:163], off
	s_waitcnt vmcnt(8)
	s_waitcnt lgkmcnt(0)
	s_barrier
	s_setprio 0
	s_waitcnt lgkmcnt(0)
	v_mfma_f32_16x16x32_bf16 v[60:63], v[170:173], v[202:205], v[60:63]
	v_mfma_f32_16x16x32_bf16 v[56:59], v[178:181], v[202:205], v[56:59]
	v_mfma_f32_16x16x32_bf16 v[48:51], v[170:173], v[210:213], v[48:51]
	v_mfma_f32_16x16x32_bf16 v[40:43], v[178:181], v[210:213], v[40:43]
	v_mfma_f32_16x16x32_bf16 v[32:35], v[170:173], v[218:221], v[32:35]
	v_mfma_f32_16x16x32_bf16 v[24:27], v[178:181], v[218:221], v[24:27]
	v_mfma_f32_16x16x32_bf16 v[16:19], v[170:173], v[226:229], v[16:19]
	v_mfma_f32_16x16x32_bf16 v[8:11], v[178:181], v[226:229], v[8:11]
	v_mfma_f32_16x16x32_bf16 v[60:63], v[174:177], v[206:209], v[60:63]
	v_mfma_f32_16x16x32_bf16 v[56:59], v[182:185], v[206:209], v[56:59]
	v_mfma_f32_16x16x32_bf16 v[48:51], v[174:177], v[214:217], v[48:51]
	v_mfma_f32_16x16x32_bf16 v[40:43], v[182:185], v[214:217], v[40:43]
	v_mfma_f32_16x16x32_bf16 v[32:35], v[174:177], v[222:225], v[32:35]
	v_mfma_f32_16x16x32_bf16 v[24:27], v[182:185], v[222:225], v[24:27]
	v_mfma_f32_16x16x32_bf16 v[16:19], v[174:177], v[230:233], v[16:19]
	v_mfma_f32_16x16x32_bf16 v[8:11], v[182:185], v[230:233], v[8:11]
	s_setprio 1
	s_setprio 0
	v_mfma_f32_16x16x32_bf16 v[52:55], v[186:189], v[202:205], v[52:55]
	v_mfma_f32_16x16x32_bf16 v[44:47], v[194:197], v[202:205], v[44:47]
	v_mfma_f32_16x16x32_bf16 v[36:39], v[186:189], v[210:213], v[36:39]
	v_mfma_f32_16x16x32_bf16 v[28:31], v[194:197], v[210:213], v[28:31]
	v_mfma_f32_16x16x32_bf16 v[20:23], v[186:189], v[218:221], v[20:23]
	v_mfma_f32_16x16x32_bf16 v[12:15], v[194:197], v[218:221], v[12:15]
	v_mfma_f32_16x16x32_bf16 v[4:7], v[186:189], v[226:229], v[4:7]
	v_mfma_f32_16x16x32_bf16 v[0:3], v[194:197], v[226:229], v[0:3]
	v_mfma_f32_16x16x32_bf16 v[52:55], v[190:193], v[206:209], v[52:55]
	v_mfma_f32_16x16x32_bf16 v[44:47], v[198:201], v[206:209], v[44:47]
	v_mfma_f32_16x16x32_bf16 v[36:39], v[190:193], v[214:217], v[36:39]
	v_mfma_f32_16x16x32_bf16 v[28:31], v[198:201], v[214:217], v[28:31]
	v_mfma_f32_16x16x32_bf16 v[20:23], v[190:193], v[222:225], v[20:23]
	v_mfma_f32_16x16x32_bf16 v[12:15], v[198:201], v[222:225], v[12:15]
	v_mfma_f32_16x16x32_bf16 v[4:7], v[190:193], v[230:233], v[4:7]
	v_mfma_f32_16x16x32_bf16 v[0:3], v[198:201], v[230:233], v[0:3]
	s_setprio 1
	s_barrier
	s_add_i32 s64, 0, 0x18000
	v_add_u32_e32 v136, s64, v149
	s_add_i32 s65, 0, 0x1c000
	ds_read_b128 v[170:173], v136
	ds_read_b128 v[174:177], v136 offset:1024
	ds_read_b128 v[178:181], v136 offset:2048
	ds_read_b128 v[182:185], v136 offset:3072
	v_add_u32_e32 v136, s65, v149
	ds_read_b128 v[186:189], v136
	ds_read_b128 v[190:193], v136 offset:1024
	ds_read_b128 v[194:197], v136 offset:2048
	ds_read_b128 v[198:201], v136 offset:3072
	s_add_u32 s30, s40, 0x40000
	s_addc_u32 s31, s41, 0
	s_mov_b32 m0, s55
	v_lshl_add_u64 v[166:167], s[30:31], 0, v[134:135]
	ds_read_b128 v[202:205], v169 offset:32768
	ds_read_b128 v[206:209], v169 offset:33792
	ds_read_b128 v[210:213], v169 offset:34816
	ds_read_b128 v[214:217], v169 offset:35840
	ds_read_b128 v[218:221], v169 offset:36864
	ds_read_b128 v[222:225], v169 offset:37888
	ds_read_b128 v[226:229], v169 offset:38912
	ds_read_b128 v[230:233], v169 offset:39936
	global_load_lds_dwordx4 v[166:167], off
	v_lshl_add_u64 v[166:167], s[30:31], 0, v[130:131]
	s_mov_b32 m0, s56
	s_nop 0
	global_load_lds_dwordx4 v[166:167], off
	s_waitcnt vmcnt(8)
	s_waitcnt lgkmcnt(0)
	s_barrier
	s_setprio 0
	s_waitcnt lgkmcnt(0)
	v_mfma_f32_16x16x32_bf16 v[124:127], v[170:173], v[202:205], v[124:127]
	v_mfma_f32_16x16x32_bf16 v[120:123], v[178:181], v[202:205], v[120:123]
	v_mfma_f32_16x16x32_bf16 v[112:115], v[170:173], v[210:213], v[112:115]
	v_mfma_f32_16x16x32_bf16 v[104:107], v[178:181], v[210:213], v[104:107]
	v_mfma_f32_16x16x32_bf16 v[96:99], v[170:173], v[218:221], v[96:99]
	v_mfma_f32_16x16x32_bf16 v[88:91], v[178:181], v[218:221], v[88:91]
	v_mfma_f32_16x16x32_bf16 v[80:83], v[170:173], v[226:229], v[80:83]
	v_mfma_f32_16x16x32_bf16 v[72:75], v[178:181], v[226:229], v[72:75]
	v_mfma_f32_16x16x32_bf16 v[124:127], v[174:177], v[206:209], v[124:127]
	v_mfma_f32_16x16x32_bf16 v[120:123], v[182:185], v[206:209], v[120:123]
	v_mfma_f32_16x16x32_bf16 v[112:115], v[174:177], v[214:217], v[112:115]
	v_mfma_f32_16x16x32_bf16 v[104:107], v[182:185], v[214:217], v[104:107]
	v_mfma_f32_16x16x32_bf16 v[96:99], v[174:177], v[222:225], v[96:99]
	v_mfma_f32_16x16x32_bf16 v[88:91], v[182:185], v[222:225], v[88:91]
	v_mfma_f32_16x16x32_bf16 v[80:83], v[174:177], v[230:233], v[80:83]
	v_mfma_f32_16x16x32_bf16 v[72:75], v[182:185], v[230:233], v[72:75]
	s_setprio 1
	s_setprio 0
	v_mfma_f32_16x16x32_bf16 v[116:119], v[186:189], v[202:205], v[116:119]
	v_mfma_f32_16x16x32_bf16 v[108:111], v[194:197], v[202:205], v[108:111]
	v_mfma_f32_16x16x32_bf16 v[100:103], v[186:189], v[210:213], v[100:103]
	v_mfma_f32_16x16x32_bf16 v[92:95], v[194:197], v[210:213], v[92:95]
	v_mfma_f32_16x16x32_bf16 v[84:87], v[186:189], v[218:221], v[84:87]
	v_mfma_f32_16x16x32_bf16 v[76:79], v[194:197], v[218:221], v[76:79]
	v_mfma_f32_16x16x32_bf16 v[68:71], v[186:189], v[226:229], v[68:71]
	v_mfma_f32_16x16x32_bf16 v[64:67], v[194:197], v[226:229], v[64:67]
	v_mfma_f32_16x16x32_bf16 v[116:119], v[190:193], v[206:209], v[116:119]
	v_mfma_f32_16x16x32_bf16 v[108:111], v[198:201], v[206:209], v[108:111]
	v_mfma_f32_16x16x32_bf16 v[100:103], v[190:193], v[214:217], v[100:103]
	v_mfma_f32_16x16x32_bf16 v[92:95], v[198:201], v[214:217], v[92:95]
	v_mfma_f32_16x16x32_bf16 v[84:87], v[190:193], v[222:225], v[84:87]
	v_mfma_f32_16x16x32_bf16 v[76:79], v[198:201], v[222:225], v[76:79]
	v_mfma_f32_16x16x32_bf16 v[68:71], v[190:193], v[230:233], v[68:71]
	v_mfma_f32_16x16x32_bf16 v[64:67], v[198:201], v[230:233], v[64:67]
	s_setprio 1
	s_barrier
	s_add_i32 s30, s64, s50
	v_lshl_add_u64 v[150:151], v[150:151], 0, s[16:17]
	s_mov_b32 m0, s30
	ds_read_b128 v[202:205], v169 offset:49152
	ds_read_b128 v[206:209], v169 offset:50176
	ds_read_b128 v[210:213], v169 offset:51200
	ds_read_b128 v[214:217], v169 offset:52224
	ds_read_b128 v[218:221], v169 offset:53248
	ds_read_b128 v[222:225], v169 offset:54272
	ds_read_b128 v[226:229], v169 offset:55296
	ds_read_b128 v[230:233], v169 offset:56320
	global_load_lds_dwordx4 v[150:151], off
	s_add_i32 m0, s30, 0x2000
	s_add_u32 s30, s38, 0x40080
	v_lshl_add_u64 v[150:151], v[154:155], 0, s[16:17]
	s_addc_u32 s31, s39, 0
	s_add_i32 s38, s65, s50
	global_load_lds_dwordx4 v[150:151], off
	v_lshl_add_u64 v[150:151], s[30:31], 0, v[132:133]
	s_mov_b32 m0, s38
	s_nop 0
	global_load_lds_dwordx4 v[150:151], off
	v_lshl_add_u64 v[150:151], s[30:31], 0, v[128:129]
	s_add_i32 m0, s38, 0x2000
	s_nop 0
	global_load_lds_dwordx4 v[150:151], off
	v_lshl_add_u64 v[150:151], v[158:159], 0, s[16:17]
	s_mov_b32 m0, s57
	s_nop 0
	global_load_lds_dwordx4 v[150:151], off
	v_lshl_add_u64 v[150:151], v[162:163], 0, s[16:17]
	s_mov_b32 m0, s58
	s_nop 0
	global_load_lds_dwordx4 v[150:151], off
	s_waitcnt vmcnt(8)
	s_waitcnt lgkmcnt(0)
	s_barrier
	s_setprio 0
	s_waitcnt lgkmcnt(0)
	v_mfma_f32_16x16x32_bf16 v[60:63], v[170:173], v[202:205], v[60:63]
	v_mfma_f32_16x16x32_bf16 v[56:59], v[178:181], v[202:205], v[56:59]
	v_mfma_f32_16x16x32_bf16 v[48:51], v[170:173], v[210:213], v[48:51]
	v_mfma_f32_16x16x32_bf16 v[40:43], v[178:181], v[210:213], v[40:43]
	v_mfma_f32_16x16x32_bf16 v[32:35], v[170:173], v[218:221], v[32:35]
	v_mfma_f32_16x16x32_bf16 v[24:27], v[178:181], v[218:221], v[24:27]
	v_mfma_f32_16x16x32_bf16 v[16:19], v[170:173], v[226:229], v[16:19]
	v_mfma_f32_16x16x32_bf16 v[8:11], v[178:181], v[226:229], v[8:11]
	v_mfma_f32_16x16x32_bf16 v[60:63], v[174:177], v[206:209], v[60:63]
	v_mfma_f32_16x16x32_bf16 v[56:59], v[182:185], v[206:209], v[56:59]
	v_mfma_f32_16x16x32_bf16 v[48:51], v[174:177], v[214:217], v[48:51]
	v_mfma_f32_16x16x32_bf16 v[40:43], v[182:185], v[214:217], v[40:43]
	v_mfma_f32_16x16x32_bf16 v[32:35], v[174:177], v[222:225], v[32:35]
	v_mfma_f32_16x16x32_bf16 v[24:27], v[182:185], v[222:225], v[24:27]
	v_mfma_f32_16x16x32_bf16 v[16:19], v[174:177], v[230:233], v[16:19]
	v_mfma_f32_16x16x32_bf16 v[8:11], v[182:185], v[230:233], v[8:11]
	s_setprio 1
	s_setprio 0
	v_mfma_f32_16x16x32_bf16 v[52:55], v[186:189], v[202:205], v[52:55]
	v_mfma_f32_16x16x32_bf16 v[44:47], v[194:197], v[202:205], v[44:47]
	v_mfma_f32_16x16x32_bf16 v[36:39], v[186:189], v[210:213], v[36:39]
	v_mfma_f32_16x16x32_bf16 v[28:31], v[194:197], v[210:213], v[28:31]
	v_mfma_f32_16x16x32_bf16 v[20:23], v[186:189], v[218:221], v[20:23]
	v_mfma_f32_16x16x32_bf16 v[12:15], v[194:197], v[218:221], v[12:15]
	v_mfma_f32_16x16x32_bf16 v[4:7], v[186:189], v[226:229], v[4:7]
	v_mfma_f32_16x16x32_bf16 v[0:3], v[194:197], v[226:229], v[0:3]
	v_mfma_f32_16x16x32_bf16 v[52:55], v[190:193], v[206:209], v[52:55]
	v_mfma_f32_16x16x32_bf16 v[44:47], v[198:201], v[206:209], v[44:47]
	v_mfma_f32_16x16x32_bf16 v[36:39], v[190:193], v[214:217], v[36:39]
	v_mfma_f32_16x16x32_bf16 v[28:31], v[198:201], v[214:217], v[28:31]
	v_mfma_f32_16x16x32_bf16 v[20:23], v[190:193], v[222:225], v[20:23]
	v_mfma_f32_16x16x32_bf16 v[12:15], v[198:201], v[222:225], v[12:15]
	v_mfma_f32_16x16x32_bf16 v[4:7], v[190:193], v[230:233], v[4:7]
	v_mfma_f32_16x16x32_bf16 v[0:3], v[198:201], v[230:233], v[0:3]
	s_setprio 1
	s_barrier
	s_add_i32 s29, s29, 2
	s_add_u32 s21, s21, 0x100
	s_addc_u32 s23, s23, 0
	s_cmp_gt_u32 s29, 13
	s_mov_b64 s[30:31], s[36:37]
	s_cbranch_scc0 .LBB0_259
	s_and_b64 vcc, exec, s[18:19]
	s_cbranch_vccz .LBB0_262
	s_barrier

.LBB0_430:
	ds_read_b128 v[112:115], v245
	ds_read_b128 v[116:119], v245 offset:1024
	ds_read_b128 v[124:127], v245 offset:2048
	ds_read_b128 v[128:131], v245 offset:3072
	ds_read_b128 v[136:139], v246
	ds_read_b128 v[140:143], v246 offset:1024
	ds_read_b128 v[148:151], v246 offset:2048
	ds_read_b128 v[156:159], v246 offset:3072
	s_add_u32 s36, s30, 0x100
	s_addc_u32 s37, s31, 0
	s_cmp_eq_u32 s64, 12
	s_cselect_b32 s41, s27, s37
	s_cselect_b32 s40, s26, s36
	s_cselect_b32 s39, s29, s25
	s_cselect_b32 s38, s28, s23
	v_lshl_add_u64 v[208:209], s[30:31], 0, v[202:203]
	s_add_i32 m0, s51, 0xc000
	ds_read_b128 v[160:163], v247
	ds_read_b128 v[164:167], v247 offset:1024
	ds_read_b128 v[168:171], v247 offset:2048
	ds_read_b128 v[172:175], v247 offset:3072
	ds_read_b128 v[176:179], v247 offset:4096
	ds_read_b128 v[180:183], v247 offset:5120
	ds_read_b128 v[184:187], v247 offset:6144
	ds_read_b128 v[188:191], v247 offset:7168
	global_load_lds_dwordx4 v[208:209], off
	v_lshl_add_u64 v[208:209], s[30:31], 0, v[200:201]
	s_add_i32 m0, s51, 0xe000
	s_nop 0
	global_load_lds_dwordx4 v[208:209], off
	s_waitcnt vmcnt(8)
	s_waitcnt lgkmcnt(0)
	s_barrier
	s_setprio 0
	s_waitcnt lgkmcnt(0)
	v_mfma_f32_16x16x32_bf16 v[152:155], v[112:115], v[160:163], v[152:155]
	v_mfma_f32_16x16x32_bf16 v[144:147], v[124:127], v[160:163], v[144:147]
	v_mfma_f32_16x16x32_bf16 v[108:111], v[112:115], v[168:171], v[108:111]
	v_mfma_f32_16x16x32_bf16 v[104:107], v[124:127], v[168:171], v[104:107]
	v_mfma_f32_16x16x32_bf16 v[92:95], v[112:115], v[176:179], v[92:95]
	v_mfma_f32_16x16x32_bf16 v[88:91], v[124:127], v[176:179], v[88:91]
	v_mfma_f32_16x16x32_bf16 v[76:79], v[112:115], v[184:187], v[76:79]
	v_mfma_f32_16x16x32_bf16 v[72:75], v[124:127], v[184:187], v[72:75]
	v_mfma_f32_16x16x32_bf16 v[152:155], v[116:119], v[164:167], v[152:155]
	v_mfma_f32_16x16x32_bf16 v[144:147], v[128:131], v[164:167], v[144:147]
	v_mfma_f32_16x16x32_bf16 v[108:111], v[116:119], v[172:175], v[108:111]
	v_mfma_f32_16x16x32_bf16 v[104:107], v[128:131], v[172:175], v[104:107]
	v_mfma_f32_16x16x32_bf16 v[92:95], v[116:119], v[180:183], v[92:95]
	v_mfma_f32_16x16x32_bf16 v[88:91], v[128:131], v[180:183], v[88:91]
	v_mfma_f32_16x16x32_bf16 v[76:79], v[116:119], v[188:191], v[76:79]
	v_mfma_f32_16x16x32_bf16 v[72:75], v[128:131], v[188:191], v[72:75]
	s_setprio 1
	s_setprio 0
	v_mfma_f32_16x16x32_bf16 v[132:135], v[136:139], v[160:163], v[132:135]
	v_mfma_f32_16x16x32_bf16 v[120:123], v[148:151], v[160:163], v[120:123]
	v_mfma_f32_16x16x32_bf16 v[100:103], v[136:139], v[168:171], v[100:103]
	v_mfma_f32_16x16x32_bf16 v[96:99], v[148:151], v[168:171], v[96:99]
	v_mfma_f32_16x16x32_bf16 v[84:87], v[136:139], v[176:179], v[84:87]
	v_mfma_f32_16x16x32_bf16 v[80:83], v[148:151], v[176:179], v[80:83]
	v_mfma_f32_16x16x32_bf16 v[68:71], v[136:139], v[184:187], v[68:71]
	v_mfma_f32_16x16x32_bf16 v[64:67], v[148:151], v[184:187], v[64:67]
	v_mfma_f32_16x16x32_bf16 v[132:135], v[140:143], v[164:167], v[132:135]
	v_mfma_f32_16x16x32_bf16 v[120:123], v[156:159], v[164:167], v[120:123]
	v_mfma_f32_16x16x32_bf16 v[100:103], v[140:143], v[172:175], v[100:103]
	v_mfma_f32_16x16x32_bf16 v[96:99], v[156:159], v[172:175], v[96:99]
	v_mfma_f32_16x16x32_bf16 v[84:87], v[140:143], v[180:183], v[84:87]
	v_mfma_f32_16x16x32_bf16 v[80:83], v[156:159], v[180:183], v[80:83]
	v_mfma_f32_16x16x32_bf16 v[68:71], v[140:143], v[188:191], v[68:71]
	v_mfma_f32_16x16x32_bf16 v[64:67], v[156:159], v[188:191], v[64:67]
	s_setprio 1
	s_barrier
	s_add_i32 s30, s60, s50
	v_lshl_add_u64 v[208:209], s[38:39], 0, v[194:195]
	s_mov_b32 m0, s30
	ds_read_b128 v[160:163], v247 offset:16384
	ds_read_b128 v[164:167], v247 offset:17408
	ds_read_b128 v[168:171], v247 offset:18432
	ds_read_b128 v[172:175], v247 offset:19456
	ds_read_b128 v[176:179], v247 offset:20480
	ds_read_b128 v[180:183], v247 offset:21504
	ds_read_b128 v[184:187], v247 offset:22528
	ds_read_b128 v[188:191], v247 offset:23552
	global_load_lds_dwordx4 v[208:209], off
	s_add_i32 m0, s30, 0x2000
	s_add_u32 s30, s38, 0x40000
	v_lshl_add_u64 v[210:211], s[38:39], 0, v[198:199]
	s_addc_u32 s31, s39, 0
	s_add_i32 s65, s61, s50
	global_load_lds_dwordx4 v[210:211], off
	v_lshl_add_u64 v[212:213], s[30:31], 0, v[194:195]
	s_mov_b32 m0, s65
	v_lshl_add_u64 v[214:215], s[40:41], 0, v[196:197]
	global_load_lds_dwordx4 v[212:213], off
	v_lshl_add_u64 v[212:213], s[30:31], 0, v[198:199]
	s_add_i32 m0, s65, 0x2000
	s_nop 0
	global_load_lds_dwordx4 v[212:213], off
	v_lshl_add_u64 v[212:213], s[40:41], 0, v[192:193]
	s_mov_b32 m0, s51
	s_nop 0
	global_load_lds_dwordx4 v[212:213], off
	s_mov_b32 m0, s52
	s_nop 0
	global_load_lds_dwordx4 v[214:215], off
	s_waitcnt vmcnt(8)
	s_waitcnt lgkmcnt(0)
	s_barrier
	s_setprio 0
	s_waitcnt lgkmcnt(0)
	v_mfma_f32_16x16x32_bf16 v[60:63], v[112:115], v[160:163], v[60:63]
	v_mfma_f32_16x16x32_bf16 v[56:59], v[124:127], v[160:163], v[56:59]
	v_mfma_f32_16x16x32_bf16 v[44:47], v[112:115], v[168:171], v[44:47]
	v_mfma_f32_16x16x32_bf16 v[40:43], v[124:127], v[168:171], v[40:43]
	v_mfma_f32_16x16x32_bf16 v[28:31], v[112:115], v[176:179], v[28:31]
	v_mfma_f32_16x16x32_bf16 v[24:27], v[124:127], v[176:179], v[24:27]
	v_mfma_f32_16x16x32_bf16 v[12:15], v[112:115], v[184:187], v[12:15]
	v_mfma_f32_16x16x32_bf16 v[8:11], v[124:127], v[184:187], v[8:11]
	v_mfma_f32_16x16x32_bf16 v[60:63], v[116:119], v[164:167], v[60:63]
	v_mfma_f32_16x16x32_bf16 v[56:59], v[128:131], v[164:167], v[56:59]
	v_mfma_f32_16x16x32_bf16 v[44:47], v[116:119], v[172:175], v[44:47]
	v_mfma_f32_16x16x32_bf16 v[40:43], v[128:131], v[172:175], v[40:43]
	v_mfma_f32_16x16x32_bf16 v[28:31], v[116:119], v[180:183], v[28:31]
	v_mfma_f32_16x16x32_bf16 v[24:27], v[128:131], v[180:183], v[24:27]
	v_mfma_f32_16x16x32_bf16 v[12:15], v[116:119], v[188:191], v[12:15]
	v_mfma_f32_16x16x32_bf16 v[8:11], v[128:131], v[188:191], v[8:11]
	s_setprio 1
	s_setprio 0
	v_mfma_f32_16x16x32_bf16 v[52:55], v[136:139], v[160:163], v[52:55]
	v_mfma_f32_16x16x32_bf16 v[48:51], v[148:151], v[160:163], v[48:51]
	v_mfma_f32_16x16x32_bf16 v[36:39], v[136:139], v[168:171], v[36:39]
	v_mfma_f32_16x16x32_bf16 v[32:35], v[148:151], v[168:171], v[32:35]
	v_mfma_f32_16x16x32_bf16 v[20:23], v[136:139], v[176:179], v[20:23]
	v_mfma_f32_16x16x32_bf16 v[16:19], v[148:151], v[176:179], v[16:19]
	v_mfma_f32_16x16x32_bf16 v[4:7], v[136:139], v[184:187], v[4:7]
	v_mfma_f32_16x16x32_bf16 v[0:3], v[148:151], v[184:187], v[0:3]
	v_mfma_f32_16x16x32_bf16 v[52:55], v[140:143], v[164:167], v[52:55]
	v_mfma_f32_16x16x32_bf16 v[48:51], v[156:159], v[164:167], v[48:51]
	v_mfma_f32_16x16x32_bf16 v[36:39], v[140:143], v[172:175], v[36:39]
	v_mfma_f32_16x16x32_bf16 v[32:35], v[156:159], v[172:175], v[32:35]
	v_mfma_f32_16x16x32_bf16 v[20:23], v[140:143], v[180:183], v[20:23]
	v_mfma_f32_16x16x32_bf16 v[16:19], v[156:159], v[180:183], v[16:19]
	v_mfma_f32_16x16x32_bf16 v[4:7], v[140:143], v[188:191], v[4:7]
	v_mfma_f32_16x16x32_bf16 v[0:3], v[156:159], v[188:191], v[0:3]
	s_setprio 1
	s_barrier
	s_add_i32 s65, 0, 0x18000
	s_add_i32 s66, 0, 0x1c000
	v_add_u32_e32 v128, s65, v241
	v_add_u32_e32 v156, s66, v241
	ds_read_b128 v[112:115], v128
	ds_read_b128 v[116:119], v128 offset:1024
	ds_read_b128 v[124:127], v128 offset:2048
	ds_read_b128 v[128:131], v128 offset:3072
	ds_read_b128 v[136:139], v156
	ds_read_b128 v[140:143], v156 offset:1024
	ds_read_b128 v[148:151], v156 offset:2048
	ds_read_b128 v[156:159], v156 offset:3072
	s_add_u32 s30, s40, 0x40000
	s_addc_u32 s31, s41, 0
	s_mov_b32 m0, s53
	v_lshl_add_u64 v[216:217], s[30:31], 0, v[192:193]
	ds_read_b128 v[160:163], v247 offset:32768
	ds_read_b128 v[164:167], v247 offset:33792
	ds_read_b128 v[168:171], v247 offset:34816
	ds_read_b128 v[172:175], v247 offset:35840
	ds_read_b128 v[176:179], v247 offset:36864
	ds_read_b128 v[180:183], v247 offset:37888
	ds_read_b128 v[184:187], v247 offset:38912
	ds_read_b128 v[188:191], v247 offset:39936
	global_load_lds_dwordx4 v[216:217], off
	v_lshl_add_u64 v[216:217], s[30:31], 0, v[196:197]
	s_mov_b32 m0, s54
	s_nop 0
	global_load_lds_dwordx4 v[216:217], off
	s_waitcnt vmcnt(8)
	s_waitcnt lgkmcnt(0)
	s_barrier
	s_setprio 0
	s_waitcnt lgkmcnt(0)
	v_mfma_f32_16x16x32_bf16 v[152:155], v[112:115], v[160:163], v[152:155]
	v_mfma_f32_16x16x32_bf16 v[144:147], v[124:127], v[160:163], v[144:147]
	v_mfma_f32_16x16x32_bf16 v[108:111], v[112:115], v[168:171], v[108:111]
	v_mfma_f32_16x16x32_bf16 v[104:107], v[124:127], v[168:171], v[104:107]
	v_mfma_f32_16x16x32_bf16 v[92:95], v[112:115], v[176:179], v[92:95]
	v_mfma_f32_16x16x32_bf16 v[88:91], v[124:127], v[176:179], v[88:91]
	v_mfma_f32_16x16x32_bf16 v[76:79], v[112:115], v[184:187], v[76:79]
	v_mfma_f32_16x16x32_bf16 v[72:75], v[124:127], v[184:187], v[72:75]
	v_mfma_f32_16x16x32_bf16 v[152:155], v[116:119], v[164:167], v[152:155]
	v_mfma_f32_16x16x32_bf16 v[144:147], v[128:131], v[164:167], v[144:147]
	v_mfma_f32_16x16x32_bf16 v[108:111], v[116:119], v[172:175], v[108:111]
	v_mfma_f32_16x16x32_bf16 v[104:107], v[128:131], v[172:175], v[104:107]
	v_mfma_f32_16x16x32_bf16 v[92:95], v[116:119], v[180:183], v[92:95]
	v_mfma_f32_16x16x32_bf16 v[88:91], v[128:131], v[180:183], v[88:91]
	v_mfma_f32_16x16x32_bf16 v[76:79], v[116:119], v[188:191], v[76:79]
	v_mfma_f32_16x16x32_bf16 v[72:75], v[128:131], v[188:191], v[72:75]
	s_setprio 1
	s_setprio 0
	v_mfma_f32_16x16x32_bf16 v[132:135], v[136:139], v[160:163], v[132:135]
	v_mfma_f32_16x16x32_bf16 v[120:123], v[148:151], v[160:163], v[120:123]
	v_mfma_f32_16x16x32_bf16 v[100:103], v[136:139], v[168:171], v[100:103]
	v_mfma_f32_16x16x32_bf16 v[96:99], v[148:151], v[168:171], v[96:99]
	v_mfma_f32_16x16x32_bf16 v[84:87], v[136:139], v[176:179], v[84:87]
	v_mfma_f32_16x16x32_bf16 v[80:83], v[148:151], v[176:179], v[80:83]
	v_mfma_f32_16x16x32_bf16 v[68:71], v[136:139], v[184:187], v[68:71]
	v_mfma_f32_16x16x32_bf16 v[64:67], v[148:151], v[184:187], v[64:67]
	v_mfma_f32_16x16x32_bf16 v[132:135], v[140:143], v[164:167], v[132:135]
	v_mfma_f32_16x16x32_bf16 v[120:123], v[156:159], v[164:167], v[120:123]
	v_mfma_f32_16x16x32_bf16 v[100:103], v[140:143], v[172:175], v[100:103]
	v_mfma_f32_16x16x32_bf16 v[96:99], v[156:159], v[172:175], v[96:99]
	v_mfma_f32_16x16x32_bf16 v[84:87], v[140:143], v[180:183], v[84:87]
	v_mfma_f32_16x16x32_bf16 v[80:83], v[156:159], v[180:183], v[80:83]
	v_mfma_f32_16x16x32_bf16 v[68:71], v[140:143], v[188:191], v[68:71]
	v_mfma_f32_16x16x32_bf16 v[64:67], v[156:159], v[188:191], v[64:67]
	s_setprio 1
	s_barrier
	s_add_i32 s30, s65, s50
	v_lshl_add_u64 v[208:209], v[208:209], 0, s[18:19]
	s_mov_b32 m0, s30
	ds_read_b128 v[160:163], v247 offset:49152
	ds_read_b128 v[164:167], v247 offset:50176
	ds_read_b128 v[168:171], v247 offset:51200
	ds_read_b128 v[172:175], v247 offset:52224
	ds_read_b128 v[176:179], v247 offset:53248
	ds_read_b128 v[180:183], v247 offset:54272
	ds_read_b128 v[184:187], v247 offset:55296
	ds_read_b128 v[188:191], v247 offset:56320
	global_load_lds_dwordx4 v[208:209], off
	s_add_i32 m0, s30, 0x2000
	s_add_u32 s30, s38, 0x40080
	v_lshl_add_u64 v[208:209], v[210:211], 0, s[18:19]
	s_addc_u32 s31, s39, 0
	s_add_i32 s38, s66, s50
	global_load_lds_dwordx4 v[208:209], off
	v_lshl_add_u64 v[208:209], s[30:31], 0, v[194:195]
	s_mov_b32 m0, s38
	s_nop 0
	global_load_lds_dwordx4 v[208:209], off
	v_lshl_add_u64 v[208:209], s[30:31], 0, v[198:199]
	s_add_i32 m0, s38, 0x2000
	s_nop 0
	global_load_lds_dwordx4 v[208:209], off
	v_lshl_add_u64 v[208:209], v[212:213], 0, s[18:19]
	s_mov_b32 m0, s56
	s_nop 0
	global_load_lds_dwordx4 v[208:209], off
	v_lshl_add_u64 v[208:209], v[214:215], 0, s[18:19]
	s_mov_b32 m0, s57
	s_nop 0
	global_load_lds_dwordx4 v[208:209], off
	s_waitcnt vmcnt(8)
	s_waitcnt lgkmcnt(0)
	s_barrier
	s_setprio 0
	s_waitcnt lgkmcnt(0)
	v_mfma_f32_16x16x32_bf16 v[60:63], v[112:115], v[160:163], v[60:63]
	v_mfma_f32_16x16x32_bf16 v[56:59], v[124:127], v[160:163], v[56:59]
	v_mfma_f32_16x16x32_bf16 v[44:47], v[112:115], v[168:171], v[44:47]
	v_mfma_f32_16x16x32_bf16 v[40:43], v[124:127], v[168:171], v[40:43]
	v_mfma_f32_16x16x32_bf16 v[28:31], v[112:115], v[176:179], v[28:31]
	v_mfma_f32_16x16x32_bf16 v[24:27], v[124:127], v[176:179], v[24:27]
	v_mfma_f32_16x16x32_bf16 v[12:15], v[112:115], v[184:187], v[12:15]
	v_mfma_f32_16x16x32_bf16 v[8:11], v[124:127], v[184:187], v[8:11]
	v_mfma_f32_16x16x32_bf16 v[60:63], v[116:119], v[164:167], v[60:63]
	v_mfma_f32_16x16x32_bf16 v[56:59], v[128:131], v[164:167], v[56:59]
	v_mfma_f32_16x16x32_bf16 v[44:47], v[116:119], v[172:175], v[44:47]
	v_mfma_f32_16x16x32_bf16 v[40:43], v[128:131], v[172:175], v[40:43]
	v_mfma_f32_16x16x32_bf16 v[28:31], v[116:119], v[180:183], v[28:31]
	v_mfma_f32_16x16x32_bf16 v[24:27], v[128:131], v[180:183], v[24:27]
	v_mfma_f32_16x16x32_bf16 v[12:15], v[116:119], v[188:191], v[12:15]
	v_mfma_f32_16x16x32_bf16 v[8:11], v[128:131], v[188:191], v[8:11]
	s_setprio 1
	s_setprio 0
	v_mfma_f32_16x16x32_bf16 v[52:55], v[136:139], v[160:163], v[52:55]
	v_mfma_f32_16x16x32_bf16 v[48:51], v[148:151], v[160:163], v[48:51]
	v_mfma_f32_16x16x32_bf16 v[36:39], v[136:139], v[168:171], v[36:39]
	v_mfma_f32_16x16x32_bf16 v[32:35], v[148:151], v[168:171], v[32:35]
	v_mfma_f32_16x16x32_bf16 v[20:23], v[136:139], v[176:179], v[20:23]
	v_mfma_f32_16x16x32_bf16 v[16:19], v[148:151], v[176:179], v[16:19]
	v_mfma_f32_16x16x32_bf16 v[4:7], v[136:139], v[184:187], v[4:7]
	v_mfma_f32_16x16x32_bf16 v[0:3], v[148:151], v[184:187], v[0:3]
	v_mfma_f32_16x16x32_bf16 v[52:55], v[140:143], v[164:167], v[52:55]
	v_mfma_f32_16x16x32_bf16 v[48:51], v[156:159], v[164:167], v[48:51]
	v_mfma_f32_16x16x32_bf16 v[36:39], v[140:143], v[172:175], v[36:39]
	v_mfma_f32_16x16x32_bf16 v[32:35], v[156:159], v[172:175], v[32:35]
	v_mfma_f32_16x16x32_bf16 v[20:23], v[140:143], v[180:183], v[20:23]
	v_mfma_f32_16x16x32_bf16 v[16:19], v[156:159], v[180:183], v[16:19]
	v_mfma_f32_16x16x32_bf16 v[4:7], v[140:143], v[188:191], v[4:7]
	v_mfma_f32_16x16x32_bf16 v[0:3], v[156:159], v[188:191], v[0:3]
	s_setprio 1
	s_barrier
	s_add_i32 s64, s64, 2
	s_add_u32 s23, s23, 0x100
	s_addc_u32 s25, s25, 0
	s_cmp_gt_u32 s64, 13
	s_mov_b64 s[30:31], s[36:37]
	s_cbranch_scc0 .LBB0_430
	s_and_b64 vcc, exec, s[20:21]
	s_cbranch_vccz .LBB0_433
	s_barrier

.LBB0_545:
	v_add_u32_e32 v85, s63, v83
	s_add_u32 s38, s22, s36
	ds_read_b128 v[86:89], v85
	ds_read_b128 v[90:93], v85 offset:1024
	ds_read_b128 v[94:97], v85 offset:2048
	ds_read_b128 v[98:101], v85 offset:3072
	s_addc_u32 s39, s23, s37
	s_add_u32 s38, s38, 0x100
	s_addc_u32 s39, s39, 0
	s_add_u32 s68, s21, s36
	s_addc_u32 s69, s66, s37
	s_cmpk_eq_i32 s36, 0x700
	s_cselect_b32 s41, s25, s39
	s_cselect_b32 s40, s24, s38
	s_cselect_b32 s39, s27, s69
	s_cselect_b32 s38, s26, s68
	v_lshl_add_u64 v[134:135], v[78:79], 0, s[36:37]
	s_add_i32 m0, s9, 0xc000
	ds_read_b128 v[102:105], v84
	ds_read_b128 v[106:109], v84 offset:1024
	ds_read_b128 v[110:113], v84 offset:2048
	ds_read_b128 v[114:117], v84 offset:3072
	ds_read_b128 v[118:121], v84 offset:4096
	ds_read_b128 v[122:125], v84 offset:5120
	ds_read_b128 v[126:129], v84 offset:6144
	ds_read_b128 v[130:133], v84 offset:7168
	global_load_lds_dwordx4 v[134:135], off
	v_lshl_add_u64 v[134:135], v[76:77], 0, s[36:37]
	s_add_i32 m0, s9, 0xe000
	s_nop 0
	global_load_lds_dwordx4 v[134:135], off
	s_waitcnt vmcnt(8)
	s_waitcnt lgkmcnt(0)
	s_barrier
	s_setprio 0
	s_waitcnt lgkmcnt(0)
	v_mfma_f32_16x16x32_bf16 v[60:63], v[86:89], v[102:105], v[60:63]
	v_mfma_f32_16x16x32_bf16 v[56:59], v[94:97], v[102:105], v[56:59]
	v_mfma_f32_16x16x32_bf16 v[52:55], v[86:89], v[110:113], v[52:55]
	v_mfma_f32_16x16x32_bf16 v[48:51], v[94:97], v[110:113], v[48:51]
	v_mfma_f32_16x16x32_bf16 v[44:47], v[86:89], v[118:121], v[44:47]
	v_mfma_f32_16x16x32_bf16 v[40:43], v[94:97], v[118:121], v[40:43]
	v_mfma_f32_16x16x32_bf16 v[36:39], v[86:89], v[126:129], v[36:39]
	v_mfma_f32_16x16x32_bf16 v[32:35], v[94:97], v[126:129], v[32:35]
	v_mfma_f32_16x16x32_bf16 v[60:63], v[90:93], v[106:109], v[60:63]
	v_mfma_f32_16x16x32_bf16 v[56:59], v[98:101], v[106:109], v[56:59]
	v_mfma_f32_16x16x32_bf16 v[52:55], v[90:93], v[114:117], v[52:55]
	v_mfma_f32_16x16x32_bf16 v[48:51], v[98:101], v[114:117], v[48:51]
	v_mfma_f32_16x16x32_bf16 v[44:47], v[90:93], v[122:125], v[44:47]
	v_mfma_f32_16x16x32_bf16 v[40:43], v[98:101], v[122:125], v[40:43]
	v_mfma_f32_16x16x32_bf16 v[36:39], v[90:93], v[130:133], v[36:39]
	v_mfma_f32_16x16x32_bf16 v[32:35], v[98:101], v[130:133], v[32:35]
	s_setprio 1
	s_barrier
	s_add_i32 s68, s63, s50
	v_lshl_add_u64 v[134:135], s[38:39], 0, v[64:65]
	s_mov_b32 m0, s68
	ds_read_b128 v[102:105], v84 offset:16384
	ds_read_b128 v[106:109], v84 offset:17408
	ds_read_b128 v[110:113], v84 offset:18432
	ds_read_b128 v[114:117], v84 offset:19456
	ds_read_b128 v[118:121], v84 offset:20480
	ds_read_b128 v[122:125], v84 offset:21504
	ds_read_b128 v[126:129], v84 offset:22528
	ds_read_b128 v[130:133], v84 offset:23552
	global_load_lds_dwordx4 v[134:135], off
	s_add_i32 m0, s68, 0x2000
	s_add_u32 s68, s38, 0x40000
	v_lshl_add_u64 v[136:137], s[38:39], 0, v[66:67]
	s_addc_u32 s69, s39, 0
	global_load_lds_dwordx4 v[136:137], off
	v_lshl_add_u64 v[138:139], s[68:69], 0, v[64:65]
	s_mov_b32 m0, s53
	v_lshl_add_u64 v[140:141], s[40:41], 0, v[66:67]
	global_load_lds_dwordx4 v[138:139], off
	v_lshl_add_u64 v[138:139], s[68:69], 0, v[66:67]
	s_mov_b32 m0, s54
	s_nop 0
	global_load_lds_dwordx4 v[138:139], off
	v_lshl_add_u64 v[138:139], s[40:41], 0, v[64:65]
	s_mov_b32 m0, s9
	s_nop 0
	global_load_lds_dwordx4 v[138:139], off
	s_mov_b32 m0, s56
	s_nop 0
	global_load_lds_dwordx4 v[140:141], off
	s_waitcnt vmcnt(8)
	s_waitcnt lgkmcnt(0)
	s_barrier
	s_setprio 0
	s_waitcnt lgkmcnt(0)
	v_mfma_f32_16x16x32_bf16 v[28:31], v[86:89], v[102:105], v[28:31]
	v_mfma_f32_16x16x32_bf16 v[24:27], v[94:97], v[102:105], v[24:27]
	v_mfma_f32_16x16x32_bf16 v[20:23], v[86:89], v[110:113], v[20:23]
	v_mfma_f32_16x16x32_bf16 v[16:19], v[94:97], v[110:113], v[16:19]
	v_mfma_f32_16x16x32_bf16 v[12:15], v[86:89], v[118:121], v[12:15]
	v_mfma_f32_16x16x32_bf16 v[8:11], v[94:97], v[118:121], v[8:11]
	v_mfma_f32_16x16x32_bf16 v[4:7], v[86:89], v[126:129], v[4:7]
	v_mfma_f32_16x16x32_bf16 v[0:3], v[94:97], v[126:129], v[0:3]
	v_mfma_f32_16x16x32_bf16 v[28:31], v[90:93], v[106:109], v[28:31]
	v_mfma_f32_16x16x32_bf16 v[24:27], v[98:101], v[106:109], v[24:27]
	v_mfma_f32_16x16x32_bf16 v[20:23], v[90:93], v[114:117], v[20:23]
	v_mfma_f32_16x16x32_bf16 v[16:19], v[98:101], v[114:117], v[16:19]
	v_mfma_f32_16x16x32_bf16 v[12:15], v[90:93], v[122:125], v[12:15]
	v_mfma_f32_16x16x32_bf16 v[8:11], v[98:101], v[122:125], v[8:11]
	v_mfma_f32_16x16x32_bf16 v[4:7], v[90:93], v[130:133], v[4:7]
	v_mfma_f32_16x16x32_bf16 v[0:3], v[98:101], v[130:133], v[0:3]
	s_setprio 1
	s_barrier
	s_add_i32 s68, 0, 0x18000
	v_add_u32_e32 v85, s68, v83
	ds_read_b128 v[86:89], v85
	ds_read_b128 v[90:93], v85 offset:1024
	ds_read_b128 v[94:97], v85 offset:2048
	ds_read_b128 v[98:101], v85 offset:3072
	s_add_u32 s40, s40, 0x40000
	s_addc_u32 s41, s41, 0
	s_mov_b32 m0, s57
	v_lshl_add_u64 v[142:143], s[40:41], 0, v[64:65]
	ds_read_b128 v[102:105], v84 offset:32768
	ds_read_b128 v[106:109], v84 offset:33792
	ds_read_b128 v[110:113], v84 offset:34816
	ds_read_b128 v[114:117], v84 offset:35840
	ds_read_b128 v[118:121], v84 offset:36864
	ds_read_b128 v[122:125], v84 offset:37888
	ds_read_b128 v[126:129], v84 offset:38912
	ds_read_b128 v[130:133], v84 offset:39936
	global_load_lds_dwordx4 v[142:143], off
	v_lshl_add_u64 v[142:143], s[40:41], 0, v[66:67]
	s_mov_b32 m0, s58
	s_nop 0
	global_load_lds_dwordx4 v[142:143], off
	s_waitcnt vmcnt(8)
	s_waitcnt lgkmcnt(0)
	s_barrier
	s_setprio 0
	s_waitcnt lgkmcnt(0)
	v_mfma_f32_16x16x32_bf16 v[60:63], v[86:89], v[102:105], v[60:63]
	v_mfma_f32_16x16x32_bf16 v[56:59], v[94:97], v[102:105], v[56:59]
	v_mfma_f32_16x16x32_bf16 v[52:55], v[86:89], v[110:113], v[52:55]
	v_mfma_f32_16x16x32_bf16 v[48:51], v[94:97], v[110:113], v[48:51]
	v_mfma_f32_16x16x32_bf16 v[44:47], v[86:89], v[118:121], v[44:47]
	v_mfma_f32_16x16x32_bf16 v[40:43], v[94:97], v[118:121], v[40:43]
	v_mfma_f32_16x16x32_bf16 v[36:39], v[86:89], v[126:129], v[36:39]
	v_mfma_f32_16x16x32_bf16 v[32:35], v[94:97], v[126:129], v[32:35]
	v_mfma_f32_16x16x32_bf16 v[60:63], v[90:93], v[106:109], v[60:63]
	v_mfma_f32_16x16x32_bf16 v[56:59], v[98:101], v[106:109], v[56:59]
	v_mfma_f32_16x16x32_bf16 v[52:55], v[90:93], v[114:117], v[52:55]
	v_mfma_f32_16x16x32_bf16 v[48:51], v[98:101], v[114:117], v[48:51]
	v_mfma_f32_16x16x32_bf16 v[44:47], v[90:93], v[122:125], v[44:47]
	v_mfma_f32_16x16x32_bf16 v[40:43], v[98:101], v[122:125], v[40:43]
	v_mfma_f32_16x16x32_bf16 v[36:39], v[90:93], v[130:133], v[36:39]
	v_mfma_f32_16x16x32_bf16 v[32:35], v[98:101], v[130:133], v[32:35]
	s_setprio 1
	s_barrier
	s_add_i32 s40, s68, s50
	v_lshl_add_u64 v[134:135], v[134:135], 0, s[16:17]
	s_mov_b32 m0, s40
	ds_read_b128 v[102:105], v84 offset:49152
	ds_read_b128 v[106:109], v84 offset:50176
	ds_read_b128 v[110:113], v84 offset:51200
	ds_read_b128 v[114:117], v84 offset:52224
	ds_read_b128 v[118:121], v84 offset:53248
	ds_read_b128 v[122:125], v84 offset:54272
	ds_read_b128 v[126:129], v84 offset:55296
	ds_read_b128 v[130:133], v84 offset:56320
	global_load_lds_dwordx4 v[134:135], off
	s_add_i32 m0, s40, 0x2000
	s_add_u32 s38, s38, 0x40080
	v_lshl_add_u64 v[134:135], v[136:137], 0, s[16:17]
	s_addc_u32 s39, s39, 0
	global_load_lds_dwordx4 v[134:135], off
	v_lshl_add_u64 v[134:135], s[38:39], 0, v[64:65]
	s_mov_b32 m0, s61
	s_nop 0
	global_load_lds_dwordx4 v[134:135], off
	v_lshl_add_u64 v[134:135], s[38:39], 0, v[66:67]
	s_mov_b32 m0, s62
	s_nop 0
	global_load_lds_dwordx4 v[134:135], off
	v_lshl_add_u64 v[134:135], v[138:139], 0, s[16:17]
	s_mov_b32 m0, s59
	s_nop 0
	global_load_lds_dwordx4 v[134:135], off
	v_lshl_add_u64 v[134:135], v[140:141], 0, s[16:17]
	s_mov_b32 m0, s60
	s_nop 0
	global_load_lds_dwordx4 v[134:135], off
	s_waitcnt vmcnt(8)
	s_waitcnt lgkmcnt(0)
	s_barrier
	s_setprio 0
	s_waitcnt lgkmcnt(0)
	v_mfma_f32_16x16x32_bf16 v[28:31], v[86:89], v[102:105], v[28:31]
	v_mfma_f32_16x16x32_bf16 v[24:27], v[94:97], v[102:105], v[24:27]
	v_mfma_f32_16x16x32_bf16 v[20:23], v[86:89], v[110:113], v[20:23]
	v_mfma_f32_16x16x32_bf16 v[16:19], v[94:97], v[110:113], v[16:19]
	v_mfma_f32_16x16x32_bf16 v[12:15], v[86:89], v[118:121], v[12:15]
	v_mfma_f32_16x16x32_bf16 v[8:11], v[94:97], v[118:121], v[8:11]
	v_mfma_f32_16x16x32_bf16 v[4:7], v[86:89], v[126:129], v[4:7]
	v_mfma_f32_16x16x32_bf16 v[0:3], v[94:97], v[126:129], v[0:3]
	v_mfma_f32_16x16x32_bf16 v[28:31], v[90:93], v[106:109], v[28:31]
	v_mfma_f32_16x16x32_bf16 v[24:27], v[98:101], v[106:109], v[24:27]
	v_mfma_f32_16x16x32_bf16 v[20:23], v[90:93], v[114:117], v[20:23]
	v_mfma_f32_16x16x32_bf16 v[16:19], v[98:101], v[114:117], v[16:19]
	v_mfma_f32_16x16x32_bf16 v[12:15], v[90:93], v[122:125], v[12:15]
	v_mfma_f32_16x16x32_bf16 v[8:11], v[98:101], v[122:125], v[8:11]
	v_mfma_f32_16x16x32_bf16 v[4:7], v[90:93], v[130:133], v[4:7]
	v_mfma_f32_16x16x32_bf16 v[0:3], v[98:101], v[130:133], v[0:3]
	s_setprio 1
	s_barrier
	s_add_i32 s67, s67, 2
	s_add_u32 s36, s36, 0x100
	s_addc_u32 s37, s37, 0
	s_cmp_gt_u32 s67, 13
	s_cbranch_scc0 .LBB0_545
	s_and_b64 vcc, exec, s[18:19]
	s_cbranch_vccz .LBB0_548
	s_barrier

.LBB0_791:
	ds_read_b128 v[160:163], v152
	ds_read_b128 v[164:167], v152 offset:1024
	ds_read_b128 v[168:171], v152 offset:2048
	ds_read_b128 v[172:175], v152 offset:3072
	ds_read_b128 v[176:179], v153
	ds_read_b128 v[180:183], v153 offset:1024
	ds_read_b128 v[184:187], v153 offset:2048
	ds_read_b128 v[188:191], v153 offset:3072
	s_add_u32 s38, s30, s36
	s_addc_u32 s39, s31, s37
	s_add_u32 s40, s38, 0x100
	s_addc_u32 s41, s39, 0
	s_add_u32 s68, s23, s36
	s_addc_u32 s69, s66, s37
	s_cmpk_eq_i32 s36, 0x700
	s_cselect_b64 vcc, -1, 0
	s_and_b64 s[38:39], vcc, exec
	v_cndmask_b32_e32 v132, v138, v157, vcc
	s_cselect_b32 s41, s27, s41
	s_cselect_b32 s40, s26, s40
	v_cndmask_b32_e32 v224, v136, v156, vcc
	v_cndmask_b32_e32 v135, v134, v155, vcc
	v_cndmask_b32_e32 v141, v140, v158, vcc
	s_cselect_b32 s39, s25, s69
	s_cselect_b32 s38, s24, s68
	s_mov_b32 m0, s60
	v_lshl_add_u64 v[226:227], v[144:145], 0, s[36:37]
	ds_read_b128 v[192:195], v154
	ds_read_b128 v[196:199], v154 offset:1024
	ds_read_b128 v[200:203], v154 offset:2048
	ds_read_b128 v[204:207], v154 offset:3072
	ds_read_b128 v[208:211], v154 offset:4096
	ds_read_b128 v[212:215], v154 offset:5120
	ds_read_b128 v[216:219], v154 offset:6144
	ds_read_b128 v[220:223], v154 offset:7168
	global_load_lds_dwordx4 v[226:227], off
	v_lshl_add_u64 v[226:227], v[142:143], 0, s[36:37]
	s_add_i32 m0, s50, 0xe000
	s_nop 0
	global_load_lds_dwordx4 v[226:227], off
	s_waitcnt vmcnt(8)
	s_waitcnt lgkmcnt(0)
	s_barrier
	s_setprio 0
	s_waitcnt lgkmcnt(0)
	v_mfma_f32_16x16x32_bf16 v[116:119], v[160:163], v[192:195], v[116:119]
	v_mfma_f32_16x16x32_bf16 v[112:115], v[168:171], v[192:195], v[112:115]
	v_mfma_f32_16x16x32_bf16 v[108:111], v[160:163], v[200:203], v[108:111]
	v_mfma_f32_16x16x32_bf16 v[104:107], v[168:171], v[200:203], v[104:107]
	v_mfma_f32_16x16x32_bf16 v[92:95], v[160:163], v[208:211], v[92:95]
	v_mfma_f32_16x16x32_bf16 v[88:91], v[168:171], v[208:211], v[88:91]
	v_mfma_f32_16x16x32_bf16 v[76:79], v[160:163], v[216:219], v[76:79]
	v_mfma_f32_16x16x32_bf16 v[72:75], v[168:171], v[216:219], v[72:75]
	v_mfma_f32_16x16x32_bf16 v[116:119], v[164:167], v[196:199], v[116:119]
	v_mfma_f32_16x16x32_bf16 v[112:115], v[172:175], v[196:199], v[112:115]
	v_mfma_f32_16x16x32_bf16 v[108:111], v[164:167], v[204:207], v[108:111]
	v_mfma_f32_16x16x32_bf16 v[104:107], v[172:175], v[204:207], v[104:107]
	v_mfma_f32_16x16x32_bf16 v[92:95], v[164:167], v[212:215], v[92:95]
	v_mfma_f32_16x16x32_bf16 v[88:91], v[172:175], v[212:215], v[88:91]
	v_mfma_f32_16x16x32_bf16 v[76:79], v[164:167], v[220:223], v[76:79]
	v_mfma_f32_16x16x32_bf16 v[72:75], v[172:175], v[220:223], v[72:75]
	s_setprio 1
	s_setprio 0
	v_mfma_f32_16x16x32_bf16 v[124:127], v[176:179], v[192:195], v[124:127]
	v_mfma_f32_16x16x32_bf16 v[120:123], v[184:187], v[192:195], v[120:123]
	v_mfma_f32_16x16x32_bf16 v[100:103], v[176:179], v[200:203], v[100:103]
	v_mfma_f32_16x16x32_bf16 v[96:99], v[184:187], v[200:203], v[96:99]
	v_mfma_f32_16x16x32_bf16 v[84:87], v[176:179], v[208:211], v[84:87]
	v_mfma_f32_16x16x32_bf16 v[80:83], v[184:187], v[208:211], v[80:83]
	v_mfma_f32_16x16x32_bf16 v[68:71], v[176:179], v[216:219], v[68:71]
	v_mfma_f32_16x16x32_bf16 v[64:67], v[184:187], v[216:219], v[64:67]
	v_mfma_f32_16x16x32_bf16 v[124:127], v[180:183], v[196:199], v[124:127]
	v_mfma_f32_16x16x32_bf16 v[120:123], v[188:191], v[196:199], v[120:123]
	v_mfma_f32_16x16x32_bf16 v[100:103], v[180:183], v[204:207], v[100:103]
	v_mfma_f32_16x16x32_bf16 v[96:99], v[188:191], v[204:207], v[96:99]
	v_mfma_f32_16x16x32_bf16 v[84:87], v[180:183], v[212:215], v[84:87]
	v_mfma_f32_16x16x32_bf16 v[80:83], v[188:191], v[212:215], v[80:83]
	v_mfma_f32_16x16x32_bf16 v[68:71], v[180:183], v[220:223], v[68:71]
	v_mfma_f32_16x16x32_bf16 v[64:67], v[188:191], v[220:223], v[64:67]
	s_setprio 1
	s_barrier
	s_add_i32 s68, s57, s29
	v_lshl_add_u64 v[226:227], s[38:39], 0, v[128:129]
	s_mov_b32 m0, s68
	ds_read_b128 v[192:195], v154 offset:16384
	ds_read_b128 v[196:199], v154 offset:17408
	ds_read_b128 v[200:203], v154 offset:18432
	ds_read_b128 v[204:207], v154 offset:19456
	ds_read_b128 v[208:211], v154 offset:20480
	ds_read_b128 v[212:215], v154 offset:21504
	ds_read_b128 v[216:219], v154 offset:22528
	ds_read_b128 v[220:223], v154 offset:23552
	global_load_lds_dwordx4 v[226:227], off
	s_add_i32 m0, s68, 0x2000
	s_add_u32 s68, s38, 0x40000
	v_lshl_add_u64 v[228:229], s[38:39], 0, v[130:131]
	s_addc_u32 s69, s39, 0
	s_add_i32 s70, s58, s29
	global_load_lds_dwordx4 v[228:229], off
	v_lshl_add_u64 v[230:231], s[68:69], 0, v[128:129]
	s_mov_b32 m0, s70
	v_mov_b32_e32 v225, v133
	global_load_lds_dwordx4 v[230:231], off
	v_lshl_add_u64 v[230:231], s[68:69], 0, v[130:131]
	s_add_i32 m0, s70, 0x2000
	s_nop 0
	global_load_lds_dwordx4 v[230:231], off
	s_mov_b32 m0, s50
	v_lshl_add_u64 v[230:231], s[40:41], 0, v[132:133]
	global_load_lds_dwordx4 v132, s[40:41]
	s_mov_b32 m0, s51
	s_nop 0
	global_load_lds_dwordx4 v224, s[40:41]
	s_waitcnt vmcnt(8)
	s_waitcnt lgkmcnt(0)
	v_lshl_add_u64 v[224:225], s[40:41], 0, v[224:225]
	s_barrier
	s_setprio 0
	s_waitcnt lgkmcnt(0)
	v_mfma_f32_16x16x32_bf16 v[60:63], v[160:163], v[192:195], v[60:63]
	v_mfma_f32_16x16x32_bf16 v[56:59], v[168:171], v[192:195], v[56:59]
	v_mfma_f32_16x16x32_bf16 v[44:47], v[160:163], v[200:203], v[44:47]
	v_mfma_f32_16x16x32_bf16 v[40:43], v[168:171], v[200:203], v[40:43]
	v_mfma_f32_16x16x32_bf16 v[28:31], v[160:163], v[208:211], v[28:31]
	v_mfma_f32_16x16x32_bf16 v[24:27], v[168:171], v[208:211], v[24:27]
	v_mfma_f32_16x16x32_bf16 v[12:15], v[160:163], v[216:219], v[12:15]
	v_mfma_f32_16x16x32_bf16 v[8:11], v[168:171], v[216:219], v[8:11]
	v_mfma_f32_16x16x32_bf16 v[60:63], v[164:167], v[196:199], v[60:63]
	v_mfma_f32_16x16x32_bf16 v[56:59], v[172:175], v[196:199], v[56:59]
	v_mfma_f32_16x16x32_bf16 v[44:47], v[164:167], v[204:207], v[44:47]
	v_mfma_f32_16x16x32_bf16 v[40:43], v[172:175], v[204:207], v[40:43]
	v_mfma_f32_16x16x32_bf16 v[28:31], v[164:167], v[212:215], v[28:31]
	v_mfma_f32_16x16x32_bf16 v[24:27], v[172:175], v[212:215], v[24:27]
	v_mfma_f32_16x16x32_bf16 v[12:15], v[164:167], v[220:223], v[12:15]
	v_mfma_f32_16x16x32_bf16 v[8:11], v[172:175], v[220:223], v[8:11]
	s_setprio 1
	s_setprio 0
	v_mfma_f32_16x16x32_bf16 v[52:55], v[176:179], v[192:195], v[52:55]
	v_mfma_f32_16x16x32_bf16 v[48:51], v[184:187], v[192:195], v[48:51]
	v_mfma_f32_16x16x32_bf16 v[36:39], v[176:179], v[200:203], v[36:39]
	v_mfma_f32_16x16x32_bf16 v[32:35], v[184:187], v[200:203], v[32:35]
	v_mfma_f32_16x16x32_bf16 v[20:23], v[176:179], v[208:211], v[20:23]
	v_mfma_f32_16x16x32_bf16 v[16:19], v[184:187], v[208:211], v[16:19]
	v_mfma_f32_16x16x32_bf16 v[4:7], v[176:179], v[216:219], v[4:7]
	v_mfma_f32_16x16x32_bf16 v[0:3], v[184:187], v[216:219], v[0:3]
	v_mfma_f32_16x16x32_bf16 v[52:55], v[180:183], v[196:199], v[52:55]
	v_mfma_f32_16x16x32_bf16 v[48:51], v[188:191], v[196:199], v[48:51]
	v_mfma_f32_16x16x32_bf16 v[36:39], v[180:183], v[204:207], v[36:39]
	v_mfma_f32_16x16x32_bf16 v[32:35], v[188:191], v[204:207], v[32:35]
	v_mfma_f32_16x16x32_bf16 v[20:23], v[180:183], v[212:215], v[20:23]
	v_mfma_f32_16x16x32_bf16 v[16:19], v[188:191], v[212:215], v[16:19]
	v_mfma_f32_16x16x32_bf16 v[4:7], v[180:183], v[220:223], v[4:7]
	v_mfma_f32_16x16x32_bf16 v[0:3], v[188:191], v[220:223], v[0:3]
	s_setprio 1
	s_barrier
	s_add_i32 s68, 0, 0x18000
	v_add_u32_e32 v132, s68, v139
	s_add_i32 s69, 0, 0x1c000
	ds_read_b128 v[160:163], v132
	ds_read_b128 v[164:167], v132 offset:1024
	ds_read_b128 v[168:171], v132 offset:2048
	ds_read_b128 v[172:175], v132 offset:3072
	v_add_u32_e32 v132, s69, v139
	ds_read_b128 v[176:179], v132
	ds_read_b128 v[180:183], v132 offset:1024
	ds_read_b128 v[184:187], v132 offset:2048
	ds_read_b128 v[188:191], v132 offset:3072
	s_mov_b32 m0, s52
	ds_read_b128 v[192:195], v154 offset:32768
	ds_read_b128 v[196:199], v154 offset:33792
	ds_read_b128 v[200:203], v154 offset:34816
	ds_read_b128 v[204:207], v154 offset:35840
	ds_read_b128 v[208:211], v154 offset:36864
	ds_read_b128 v[212:215], v154 offset:37888
	ds_read_b128 v[216:219], v154 offset:38912
	ds_read_b128 v[220:223], v154 offset:39936
	global_load_lds_dwordx4 v135, s[40:41]
	s_mov_b32 m0, s53
	s_nop 0
	global_load_lds_dwordx4 v141, s[40:41]
	s_waitcnt vmcnt(8)
	s_waitcnt lgkmcnt(0)
	s_barrier
	s_setprio 0
	s_waitcnt lgkmcnt(0)
	v_mfma_f32_16x16x32_bf16 v[116:119], v[160:163], v[192:195], v[116:119]
	v_mfma_f32_16x16x32_bf16 v[112:115], v[168:171], v[192:195], v[112:115]
	v_mfma_f32_16x16x32_bf16 v[108:111], v[160:163], v[200:203], v[108:111]
	v_mfma_f32_16x16x32_bf16 v[104:107], v[168:171], v[200:203], v[104:107]
	v_mfma_f32_16x16x32_bf16 v[92:95], v[160:163], v[208:211], v[92:95]
	v_mfma_f32_16x16x32_bf16 v[88:91], v[168:171], v[208:211], v[88:91]
	v_mfma_f32_16x16x32_bf16 v[76:79], v[160:163], v[216:219], v[76:79]
	v_mfma_f32_16x16x32_bf16 v[72:75], v[168:171], v[216:219], v[72:75]
	v_mfma_f32_16x16x32_bf16 v[116:119], v[164:167], v[196:199], v[116:119]
	v_mfma_f32_16x16x32_bf16 v[112:115], v[172:175], v[196:199], v[112:115]
	v_mfma_f32_16x16x32_bf16 v[108:111], v[164:167], v[204:207], v[108:111]
	v_mfma_f32_16x16x32_bf16 v[104:107], v[172:175], v[204:207], v[104:107]
	v_mfma_f32_16x16x32_bf16 v[92:95], v[164:167], v[212:215], v[92:95]
	v_mfma_f32_16x16x32_bf16 v[88:91], v[172:175], v[212:215], v[88:91]
	v_mfma_f32_16x16x32_bf16 v[76:79], v[164:167], v[220:223], v[76:79]
	v_mfma_f32_16x16x32_bf16 v[72:75], v[172:175], v[220:223], v[72:75]
	s_setprio 1
	s_setprio 0
	v_mfma_f32_16x16x32_bf16 v[124:127], v[176:179], v[192:195], v[124:127]
	v_mfma_f32_16x16x32_bf16 v[120:123], v[184:187], v[192:195], v[120:123]
	v_mfma_f32_16x16x32_bf16 v[100:103], v[176:179], v[200:203], v[100:103]
	v_mfma_f32_16x16x32_bf16 v[96:99], v[184:187], v[200:203], v[96:99]
	v_mfma_f32_16x16x32_bf16 v[84:87], v[176:179], v[208:211], v[84:87]
	v_mfma_f32_16x16x32_bf16 v[80:83], v[184:187], v[208:211], v[80:83]
	v_mfma_f32_16x16x32_bf16 v[68:71], v[176:179], v[216:219], v[68:71]
	v_mfma_f32_16x16x32_bf16 v[64:67], v[184:187], v[216:219], v[64:67]
	v_mfma_f32_16x16x32_bf16 v[124:127], v[180:183], v[196:199], v[124:127]
	v_mfma_f32_16x16x32_bf16 v[120:123], v[188:191], v[196:199], v[120:123]
	v_mfma_f32_16x16x32_bf16 v[100:103], v[180:183], v[204:207], v[100:103]
	v_mfma_f32_16x16x32_bf16 v[96:99], v[188:191], v[204:207], v[96:99]
	v_mfma_f32_16x16x32_bf16 v[84:87], v[180:183], v[212:215], v[84:87]
	v_mfma_f32_16x16x32_bf16 v[80:83], v[188:191], v[212:215], v[80:83]
	v_mfma_f32_16x16x32_bf16 v[68:71], v[180:183], v[220:223], v[68:71]
	v_mfma_f32_16x16x32_bf16 v[64:67], v[188:191], v[220:223], v[64:67]
	s_setprio 1
	s_barrier
	s_add_i32 s40, s68, s29
	v_lshl_add_u64 v[226:227], v[226:227], 0, s[18:19]
	s_mov_b32 m0, s40
	ds_read_b128 v[192:195], v154 offset:49152
	ds_read_b128 v[196:199], v154 offset:50176
	ds_read_b128 v[200:203], v154 offset:51200
	ds_read_b128 v[204:207], v154 offset:52224
	ds_read_b128 v[208:211], v154 offset:53248
	ds_read_b128 v[212:215], v154 offset:54272
	ds_read_b128 v[216:219], v154 offset:55296
	ds_read_b128 v[220:223], v154 offset:56320
	global_load_lds_dwordx4 v[226:227], off
	s_add_i32 m0, s40, 0x2000
	s_add_u32 s38, s38, 0x40080
	v_lshl_add_u64 v[226:227], v[228:229], 0, s[18:19]
	s_addc_u32 s39, s39, 0
	s_add_i32 s40, s69, s29
	global_load_lds_dwordx4 v[226:227], off
	v_lshl_add_u64 v[226:227], s[38:39], 0, v[128:129]
	s_mov_b32 m0, s40
	v_lshl_add_u64 v[224:225], v[224:225], 0, s[18:19]
	global_load_lds_dwordx4 v[226:227], off
	v_lshl_add_u64 v[226:227], s[38:39], 0, v[130:131]
	s_add_i32 m0, s40, 0x2000
	s_nop 0
	global_load_lds_dwordx4 v[226:227], off
	v_lshl_add_u64 v[226:227], v[230:231], 0, s[18:19]
	s_mov_b32 m0, s55
	s_nop 0
	global_load_lds_dwordx4 v[226:227], off
	s_mov_b32 m0, s56
	s_nop 0
	global_load_lds_dwordx4 v[224:225], off
	s_waitcnt vmcnt(8)
	s_waitcnt lgkmcnt(0)
	s_barrier
	s_setprio 0
	s_waitcnt lgkmcnt(0)
	v_mfma_f32_16x16x32_bf16 v[60:63], v[160:163], v[192:195], v[60:63]
	v_mfma_f32_16x16x32_bf16 v[56:59], v[168:171], v[192:195], v[56:59]
	v_mfma_f32_16x16x32_bf16 v[44:47], v[160:163], v[200:203], v[44:47]
	v_mfma_f32_16x16x32_bf16 v[40:43], v[168:171], v[200:203], v[40:43]
	v_mfma_f32_16x16x32_bf16 v[28:31], v[160:163], v[208:211], v[28:31]
	v_mfma_f32_16x16x32_bf16 v[24:27], v[168:171], v[208:211], v[24:27]
	v_mfma_f32_16x16x32_bf16 v[12:15], v[160:163], v[216:219], v[12:15]
	v_mfma_f32_16x16x32_bf16 v[8:11], v[168:171], v[216:219], v[8:11]
	v_mfma_f32_16x16x32_bf16 v[60:63], v[164:167], v[196:199], v[60:63]
	v_mfma_f32_16x16x32_bf16 v[56:59], v[172:175], v[196:199], v[56:59]
	v_mfma_f32_16x16x32_bf16 v[44:47], v[164:167], v[204:207], v[44:47]
	v_mfma_f32_16x16x32_bf16 v[40:43], v[172:175], v[204:207], v[40:43]
	v_mfma_f32_16x16x32_bf16 v[28:31], v[164:167], v[212:215], v[28:31]
	v_mfma_f32_16x16x32_bf16 v[24:27], v[172:175], v[212:215], v[24:27]
	v_mfma_f32_16x16x32_bf16 v[12:15], v[164:167], v[220:223], v[12:15]
	v_mfma_f32_16x16x32_bf16 v[8:11], v[172:175], v[220:223], v[8:11]
	s_setprio 1
	s_setprio 0
	v_mfma_f32_16x16x32_bf16 v[52:55], v[176:179], v[192:195], v[52:55]
	v_mfma_f32_16x16x32_bf16 v[48:51], v[184:187], v[192:195], v[48:51]
	v_mfma_f32_16x16x32_bf16 v[36:39], v[176:179], v[200:203], v[36:39]
	v_mfma_f32_16x16x32_bf16 v[32:35], v[184:187], v[200:203], v[32:35]
	v_mfma_f32_16x16x32_bf16 v[20:23], v[176:179], v[208:211], v[20:23]
	v_mfma_f32_16x16x32_bf16 v[16:19], v[184:187], v[208:211], v[16:19]
	v_mfma_f32_16x16x32_bf16 v[4:7], v[176:179], v[216:219], v[4:7]
	v_mfma_f32_16x16x32_bf16 v[0:3], v[184:187], v[216:219], v[0:3]
	v_mfma_f32_16x16x32_bf16 v[52:55], v[180:183], v[196:199], v[52:55]
	v_mfma_f32_16x16x32_bf16 v[48:51], v[188:191], v[196:199], v[48:51]
	v_mfma_f32_16x16x32_bf16 v[36:39], v[180:183], v[204:207], v[36:39]
	v_mfma_f32_16x16x32_bf16 v[32:35], v[188:191], v[204:207], v[32:35]
	v_mfma_f32_16x16x32_bf16 v[20:23], v[180:183], v[212:215], v[20:23]
	v_mfma_f32_16x16x32_bf16 v[16:19], v[188:191], v[212:215], v[16:19]
	v_mfma_f32_16x16x32_bf16 v[4:7], v[180:183], v[220:223], v[4:7]
	v_mfma_f32_16x16x32_bf16 v[0:3], v[188:191], v[220:223], v[0:3]
	s_setprio 1
	s_barrier
	s_add_i32 s67, s67, 2
	s_add_u32 s36, s36, 0x100
	s_addc_u32 s37, s37, 0
	s_cmp_gt_u32 s67, 13
	s_cbranch_scc0 .LBB0_791
	s_and_b64 vcc, exec, s[20:21]
	s_cbranch_vccz .LBB0_794
	s_barrier

.LBB0_1068:
	ds_read_b128 v[8:11], v149
	ds_read_b128 v[12:15], v149 offset:1024
	ds_read_b128 v[16:19], v149 offset:2048
	ds_read_b128 v[20:23], v149 offset:3072
	ds_read_b128 v[24:27], v150
	ds_read_b128 v[28:31], v150 offset:1024
	ds_read_b128 v[32:35], v150 offset:2048
	ds_read_b128 v[36:39], v150 offset:3072
	s_add_u32 s68, s36, 0x18080
	s_addc_u32 s69, s37, 0
	s_mov_b32 m0, s62
	v_lshl_add_u64 v[64:65], s[68:69], 0, v[128:129]
	ds_read_b128 v[0:3], v140
	ds_read_b128 v[4:7], v140 offset:1024
	ds_read_b128 v[40:43], v140 offset:2048
	ds_read_b128 v[44:47], v140 offset:3072
	ds_read_b128 v[48:51], v140 offset:4096
	ds_read_b128 v[52:55], v140 offset:5120
	ds_read_b128 v[56:59], v140 offset:6144
	ds_read_b128 v[60:63], v140 offset:7168
	global_load_lds_dwordx4 v[64:65], off
	v_lshl_add_u64 v[64:65], s[68:69], 0, v[132:133]
	s_mov_b32 m0, s63
	s_nop 0
	global_load_lds_dwordx4 v[64:65], off
	s_waitcnt vmcnt(8)
	s_waitcnt lgkmcnt(0)
	s_barrier
	s_setprio 0
	s_waitcnt lgkmcnt(0)
	v_mfma_f32_16x16x32_bf16 v[64:67], v[8:11], v[0:3], 0
	v_mfma_f32_16x16x32_bf16 v[68:71], v[16:19], v[0:3], 0
	v_mfma_f32_16x16x32_bf16 v[72:75], v[8:11], v[40:43], 0
	v_mfma_f32_16x16x32_bf16 v[76:79], v[16:19], v[40:43], 0
	v_mfma_f32_16x16x32_bf16 v[80:83], v[8:11], v[48:51], 0
	v_mfma_f32_16x16x32_bf16 v[84:87], v[16:19], v[48:51], 0
	v_mfma_f32_16x16x32_bf16 v[88:91], v[8:11], v[56:59], 0
	v_mfma_f32_16x16x32_bf16 v[92:95], v[16:19], v[56:59], 0
	v_mfma_f32_16x16x32_bf16 v[64:67], v[12:15], v[4:7], v[64:67]
	v_mfma_f32_16x16x32_bf16 v[68:71], v[20:23], v[4:7], v[68:71]
	v_mfma_f32_16x16x32_bf16 v[72:75], v[12:15], v[44:47], v[72:75]
	v_mfma_f32_16x16x32_bf16 v[76:79], v[20:23], v[44:47], v[76:79]
	v_mfma_f32_16x16x32_bf16 v[80:83], v[12:15], v[52:55], v[80:83]
	v_mfma_f32_16x16x32_bf16 v[84:87], v[20:23], v[52:55], v[84:87]
	v_mfma_f32_16x16x32_bf16 v[88:91], v[12:15], v[60:63], v[88:91]
	v_mfma_f32_16x16x32_bf16 v[92:95], v[20:23], v[60:63], v[92:95]
	s_setprio 1
	s_setprio 0
	v_mfma_f32_16x16x32_bf16 v[96:99], v[24:27], v[0:3], 0
	v_mfma_f32_16x16x32_bf16 v[0:3], v[32:35], v[0:3], 0
	v_mfma_f32_16x16x32_bf16 v[100:103], v[36:39], v[4:7], v[0:3]
	v_mfma_f32_16x16x32_bf16 v[0:3], v[24:27], v[40:43], 0
	v_mfma_f32_16x16x32_bf16 v[104:107], v[28:31], v[44:47], v[0:3]
	v_mfma_f32_16x16x32_bf16 v[0:3], v[32:35], v[40:43], 0
	v_mfma_f32_16x16x32_bf16 v[40:43], v[36:39], v[44:47], v[0:3]
	v_mfma_f32_16x16x32_bf16 v[0:3], v[24:27], v[48:51], 0
	v_mfma_f32_16x16x32_bf16 v[44:47], v[28:31], v[52:55], v[0:3]
	v_mfma_f32_16x16x32_bf16 v[0:3], v[32:35], v[48:51], 0
	v_mfma_f32_16x16x32_bf16 v[48:51], v[36:39], v[52:55], v[0:3]
	v_mfma_f32_16x16x32_bf16 v[0:3], v[24:27], v[56:59], 0
	v_mfma_f32_16x16x32_bf16 v[52:55], v[28:31], v[60:63], v[0:3]
	v_mfma_f32_16x16x32_bf16 v[0:3], v[32:35], v[56:59], 0
	v_mfma_f32_16x16x32_bf16 v[96:99], v[28:31], v[4:7], v[96:99]
	v_mfma_f32_16x16x32_bf16 v[56:59], v[36:39], v[60:63], v[0:3]
	s_setprio 1
	s_barrier
	s_nop 3
	v_lshl_add_u64 v[0:1], s[38:39], 0, v[130:131]
	s_add_i32 s71, s60, s46
	v_lshl_add_u64 v[2:3], v[0:1], 0, s[18:19]
	s_mov_b32 m0, s71
	s_add_i32 s68, s71, 0x2000
	ds_read_b128 v[60:63], v140 offset:16384
	ds_read_b128 v[108:111], v140 offset:17408
	ds_read_b128 v[112:115], v140 offset:18432
	ds_read_b128 v[116:119], v140 offset:19456
	ds_read_b128 v[120:123], v140 offset:20480
	ds_read_b128 v[124:127], v140 offset:21504
	ds_read_b128 v[152:155], v140 offset:22528
	ds_read_b128 v[156:159], v140 offset:23552
	global_load_lds_dwordx4 v[2:3], off
	v_lshl_add_u64 v[2:3], s[38:39], 0, v[134:135]
	s_add_u32 s72, s38, 0x1900
	v_lshl_add_u64 v[4:5], v[2:3], 0, s[18:19]
	s_mov_b32 m0, s68
	s_addc_u32 s73, s39, 0
	s_add_i32 s69, s61, s46
	global_load_lds_dwordx4 v[4:5], off
	v_lshl_add_u64 v[4:5], s[72:73], 0, v[130:131]
	s_mov_b32 m0, s69
	s_add_i32 s70, s69, 0x2000
	global_load_lds_dwordx4 v[4:5], off
	v_lshl_add_u64 v[4:5], s[72:73], 0, v[134:135]
	s_mov_b32 m0, s70
	s_nop 0
	global_load_lds_dwordx4 v[4:5], off
	v_lshl_add_u64 v[4:5], s[36:37], 0, v[128:129]
	v_lshl_add_u64 v[6:7], v[4:5], 0, s[18:19]
	s_mov_b32 m0, s47
	s_nop 0
	global_load_lds_dwordx4 v[6:7], off
	v_lshl_add_u64 v[6:7], s[36:37], 0, v[132:133]
	v_lshl_add_u64 v[136:137], v[6:7], 0, s[18:19]
	s_mov_b32 m0, s48
	s_nop 0
	global_load_lds_dwordx4 v[136:137], off
	s_waitcnt vmcnt(8)
	s_waitcnt lgkmcnt(0)
	s_barrier
	s_setprio 0
	s_waitcnt lgkmcnt(0)
	v_mfma_f32_16x16x32_bf16 v[160:163], v[8:11], v[60:63], 0
	v_mfma_f32_16x16x32_bf16 v[168:171], v[8:11], v[112:115], 0
	v_mfma_f32_16x16x32_bf16 v[176:179], v[8:11], v[120:123], 0
	v_mfma_f32_16x16x32_bf16 v[8:11], v[8:11], v[152:155], 0
	v_mfma_f32_16x16x32_bf16 v[160:163], v[12:15], v[108:111], v[160:163]
	v_mfma_f32_16x16x32_bf16 v[164:167], v[16:19], v[60:63], 0
	v_mfma_f32_16x16x32_bf16 v[168:171], v[12:15], v[116:119], v[168:171]
	v_mfma_f32_16x16x32_bf16 v[172:175], v[16:19], v[112:115], 0
	v_mfma_f32_16x16x32_bf16 v[176:179], v[12:15], v[124:127], v[176:179]
	v_mfma_f32_16x16x32_bf16 v[180:183], v[16:19], v[120:123], 0
	v_mfma_f32_16x16x32_bf16 v[10:13], v[12:15], v[156:159], v[8:11]
	v_mfma_f32_16x16x32_bf16 v[14:17], v[16:19], v[152:155], 0
	v_mfma_f32_16x16x32_bf16 v[14:17], v[20:23], v[156:159], v[14:17]
	v_mfma_f32_16x16x32_bf16 v[164:167], v[20:23], v[108:111], v[164:167]
	v_mfma_f32_16x16x32_bf16 v[172:175], v[20:23], v[116:119], v[172:175]
	v_mfma_f32_16x16x32_bf16 v[180:183], v[20:23], v[124:127], v[180:183]
	s_setprio 1
	s_setprio 0
	v_mfma_f32_16x16x32_bf16 v[18:21], v[24:27], v[60:63], 0
	v_mfma_f32_16x16x32_bf16 v[60:63], v[32:35], v[60:63], 0
	v_mfma_f32_16x16x32_bf16 v[18:21], v[28:31], v[108:111], v[18:21]
	v_mfma_f32_16x16x32_bf16 v[60:63], v[36:39], v[108:111], v[60:63]
	v_mfma_f32_16x16x32_bf16 v[108:111], v[24:27], v[112:115], 0
	v_mfma_f32_16x16x32_bf16 v[112:115], v[32:35], v[112:115], 0
	v_mfma_f32_16x16x32_bf16 v[108:111], v[28:31], v[116:119], v[108:111]
	v_mfma_f32_16x16x32_bf16 v[112:115], v[36:39], v[116:119], v[112:115]
	v_mfma_f32_16x16x32_bf16 v[116:119], v[24:27], v[120:123], 0
	v_mfma_f32_16x16x32_bf16 v[22:25], v[24:27], v[152:155], 0
	v_mfma_f32_16x16x32_bf16 v[116:119], v[28:31], v[124:127], v[116:119]
	v_mfma_f32_16x16x32_bf16 v[120:123], v[32:35], v[120:123], 0
	v_mfma_f32_16x16x32_bf16 v[22:25], v[28:31], v[156:159], v[22:25]
	v_mfma_f32_16x16x32_bf16 v[26:29], v[32:35], v[152:155], 0
	v_mfma_f32_16x16x32_bf16 v[120:123], v[36:39], v[124:127], v[120:123]
	v_mfma_f32_16x16x32_bf16 v[26:29], v[36:39], v[156:159], v[26:29]
	s_setprio 1
	s_barrier
	s_add_i32 s75, 0, 0x18000
	s_add_i32 s74, 0, 0x1c000
	v_add_u32_e32 v8, s75, v139
	v_add_u32_e32 v9, s74, v139
	ds_read_b128 v[30:33], v8
	ds_read_b128 v[34:37], v8 offset:1024
	ds_read_b128 v[124:127], v8 offset:2048
	ds_read_b128 v[152:155], v8 offset:3072
	ds_read_b128 v[156:159], v9
	ds_read_b128 v[184:187], v9 offset:1024
	ds_read_b128 v[188:191], v9 offset:2048
	ds_read_b128 v[192:195], v9 offset:3072
	s_add_u32 s72, s36, 0x18100
	s_addc_u32 s73, s37, 0
	s_mov_b32 m0, s50
	v_lshl_add_u64 v[38:39], s[72:73], 0, v[128:129]
	ds_read_b128 v[196:199], v140 offset:32768
	ds_read_b128 v[200:203], v140 offset:33792
	ds_read_b128 v[204:207], v140 offset:34816
	ds_read_b128 v[208:211], v140 offset:35840
	ds_read_b128 v[212:215], v140 offset:36864
	ds_read_b128 v[216:219], v140 offset:37888
	ds_read_b128 v[220:223], v140 offset:38912
	ds_read_b128 v[224:227], v140 offset:39936
	global_load_lds_dwordx4 v[38:39], off
	v_lshl_add_u64 v[38:39], s[72:73], 0, v[132:133]
	s_mov_b32 m0, s51
	s_nop 0
	global_load_lds_dwordx4 v[38:39], off
	s_waitcnt vmcnt(8)
	s_waitcnt lgkmcnt(0)
	s_barrier
	s_setprio 0
	s_waitcnt lgkmcnt(0)
	v_mfma_f32_16x16x32_bf16 v[64:67], v[30:33], v[196:199], v[64:67]
	v_mfma_f32_16x16x32_bf16 v[68:71], v[124:127], v[196:199], v[68:71]
	v_mfma_f32_16x16x32_bf16 v[72:75], v[30:33], v[204:207], v[72:75]
	v_mfma_f32_16x16x32_bf16 v[76:79], v[124:127], v[204:207], v[76:79]
	v_mfma_f32_16x16x32_bf16 v[80:83], v[30:33], v[212:215], v[80:83]
	v_mfma_f32_16x16x32_bf16 v[84:87], v[124:127], v[212:215], v[84:87]
	v_mfma_f32_16x16x32_bf16 v[88:91], v[30:33], v[220:223], v[88:91]
	v_mfma_f32_16x16x32_bf16 v[92:95], v[124:127], v[220:223], v[92:95]
	v_mfma_f32_16x16x32_bf16 v[64:67], v[34:37], v[200:203], v[64:67]
	v_mfma_f32_16x16x32_bf16 v[68:71], v[152:155], v[200:203], v[68:71]
	v_mfma_f32_16x16x32_bf16 v[72:75], v[34:37], v[208:211], v[72:75]
	v_mfma_f32_16x16x32_bf16 v[76:79], v[152:155], v[208:211], v[76:79]
	v_mfma_f32_16x16x32_bf16 v[80:83], v[34:37], v[216:219], v[80:83]
	v_mfma_f32_16x16x32_bf16 v[84:87], v[152:155], v[216:219], v[84:87]
	v_mfma_f32_16x16x32_bf16 v[88:91], v[34:37], v[224:227], v[88:91]
	v_mfma_f32_16x16x32_bf16 v[92:95], v[152:155], v[224:227], v[92:95]
	s_setprio 1
	s_setprio 0
	v_mfma_f32_16x16x32_bf16 v[96:99], v[156:159], v[196:199], v[96:99]
	v_mfma_f32_16x16x32_bf16 v[100:103], v[188:191], v[196:199], v[100:103]
	v_mfma_f32_16x16x32_bf16 v[104:107], v[156:159], v[204:207], v[104:107]
	v_mfma_f32_16x16x32_bf16 v[38:41], v[188:191], v[204:207], v[40:43]
	v_mfma_f32_16x16x32_bf16 v[42:45], v[156:159], v[212:215], v[44:47]
	v_mfma_f32_16x16x32_bf16 v[46:49], v[188:191], v[212:215], v[48:51]
	v_mfma_f32_16x16x32_bf16 v[50:53], v[156:159], v[220:223], v[52:55]
	v_mfma_f32_16x16x32_bf16 v[54:57], v[188:191], v[220:223], v[56:59]
	v_mfma_f32_16x16x32_bf16 v[96:99], v[184:187], v[200:203], v[96:99]
	v_mfma_f32_16x16x32_bf16 v[100:103], v[192:195], v[200:203], v[100:103]
	v_mfma_f32_16x16x32_bf16 v[104:107], v[184:187], v[208:211], v[104:107]
	v_mfma_f32_16x16x32_bf16 v[38:41], v[192:195], v[208:211], v[38:41]
	v_mfma_f32_16x16x32_bf16 v[42:45], v[184:187], v[216:219], v[42:45]
	v_mfma_f32_16x16x32_bf16 v[46:49], v[192:195], v[216:219], v[46:49]
	v_mfma_f32_16x16x32_bf16 v[50:53], v[184:187], v[224:227], v[50:53]
	v_mfma_f32_16x16x32_bf16 v[54:57], v[192:195], v[224:227], v[54:57]
	s_setprio 1
	s_barrier
	s_add_i32 s75, s75, s46
	s_add_i32 s72, s75, 0x2000
	v_lshl_add_u64 v[58:59], v[0:1], 0, s[20:21]
	s_mov_b32 m0, s75
	s_add_u32 s76, s38, 0x1980
	ds_read_b128 v[196:199], v140 offset:49152
	ds_read_b128 v[200:203], v140 offset:50176
	ds_read_b128 v[204:207], v140 offset:51200
	ds_read_b128 v[208:211], v140 offset:52224
	ds_read_b128 v[212:215], v140 offset:53248
	ds_read_b128 v[216:219], v140 offset:54272
	ds_read_b128 v[220:223], v140 offset:55296
	ds_read_b128 v[224:227], v140 offset:56320
	global_load_lds_dwordx4 v[58:59], off
	v_lshl_add_u64 v[58:59], v[2:3], 0, s[20:21]
	s_mov_b32 m0, s72
	s_addc_u32 s77, s39, 0
	s_add_i32 s73, s74, s46
	global_load_lds_dwordx4 v[58:59], off
	v_lshl_add_u64 v[58:59], s[76:77], 0, v[130:131]
	s_mov_b32 m0, s73
	s_add_i32 s74, s73, 0x2000
	global_load_lds_dwordx4 v[58:59], off
	v_lshl_add_u64 v[58:59], s[76:77], 0, v[134:135]
	s_mov_b32 m0, s74
	s_nop 0
	global_load_lds_dwordx4 v[58:59], off
	v_lshl_add_u64 v[58:59], v[4:5], 0, s[20:21]
	s_mov_b32 m0, s53
	s_nop 0
	global_load_lds_dwordx4 v[58:59], off
	v_lshl_add_u64 v[58:59], v[6:7], 0, s[20:21]
	s_mov_b32 m0, s54
	s_nop 0
	global_load_lds_dwordx4 v[58:59], off
	s_waitcnt vmcnt(8)
	s_waitcnt lgkmcnt(0)
	s_barrier
	s_setprio 0
	s_waitcnt lgkmcnt(0)
	v_mfma_f32_16x16x32_bf16 v[10:13], v[30:33], v[220:223], v[10:13]
	v_mfma_f32_16x16x32_bf16 v[14:17], v[124:127], v[220:223], v[14:17]
	v_mfma_f32_16x16x32_bf16 v[160:163], v[30:33], v[196:199], v[160:163]
	v_mfma_f32_16x16x32_bf16 v[164:167], v[124:127], v[196:199], v[164:167]
	v_mfma_f32_16x16x32_bf16 v[168:171], v[30:33], v[204:207], v[168:171]
	v_mfma_f32_16x16x32_bf16 v[172:175], v[124:127], v[204:207], v[172:175]
	v_mfma_f32_16x16x32_bf16 v[176:179], v[30:33], v[212:215], v[176:179]
	v_mfma_f32_16x16x32_bf16 v[180:183], v[124:127], v[212:215], v[180:183]
	v_mfma_f32_16x16x32_bf16 v[10:13], v[34:37], v[224:227], v[10:13]
	v_mfma_f32_16x16x32_bf16 v[14:17], v[152:155], v[224:227], v[14:17]
	v_mfma_f32_16x16x32_bf16 v[160:163], v[34:37], v[200:203], v[160:163]
	v_mfma_f32_16x16x32_bf16 v[164:167], v[152:155], v[200:203], v[164:167]
	v_mfma_f32_16x16x32_bf16 v[168:171], v[34:37], v[208:211], v[168:171]
	v_mfma_f32_16x16x32_bf16 v[172:175], v[152:155], v[208:211], v[172:175]
	v_mfma_f32_16x16x32_bf16 v[176:179], v[34:37], v[216:219], v[176:179]
	v_mfma_f32_16x16x32_bf16 v[180:183], v[152:155], v[216:219], v[180:183]
	s_setprio 1
	s_setprio 0
	v_mfma_f32_16x16x32_bf16 v[18:21], v[156:159], v[196:199], v[18:21]
	v_mfma_f32_16x16x32_bf16 v[30:33], v[188:191], v[196:199], v[60:63]
	v_mfma_f32_16x16x32_bf16 v[34:37], v[156:159], v[204:207], v[108:111]
	v_mfma_f32_16x16x32_bf16 v[58:61], v[188:191], v[204:207], v[112:115]
	v_mfma_f32_16x16x32_bf16 v[108:111], v[156:159], v[212:215], v[116:119]
	v_mfma_f32_16x16x32_bf16 v[112:115], v[188:191], v[212:215], v[120:123]
	v_mfma_f32_16x16x32_bf16 v[22:25], v[156:159], v[220:223], v[22:25]
	v_mfma_f32_16x16x32_bf16 v[26:29], v[188:191], v[220:223], v[26:29]
	v_mfma_f32_16x16x32_bf16 v[18:21], v[184:187], v[200:203], v[18:21]
	v_mfma_f32_16x16x32_bf16 v[30:33], v[192:195], v[200:203], v[30:33]
	v_mfma_f32_16x16x32_bf16 v[34:37], v[184:187], v[208:211], v[34:37]
	v_mfma_f32_16x16x32_bf16 v[58:61], v[192:195], v[208:211], v[58:61]
	v_mfma_f32_16x16x32_bf16 v[108:111], v[184:187], v[216:219], v[108:111]
	v_mfma_f32_16x16x32_bf16 v[112:115], v[192:195], v[216:219], v[112:115]
	v_mfma_f32_16x16x32_bf16 v[22:25], v[184:187], v[224:227], v[22:25]
	v_mfma_f32_16x16x32_bf16 v[26:29], v[192:195], v[224:227], v[26:29]
	s_setprio 1
	s_barrier
	ds_read_b128 v[116:119], v149
	ds_read_b128 v[120:123], v149 offset:1024
	ds_read_b128 v[124:127], v149 offset:2048
	ds_read_b128 v[152:155], v149 offset:3072
	ds_read_b128 v[156:159], v150
	ds_read_b128 v[184:187], v150 offset:1024
	ds_read_b128 v[188:191], v150 offset:2048
	ds_read_b128 v[192:195], v150 offset:3072
	s_add_u32 s76, s36, 0x18180
	s_addc_u32 s77, s37, 0
	s_mov_b32 m0, s62
	v_lshl_add_u64 v[62:63], s[76:77], 0, v[128:129]
	ds_read_b128 v[196:199], v140
	ds_read_b128 v[200:203], v140 offset:1024
	ds_read_b128 v[204:207], v140 offset:2048
	ds_read_b128 v[208:211], v140 offset:3072
	ds_read_b128 v[212:215], v140 offset:4096
	ds_read_b128 v[216:219], v140 offset:5120
	ds_read_b128 v[220:223], v140 offset:6144
	ds_read_b128 v[224:227], v140 offset:7168
	global_load_lds_dwordx4 v[62:63], off
	v_lshl_add_u64 v[62:63], s[76:77], 0, v[132:133]
	s_mov_b32 m0, s63
	s_nop 0
	global_load_lds_dwordx4 v[62:63], off
	s_waitcnt vmcnt(8)
	s_waitcnt lgkmcnt(0)
	s_barrier
	s_setprio 0
	s_waitcnt lgkmcnt(0)
	v_mfma_f32_16x16x32_bf16 v[62:65], v[116:119], v[196:199], v[64:67]
	v_mfma_f32_16x16x32_bf16 v[66:69], v[124:127], v[196:199], v[68:71]
	v_mfma_f32_16x16x32_bf16 v[70:73], v[116:119], v[204:207], v[72:75]
	v_mfma_f32_16x16x32_bf16 v[74:77], v[124:127], v[204:207], v[76:79]
	v_mfma_f32_16x16x32_bf16 v[78:81], v[116:119], v[212:215], v[80:83]
	v_mfma_f32_16x16x32_bf16 v[82:85], v[124:127], v[212:215], v[84:87]
	v_mfma_f32_16x16x32_bf16 v[86:89], v[116:119], v[220:223], v[88:91]
	v_mfma_f32_16x16x32_bf16 v[90:93], v[124:127], v[220:223], v[92:95]
	v_mfma_f32_16x16x32_bf16 v[62:65], v[120:123], v[200:203], v[62:65]
	v_mfma_f32_16x16x32_bf16 v[66:69], v[152:155], v[200:203], v[66:69]
	v_mfma_f32_16x16x32_bf16 v[70:73], v[120:123], v[208:211], v[70:73]
	v_mfma_f32_16x16x32_bf16 v[74:77], v[152:155], v[208:211], v[74:77]
	v_mfma_f32_16x16x32_bf16 v[78:81], v[120:123], v[216:219], v[78:81]
	v_mfma_f32_16x16x32_bf16 v[82:85], v[152:155], v[216:219], v[82:85]
	v_mfma_f32_16x16x32_bf16 v[86:89], v[120:123], v[224:227], v[86:89]
	v_mfma_f32_16x16x32_bf16 v[90:93], v[152:155], v[224:227], v[90:93]
	s_setprio 1
	s_setprio 0
	v_mfma_f32_16x16x32_bf16 v[94:97], v[156:159], v[196:199], v[96:99]
	v_mfma_f32_16x16x32_bf16 v[98:101], v[188:191], v[196:199], v[100:103]
	v_mfma_f32_16x16x32_bf16 v[102:105], v[156:159], v[204:207], v[104:107]
	v_mfma_f32_16x16x32_bf16 v[38:41], v[188:191], v[204:207], v[38:41]
	v_mfma_f32_16x16x32_bf16 v[42:45], v[156:159], v[212:215], v[42:45]
	v_mfma_f32_16x16x32_bf16 v[46:49], v[188:191], v[212:215], v[46:49]
	v_mfma_f32_16x16x32_bf16 v[50:53], v[156:159], v[220:223], v[50:53]
	v_mfma_f32_16x16x32_bf16 v[54:57], v[188:191], v[220:223], v[54:57]
	v_mfma_f32_16x16x32_bf16 v[94:97], v[184:187], v[200:203], v[94:97]
	v_mfma_f32_16x16x32_bf16 v[98:101], v[192:195], v[200:203], v[98:101]
	v_mfma_f32_16x16x32_bf16 v[102:105], v[184:187], v[208:211], v[102:105]
	v_mfma_f32_16x16x32_bf16 v[38:41], v[192:195], v[208:211], v[38:41]
	v_mfma_f32_16x16x32_bf16 v[42:45], v[184:187], v[216:219], v[42:45]
	v_mfma_f32_16x16x32_bf16 v[46:49], v[192:195], v[216:219], v[46:49]
	v_mfma_f32_16x16x32_bf16 v[50:53], v[184:187], v[224:227], v[50:53]
	v_mfma_f32_16x16x32_bf16 v[54:57], v[192:195], v[224:227], v[54:57]
	s_setprio 1
	s_barrier
	s_mov_b32 m0, s71
	v_lshl_add_u64 v[106:107], v[0:1], 0, s[22:23]
	s_add_u32 s76, s38, 0x1a00
	ds_read_b128 v[196:199], v140 offset:16384
	ds_read_b128 v[200:203], v140 offset:17408
	ds_read_b128 v[204:207], v140 offset:18432
	ds_read_b128 v[208:211], v140 offset:19456
	ds_read_b128 v[212:215], v140 offset:20480
	ds_read_b128 v[216:219], v140 offset:21504
	ds_read_b128 v[220:223], v140 offset:22528
	ds_read_b128 v[224:227], v140 offset:23552
	global_load_lds_dwordx4 v[106:107], off
	v_lshl_add_u64 v[106:107], v[2:3], 0, s[22:23]
	s_mov_b32 m0, s68
	s_addc_u32 s77, s39, 0
	global_load_lds_dwordx4 v[106:107], off
	v_lshl_add_u64 v[106:107], s[76:77], 0, v[130:131]
	s_mov_b32 m0, s69
	s_nop 0
	global_load_lds_dwordx4 v[106:107], off
	v_lshl_add_u64 v[106:107], s[76:77], 0, v[134:135]
	s_mov_b32 m0, s70
	s_nop 0
	global_load_lds_dwordx4 v[106:107], off
	v_lshl_add_u64 v[106:107], v[4:5], 0, s[22:23]
	s_mov_b32 m0, s47
	s_nop 0
	global_load_lds_dwordx4 v[106:107], off
	v_lshl_add_u64 v[106:107], v[6:7], 0, s[22:23]
	s_mov_b32 m0, s48
	s_nop 0
	global_load_lds_dwordx4 v[106:107], off
	s_waitcnt vmcnt(8)
	s_waitcnt lgkmcnt(0)
	s_barrier
	s_setprio 0
	s_waitcnt lgkmcnt(0)
	v_mfma_f32_16x16x32_bf16 v[10:13], v[116:119], v[220:223], v[10:13]
	v_mfma_f32_16x16x32_bf16 v[14:17], v[124:127], v[220:223], v[14:17]
	v_mfma_f32_16x16x32_bf16 v[160:163], v[116:119], v[196:199], v[160:163]
	v_mfma_f32_16x16x32_bf16 v[164:167], v[124:127], v[196:199], v[164:167]
	v_mfma_f32_16x16x32_bf16 v[168:171], v[116:119], v[204:207], v[168:171]
	v_mfma_f32_16x16x32_bf16 v[172:175], v[124:127], v[204:207], v[172:175]
	v_mfma_f32_16x16x32_bf16 v[176:179], v[116:119], v[212:215], v[176:179]
	v_mfma_f32_16x16x32_bf16 v[180:183], v[124:127], v[212:215], v[180:183]
	v_mfma_f32_16x16x32_bf16 v[10:13], v[120:123], v[224:227], v[10:13]
	v_mfma_f32_16x16x32_bf16 v[14:17], v[152:155], v[224:227], v[14:17]
	v_mfma_f32_16x16x32_bf16 v[160:163], v[120:123], v[200:203], v[160:163]
	v_mfma_f32_16x16x32_bf16 v[164:167], v[152:155], v[200:203], v[164:167]
	v_mfma_f32_16x16x32_bf16 v[168:171], v[120:123], v[208:211], v[168:171]
	v_mfma_f32_16x16x32_bf16 v[172:175], v[152:155], v[208:211], v[172:175]
	v_mfma_f32_16x16x32_bf16 v[176:179], v[120:123], v[216:219], v[176:179]
	v_mfma_f32_16x16x32_bf16 v[180:183], v[152:155], v[216:219], v[180:183]
	s_setprio 1
	s_setprio 0
	v_mfma_f32_16x16x32_bf16 v[18:21], v[156:159], v[196:199], v[18:21]
	v_mfma_f32_16x16x32_bf16 v[30:33], v[188:191], v[196:199], v[30:33]
	v_mfma_f32_16x16x32_bf16 v[34:37], v[156:159], v[204:207], v[34:37]
	v_mfma_f32_16x16x32_bf16 v[58:61], v[188:191], v[204:207], v[58:61]
	v_mfma_f32_16x16x32_bf16 v[106:109], v[156:159], v[212:215], v[108:111]
	v_mfma_f32_16x16x32_bf16 v[110:113], v[188:191], v[212:215], v[112:115]
	v_mfma_f32_16x16x32_bf16 v[22:25], v[156:159], v[220:223], v[22:25]
	v_mfma_f32_16x16x32_bf16 v[26:29], v[188:191], v[220:223], v[26:29]
	v_mfma_f32_16x16x32_bf16 v[18:21], v[184:187], v[200:203], v[18:21]
	v_mfma_f32_16x16x32_bf16 v[30:33], v[192:195], v[200:203], v[30:33]
	v_mfma_f32_16x16x32_bf16 v[34:37], v[184:187], v[208:211], v[34:37]
	v_mfma_f32_16x16x32_bf16 v[58:61], v[192:195], v[208:211], v[58:61]
	v_mfma_f32_16x16x32_bf16 v[106:109], v[184:187], v[216:219], v[106:109]
	v_mfma_f32_16x16x32_bf16 v[110:113], v[192:195], v[216:219], v[110:113]
	v_mfma_f32_16x16x32_bf16 v[22:25], v[184:187], v[224:227], v[22:25]
	v_mfma_f32_16x16x32_bf16 v[26:29], v[192:195], v[224:227], v[26:29]
	s_setprio 1
	s_barrier
	ds_read_b128 v[114:117], v8
	ds_read_b128 v[118:121], v8 offset:1024
	ds_read_b128 v[122:125], v8 offset:2048
	ds_read_b128 v[152:155], v8 offset:3072
	ds_read_b128 v[156:159], v9
	ds_read_b128 v[184:187], v9 offset:1024
	ds_read_b128 v[188:191], v9 offset:2048
	ds_read_b128 v[192:195], v9 offset:3072
	s_add_u32 s76, s36, 0x18200
	s_addc_u32 s77, s37, 0
	s_mov_b32 m0, s50
	v_lshl_add_u64 v[126:127], s[76:77], 0, v[128:129]
	ds_read_b128 v[196:199], v140 offset:32768
	ds_read_b128 v[200:203], v140 offset:33792
	ds_read_b128 v[204:207], v140 offset:34816
	ds_read_b128 v[208:211], v140 offset:35840
	ds_read_b128 v[212:215], v140 offset:36864
	ds_read_b128 v[216:219], v140 offset:37888
	ds_read_b128 v[220:223], v140 offset:38912
	ds_read_b128 v[224:227], v140 offset:39936
	global_load_lds_dwordx4 v[126:127], off
	v_lshl_add_u64 v[126:127], s[76:77], 0, v[132:133]
	s_mov_b32 m0, s51
	s_nop 0
	global_load_lds_dwordx4 v[126:127], off
	s_waitcnt vmcnt(8)
	s_waitcnt lgkmcnt(0)
	s_barrier
	s_setprio 0
	s_waitcnt lgkmcnt(0)
	v_mfma_f32_16x16x32_bf16 v[62:65], v[114:117], v[196:199], v[62:65]
	v_mfma_f32_16x16x32_bf16 v[66:69], v[122:125], v[196:199], v[66:69]
	v_mfma_f32_16x16x32_bf16 v[70:73], v[114:117], v[204:207], v[70:73]
	v_mfma_f32_16x16x32_bf16 v[74:77], v[122:125], v[204:207], v[74:77]
	v_mfma_f32_16x16x32_bf16 v[78:81], v[114:117], v[212:215], v[78:81]
	v_mfma_f32_16x16x32_bf16 v[82:85], v[122:125], v[212:215], v[82:85]
	v_mfma_f32_16x16x32_bf16 v[86:89], v[114:117], v[220:223], v[86:89]
	v_mfma_f32_16x16x32_bf16 v[90:93], v[122:125], v[220:223], v[90:93]
	v_mfma_f32_16x16x32_bf16 v[62:65], v[118:121], v[200:203], v[62:65]
	v_mfma_f32_16x16x32_bf16 v[66:69], v[152:155], v[200:203], v[66:69]
	v_mfma_f32_16x16x32_bf16 v[70:73], v[118:121], v[208:211], v[70:73]
	v_mfma_f32_16x16x32_bf16 v[74:77], v[152:155], v[208:211], v[74:77]
	v_mfma_f32_16x16x32_bf16 v[78:81], v[118:121], v[216:219], v[78:81]
	v_mfma_f32_16x16x32_bf16 v[82:85], v[152:155], v[216:219], v[82:85]
	v_mfma_f32_16x16x32_bf16 v[86:89], v[118:121], v[224:227], v[86:89]
	v_mfma_f32_16x16x32_bf16 v[90:93], v[152:155], v[224:227], v[90:93]
	s_setprio 1
	s_setprio 0
	v_mfma_f32_16x16x32_bf16 v[94:97], v[156:159], v[196:199], v[94:97]
	v_mfma_f32_16x16x32_bf16 v[98:101], v[188:191], v[196:199], v[98:101]
	v_mfma_f32_16x16x32_bf16 v[102:105], v[156:159], v[204:207], v[102:105]
	v_mfma_f32_16x16x32_bf16 v[38:41], v[188:191], v[204:207], v[38:41]
	v_mfma_f32_16x16x32_bf16 v[42:45], v[156:159], v[212:215], v[42:45]
	v_mfma_f32_16x16x32_bf16 v[46:49], v[188:191], v[212:215], v[46:49]
	v_mfma_f32_16x16x32_bf16 v[50:53], v[156:159], v[220:223], v[50:53]
	v_mfma_f32_16x16x32_bf16 v[54:57], v[188:191], v[220:223], v[54:57]
	v_mfma_f32_16x16x32_bf16 v[94:97], v[184:187], v[200:203], v[94:97]
	v_mfma_f32_16x16x32_bf16 v[98:101], v[192:195], v[200:203], v[98:101]
	v_mfma_f32_16x16x32_bf16 v[102:105], v[184:187], v[208:211], v[102:105]
	v_mfma_f32_16x16x32_bf16 v[38:41], v[192:195], v[208:211], v[38:41]
	v_mfma_f32_16x16x32_bf16 v[42:45], v[184:187], v[216:219], v[42:45]
	v_mfma_f32_16x16x32_bf16 v[46:49], v[192:195], v[216:219], v[46:49]
	v_mfma_f32_16x16x32_bf16 v[50:53], v[184:187], v[224:227], v[50:53]
	v_mfma_f32_16x16x32_bf16 v[54:57], v[192:195], v[224:227], v[54:57]
	s_setprio 1
	s_barrier
	s_mov_b32 m0, s75
	v_lshl_add_u64 v[0:1], v[0:1], 0, s[24:25]
	s_add_u32 s38, s38, 0x1a80
	ds_read_b128 v[196:199], v140 offset:49152
	ds_read_b128 v[200:203], v140 offset:50176
	ds_read_b128 v[204:207], v140 offset:51200
	ds_read_b128 v[208:211], v140 offset:52224
	ds_read_b128 v[212:215], v140 offset:53248
	ds_read_b128 v[216:219], v140 offset:54272
	ds_read_b128 v[220:223], v140 offset:55296
	ds_read_b128 v[224:227], v140 offset:56320
	global_load_lds_dwordx4 v[0:1], off
	v_lshl_add_u64 v[0:1], v[2:3], 0, s[24:25]
	s_mov_b32 m0, s72
	s_addc_u32 s39, s39, 0
	global_load_lds_dwordx4 v[0:1], off
	v_lshl_add_u64 v[0:1], s[38:39], 0, v[130:131]
	s_mov_b32 m0, s73
	s_nop 0
	global_load_lds_dwordx4 v[0:1], off
	v_lshl_add_u64 v[0:1], s[38:39], 0, v[134:135]
	s_mov_b32 m0, s74
	s_nop 0
	global_load_lds_dwordx4 v[0:1], off
	v_lshl_add_u64 v[0:1], v[4:5], 0, s[24:25]
	s_mov_b32 m0, s53
	s_nop 0
	global_load_lds_dwordx4 v[0:1], off
	v_lshl_add_u64 v[0:1], v[6:7], 0, s[24:25]
	s_mov_b32 m0, s54
	s_nop 0
	global_load_lds_dwordx4 v[0:1], off
	s_waitcnt vmcnt(8)
	s_waitcnt lgkmcnt(0)
	s_barrier
	s_setprio 0
	s_waitcnt lgkmcnt(0)
	v_mfma_f32_16x16x32_bf16 v[0:3], v[114:117], v[196:199], v[160:163]
	v_mfma_f32_16x16x32_bf16 v[4:7], v[122:125], v[196:199], v[164:167]
	v_mfma_f32_16x16x32_bf16 v[10:13], v[114:117], v[220:223], v[10:13]
	v_mfma_f32_16x16x32_bf16 v[14:17], v[122:125], v[220:223], v[14:17]
	v_mfma_f32_16x16x32_bf16 v[0:3], v[118:121], v[200:203], v[0:3]
	v_mfma_f32_16x16x32_bf16 v[4:7], v[152:155], v[200:203], v[4:7]
	v_mfma_f32_16x16x32_bf16 v[160:163], v[114:117], v[204:207], v[168:171]
	v_mfma_f32_16x16x32_bf16 v[164:167], v[122:125], v[204:207], v[172:175]
	v_mfma_f32_16x16x32_bf16 v[168:171], v[114:117], v[212:215], v[176:179]
	v_mfma_f32_16x16x32_bf16 v[172:175], v[122:125], v[212:215], v[180:183]
	v_mfma_f32_16x16x32_bf16 v[10:13], v[118:121], v[224:227], v[10:13]
	v_mfma_f32_16x16x32_bf16 v[14:17], v[152:155], v[224:227], v[14:17]
	v_mfma_f32_16x16x32_bf16 v[160:163], v[118:121], v[208:211], v[160:163]
	v_mfma_f32_16x16x32_bf16 v[164:167], v[152:155], v[208:211], v[164:167]
	v_mfma_f32_16x16x32_bf16 v[168:171], v[118:121], v[216:219], v[168:171]
	v_mfma_f32_16x16x32_bf16 v[172:175], v[152:155], v[216:219], v[172:175]
	s_setprio 1
	s_setprio 0
	v_mfma_f32_16x16x32_bf16 v[18:21], v[156:159], v[196:199], v[18:21]
	v_mfma_f32_16x16x32_bf16 v[30:33], v[188:191], v[196:199], v[30:33]
	v_mfma_f32_16x16x32_bf16 v[34:37], v[156:159], v[204:207], v[34:37]
	v_mfma_f32_16x16x32_bf16 v[58:61], v[188:191], v[204:207], v[58:61]
	v_mfma_f32_16x16x32_bf16 v[106:109], v[156:159], v[212:215], v[106:109]
	v_mfma_f32_16x16x32_bf16 v[110:113], v[188:191], v[212:215], v[110:113]
	v_mfma_f32_16x16x32_bf16 v[22:25], v[156:159], v[220:223], v[22:25]
	v_mfma_f32_16x16x32_bf16 v[26:29], v[188:191], v[220:223], v[26:29]
	v_mfma_f32_16x16x32_bf16 v[18:21], v[184:187], v[200:203], v[18:21]
	v_mfma_f32_16x16x32_bf16 v[30:33], v[192:195], v[200:203], v[30:33]
	v_mfma_f32_16x16x32_bf16 v[34:37], v[184:187], v[208:211], v[34:37]
	v_mfma_f32_16x16x32_bf16 v[58:61], v[192:195], v[208:211], v[58:61]
	v_mfma_f32_16x16x32_bf16 v[106:109], v[184:187], v[216:219], v[106:109]
	v_mfma_f32_16x16x32_bf16 v[110:113], v[192:195], v[216:219], v[110:113]
	v_mfma_f32_16x16x32_bf16 v[22:25], v[184:187], v[224:227], v[22:25]
	v_mfma_f32_16x16x32_bf16 v[26:29], v[192:195], v[224:227], v[26:29]
	s_setprio 1
	s_barrier
	ds_read_b128 v[114:117], v149
	ds_read_b128 v[118:121], v149 offset:1024
	ds_read_b128 v[122:125], v149 offset:2048
	ds_read_b128 v[152:155], v149 offset:3072
	ds_read_b128 v[156:159], v150
	ds_read_b128 v[176:179], v150 offset:1024
	ds_read_b128 v[180:183], v150 offset:2048
	ds_read_b128 v[184:187], v150 offset:3072
	s_add_u32 s36, s36, 0x18280
	s_addc_u32 s37, s37, 0
	s_mov_b32 m0, s62
	v_lshl_add_u64 v[126:127], s[36:37], 0, v[128:129]
	ds_read_b128 v[188:191], v140
	ds_read_b128 v[192:195], v140 offset:1024
	ds_read_b128 v[196:199], v140 offset:2048
	ds_read_b128 v[200:203], v140 offset:3072
	ds_read_b128 v[204:207], v140 offset:4096
	ds_read_b128 v[208:211], v140 offset:5120
	ds_read_b128 v[212:215], v140 offset:6144
	ds_read_b128 v[216:219], v140 offset:7168
	global_load_lds_dwordx4 v[126:127], off
	v_lshl_add_u64 v[126:127], s[36:37], 0, v[132:133]
	s_mov_b32 m0, s63
	s_nop 0
	global_load_lds_dwordx4 v[126:127], off
	s_waitcnt vmcnt(8)
	s_waitcnt lgkmcnt(0)
	s_barrier
	s_setprio 0
	s_waitcnt lgkmcnt(0)
	v_mfma_f32_16x16x32_bf16 v[82:85], v[122:125], v[204:207], v[82:85]
	v_mfma_f32_16x16x32_bf16 v[220:223], v[152:155], v[208:211], v[82:85]
	v_mfma_f32_16x16x32_bf16 v[82:85], v[114:117], v[212:215], v[86:89]
	v_mfma_f32_16x16x32_bf16 v[62:65], v[114:117], v[188:191], v[62:65]
	v_mfma_f32_16x16x32_bf16 v[66:69], v[122:125], v[188:191], v[66:69]
	v_mfma_f32_16x16x32_bf16 v[70:73], v[114:117], v[196:199], v[70:73]
	v_mfma_f32_16x16x32_bf16 v[74:77], v[122:125], v[196:199], v[74:77]
	v_mfma_f32_16x16x32_bf16 v[78:81], v[114:117], v[204:207], v[78:81]
	v_mfma_f32_16x16x32_bf16 v[224:227], v[118:121], v[216:219], v[82:85]
	v_mfma_f32_16x16x32_bf16 v[82:85], v[122:125], v[212:215], v[90:93]
	v_mfma_f32_16x16x32_bf16 v[62:65], v[118:121], v[192:195], v[62:65]
	v_mfma_f32_16x16x32_bf16 v[66:69], v[152:155], v[192:195], v[66:69]
	v_mfma_f32_16x16x32_bf16 v[70:73], v[118:121], v[200:203], v[70:73]
	v_mfma_f32_16x16x32_bf16 v[74:77], v[152:155], v[200:203], v[74:77]
	v_mfma_f32_16x16x32_bf16 v[78:81], v[118:121], v[208:211], v[78:81]
	v_mfma_f32_16x16x32_bf16 v[88:91], v[152:155], v[216:219], v[82:85]
	s_setprio 1
	s_setprio 0
	v_mfma_f32_16x16x32_bf16 v[82:85], v[156:159], v[188:191], v[94:97]
	v_mfma_f32_16x16x32_bf16 v[92:95], v[176:179], v[192:195], v[82:85]
	v_mfma_f32_16x16x32_bf16 v[82:85], v[180:183], v[188:191], v[98:101]
	v_mfma_f32_16x16x32_bf16 v[38:41], v[180:183], v[196:199], v[38:41]
	v_mfma_f32_16x16x32_bf16 v[42:45], v[156:159], v[204:207], v[42:45]
	v_mfma_f32_16x16x32_bf16 v[46:49], v[180:183], v[204:207], v[46:49]
	v_mfma_f32_16x16x32_bf16 v[50:53], v[156:159], v[212:215], v[50:53]
	v_mfma_f32_16x16x32_bf16 v[54:57], v[180:183], v[212:215], v[54:57]
	v_mfma_f32_16x16x32_bf16 v[188:191], v[184:187], v[192:195], v[82:85]
	v_mfma_f32_16x16x32_bf16 v[82:85], v[156:159], v[196:199], v[102:105]
	v_mfma_f32_16x16x32_bf16 v[38:41], v[184:187], v[200:203], v[38:41]
	v_mfma_f32_16x16x32_bf16 v[42:45], v[176:179], v[208:211], v[42:45]
	v_mfma_f32_16x16x32_bf16 v[46:49], v[184:187], v[208:211], v[46:49]
	v_mfma_f32_16x16x32_bf16 v[50:53], v[176:179], v[216:219], v[50:53]
	v_mfma_f32_16x16x32_bf16 v[54:57], v[184:187], v[216:219], v[54:57]
	v_mfma_f32_16x16x32_bf16 v[192:195], v[176:179], v[200:203], v[82:85]
	s_setprio 1
	s_barrier
	s_mov_b32 m0, s71
	v_lshl_add_u64 v[136:137], s[28:29], 0, v[130:131]
	s_add_u32 s36, s28, 0x1800
	ds_read_b128 v[82:85], v140 offset:16384
	ds_read_b128 v[96:99], v140 offset:17408
	ds_read_b128 v[100:103], v140 offset:18432
	ds_read_b128 v[196:199], v140 offset:19456
	ds_read_b128 v[200:203], v140 offset:20480
	ds_read_b128 v[204:207], v140 offset:21504
	ds_read_b128 v[208:211], v140 offset:22528
	ds_read_b128 v[212:215], v140 offset:23552
	global_load_lds_dwordx4 v[136:137], off
	v_lshl_add_u64 v[142:143], s[28:29], 0, v[134:135]
	s_mov_b32 m0, s68
	s_addc_u32 s37, s29, 0
	global_load_lds_dwordx4 v[142:143], off
	v_lshl_add_u64 v[86:87], s[36:37], 0, v[130:131]
	s_mov_b32 m0, s69
	v_lshl_add_u64 v[144:145], s[26:27], 0, v[128:129]
	global_load_lds_dwordx4 v[86:87], off
	v_lshl_add_u64 v[86:87], s[36:37], 0, v[134:135]
	s_mov_b32 m0, s70
	v_lshl_add_u64 v[146:147], s[26:27], 0, v[132:133]
	global_load_lds_dwordx4 v[86:87], off
	s_mov_b32 m0, s47
	s_nop 0
	global_load_lds_dwordx4 v[144:145], off
	s_mov_b32 m0, s48
	s_nop 0
	global_load_lds_dwordx4 v[146:147], off
	s_waitcnt vmcnt(8)
	s_waitcnt lgkmcnt(0)
	s_barrier
	s_setprio 0
	s_waitcnt lgkmcnt(0)
	v_mfma_f32_16x16x32_bf16 v[0:3], v[114:117], v[82:85], v[0:3]
	v_mfma_f32_16x16x32_bf16 v[4:7], v[122:125], v[82:85], v[4:7]
	v_mfma_f32_16x16x32_bf16 v[10:13], v[114:117], v[208:211], v[10:13]
	v_mfma_f32_16x16x32_bf16 v[0:3], v[118:121], v[96:99], v[0:3]
	v_mfma_f32_16x16x32_bf16 v[4:7], v[152:155], v[96:99], v[4:7]
	v_mfma_f32_16x16x32_bf16 v[160:163], v[114:117], v[100:103], v[160:163]
	v_mfma_f32_16x16x32_bf16 v[164:167], v[122:125], v[100:103], v[164:167]
	v_mfma_f32_16x16x32_bf16 v[168:171], v[114:117], v[200:203], v[168:171]
	v_mfma_f32_16x16x32_bf16 v[172:175], v[122:125], v[200:203], v[172:175]
	v_mfma_f32_16x16x32_bf16 v[10:13], v[118:121], v[212:215], v[10:13]
	v_mfma_f32_16x16x32_bf16 v[14:17], v[122:125], v[208:211], v[14:17]
	v_mfma_f32_16x16x32_bf16 v[160:163], v[118:121], v[196:199], v[160:163]
	v_mfma_f32_16x16x32_bf16 v[164:167], v[152:155], v[196:199], v[164:167]
	v_mfma_f32_16x16x32_bf16 v[168:171], v[118:121], v[204:207], v[168:171]
	v_mfma_f32_16x16x32_bf16 v[172:175], v[152:155], v[204:207], v[172:175]
	v_mfma_f32_16x16x32_bf16 v[152:155], v[152:155], v[212:215], v[14:17]
	s_setprio 1
	s_setprio 0
	v_mfma_f32_16x16x32_bf16 v[14:17], v[156:159], v[82:85], v[18:21]
	v_mfma_f32_16x16x32_bf16 v[216:219], v[176:179], v[96:99], v[14:17]
	v_mfma_f32_16x16x32_bf16 v[14:17], v[180:183], v[82:85], v[30:33]
	v_mfma_f32_16x16x32_bf16 v[228:231], v[184:187], v[96:99], v[14:17]
	v_mfma_f32_16x16x32_bf16 v[14:17], v[156:159], v[100:103], v[34:37]
	v_mfma_f32_16x16x32_bf16 v[232:235], v[176:179], v[196:199], v[14:17]
	v_mfma_f32_16x16x32_bf16 v[14:17], v[180:183], v[100:103], v[58:61]
	v_mfma_f32_16x16x32_bf16 v[196:199], v[184:187], v[196:199], v[14:17]
	v_mfma_f32_16x16x32_bf16 v[14:17], v[156:159], v[200:203], v[106:109]
	v_mfma_f32_16x16x32_bf16 v[236:239], v[176:179], v[204:207], v[14:17]
	v_mfma_f32_16x16x32_bf16 v[14:17], v[180:183], v[200:203], v[110:113]
	v_mfma_f32_16x16x32_bf16 v[200:203], v[184:187], v[204:207], v[14:17]
	v_mfma_f32_16x16x32_bf16 v[14:17], v[156:159], v[208:211], v[22:25]
	v_mfma_f32_16x16x32_bf16 v[156:159], v[176:179], v[212:215], v[14:17]
	v_mfma_f32_16x16x32_bf16 v[14:17], v[180:183], v[208:211], v[26:29]
	v_mfma_f32_16x16x32_bf16 v[176:179], v[184:187], v[212:215], v[14:17]
	s_setprio 1
	s_barrier
	ds_read_b128 v[24:27], v8
	ds_read_b128 v[28:31], v8 offset:1024
	ds_read_b128 v[58:61], v8 offset:2048
	ds_read_b128 v[180:183], v8 offset:3072
	ds_read_b128 v[184:187], v9
	ds_read_b128 v[204:207], v9 offset:1024
	ds_read_b128 v[208:211], v9 offset:2048
	ds_read_b128 v[212:215], v9 offset:3072
	s_add_u32 s36, s26, 0x18000
	s_addc_u32 s37, s27, 0
	s_mov_b32 m0, s50
	v_lshl_add_u64 v[8:9], s[36:37], 0, v[128:129]
	ds_read_b128 v[14:17], v140 offset:32768
	ds_read_b128 v[18:21], v140 offset:33792
	ds_read_b128 v[32:35], v140 offset:34816
	ds_read_b128 v[108:111], v140 offset:35840
	ds_read_b128 v[240:243], v140 offset:36864
	ds_read_b128 v[244:247], v140 offset:37888
	ds_read_b128 v[248:251], v140 offset:38912
	ds_read_b128 v[252:255], v140 offset:39936
	global_load_lds_dwordx4 v[8:9], off
	v_lshl_add_u64 v[8:9], s[36:37], 0, v[132:133]
	s_mov_b32 m0, s51
	s_nop 0
	global_load_lds_dwordx4 v[8:9], off
	s_waitcnt vmcnt(8)
	s_waitcnt lgkmcnt(0)
	s_barrier
	s_setprio 0
	s_waitcnt lgkmcnt(0)
	v_mfma_f32_16x16x32_bf16 v[62:65], v[24:27], v[14:17], v[62:65]
	v_mfma_f32_16x16x32_bf16 v[112:115], v[28:31], v[18:21], v[62:65]
	v_mfma_f32_16x16x32_bf16 v[62:65], v[58:61], v[14:17], v[66:69]
	v_mfma_f32_16x16x32_bf16 v[116:119], v[180:183], v[18:21], v[62:65]
	v_mfma_f32_16x16x32_bf16 v[62:65], v[24:27], v[32:35], v[70:73]
	v_mfma_f32_16x16x32_bf16 v[96:99], v[28:31], v[108:111], v[62:65]
	v_mfma_f32_16x16x32_bf16 v[62:65], v[58:61], v[32:35], v[74:77]
	v_mfma_f32_16x16x32_bf16 v[100:103], v[180:183], v[108:111], v[62:65]
	v_mfma_f32_16x16x32_bf16 v[62:65], v[24:27], v[240:243], v[78:81]
	v_mfma_f32_16x16x32_bf16 v[80:83], v[28:31], v[244:247], v[62:65]
	v_mfma_f32_16x16x32_bf16 v[62:65], v[58:61], v[240:243], v[220:223]
	v_mfma_f32_16x16x32_bf16 v[84:87], v[180:183], v[244:247], v[62:65]
	v_mfma_f32_16x16x32_bf16 v[62:65], v[24:27], v[248:251], v[224:227]
	v_mfma_f32_16x16x32_bf16 v[68:71], v[58:61], v[248:251], v[88:91]
	v_mfma_f32_16x16x32_bf16 v[64:67], v[28:31], v[252:255], v[62:65]
	v_mfma_f32_16x16x32_bf16 v[68:71], v[180:183], v[252:255], v[68:71]
	s_setprio 1
	s_setprio 0
	v_mfma_f32_16x16x32_bf16 v[72:75], v[184:187], v[14:17], v[92:95]
	v_mfma_f32_16x16x32_bf16 v[14:17], v[208:211], v[14:17], v[188:191]
	v_mfma_f32_16x16x32_bf16 v[124:127], v[212:215], v[18:21], v[14:17]
	v_mfma_f32_16x16x32_bf16 v[14:17], v[184:187], v[32:35], v[192:195]
	v_mfma_f32_16x16x32_bf16 v[104:107], v[204:207], v[108:111], v[14:17]
	v_mfma_f32_16x16x32_bf16 v[14:17], v[208:211], v[32:35], v[38:41]
	v_mfma_f32_16x16x32_bf16 v[108:111], v[212:215], v[108:111], v[14:17]
	v_mfma_f32_16x16x32_bf16 v[14:17], v[184:187], v[240:243], v[42:45]
	v_mfma_f32_16x16x32_bf16 v[88:91], v[204:207], v[244:247], v[14:17]
	v_mfma_f32_16x16x32_bf16 v[14:17], v[208:211], v[240:243], v[46:49]
	v_mfma_f32_16x16x32_bf16 v[92:95], v[212:215], v[244:247], v[14:17]
	v_mfma_f32_16x16x32_bf16 v[14:17], v[184:187], v[248:251], v[50:53]
	v_mfma_f32_16x16x32_bf16 v[120:123], v[204:207], v[18:21], v[72:75]
	v_mfma_f32_16x16x32_bf16 v[72:75], v[204:207], v[252:255], v[14:17]
	v_mfma_f32_16x16x32_bf16 v[14:17], v[208:211], v[248:251], v[54:57]
	v_mfma_f32_16x16x32_bf16 v[76:79], v[212:215], v[252:255], v[14:17]
	s_setprio 1
	s_barrier
	s_mov_b32 m0, s75
	v_lshl_add_u64 v[8:9], v[136:137], 0, s[14:15]
	s_add_u32 s36, s28, 0x1880
	ds_read_b128 v[40:43], v140 offset:49152
	ds_read_b128 v[44:47], v140 offset:50176
	ds_read_b128 v[188:191], v140 offset:51200
	ds_read_b128 v[192:195], v140 offset:52224
	ds_read_b128 v[220:223], v140 offset:53248
	ds_read_b128 v[224:227], v140 offset:54272
	ds_read_b128 v[240:243], v140 offset:55296
	ds_read_b128 v[244:247], v140 offset:56320
	global_load_lds_dwordx4 v[8:9], off
	v_lshl_add_u64 v[8:9], v[142:143], 0, s[14:15]
	s_mov_b32 m0, s72
	s_addc_u32 s37, s29, 0
	global_load_lds_dwordx4 v[8:9], off
	v_lshl_add_u64 v[8:9], s[36:37], 0, v[130:131]
	s_mov_b32 m0, s73
	s_nop 0
	global_load_lds_dwordx4 v[8:9], off
	v_lshl_add_u64 v[8:9], s[36:37], 0, v[134:135]
	s_mov_b32 m0, s74
	s_nop 0
	global_load_lds_dwordx4 v[8:9], off
	v_lshl_add_u64 v[8:9], v[144:145], 0, s[14:15]
	s_mov_b32 m0, s53
	s_nop 0
	global_load_lds_dwordx4 v[8:9], off
	v_lshl_add_u64 v[8:9], v[146:147], 0, s[14:15]
	s_mov_b32 m0, s54
	s_nop 0
	global_load_lds_dwordx4 v[8:9], off
	s_waitcnt vmcnt(8)
	s_waitcnt lgkmcnt(0)
	s_barrier
	s_setprio 0
	s_waitcnt lgkmcnt(0)
	v_mfma_f32_16x16x32_bf16 v[0:3], v[24:27], v[40:43], v[0:3]
	v_mfma_f32_16x16x32_bf16 v[48:51], v[28:31], v[44:47], v[0:3]
	v_mfma_f32_16x16x32_bf16 v[0:3], v[58:61], v[40:43], v[4:7]
	v_mfma_f32_16x16x32_bf16 v[52:55], v[180:183], v[44:47], v[0:3]
	v_mfma_f32_16x16x32_bf16 v[0:3], v[24:27], v[188:191], v[160:163]
	v_mfma_f32_16x16x32_bf16 v[32:35], v[28:31], v[192:195], v[0:3]
	v_mfma_f32_16x16x32_bf16 v[0:3], v[58:61], v[188:191], v[164:167]
	v_mfma_f32_16x16x32_bf16 v[36:39], v[180:183], v[192:195], v[0:3]
	v_mfma_f32_16x16x32_bf16 v[0:3], v[24:27], v[220:223], v[168:171]
	v_mfma_f32_16x16x32_bf16 v[16:19], v[28:31], v[224:227], v[0:3]
	v_mfma_f32_16x16x32_bf16 v[0:3], v[58:61], v[220:223], v[172:175]
	v_mfma_f32_16x16x32_bf16 v[20:23], v[180:183], v[224:227], v[0:3]
	v_mfma_f32_16x16x32_bf16 v[0:3], v[24:27], v[240:243], v[10:13]
	v_mfma_f32_16x16x32_bf16 v[4:7], v[58:61], v[240:243], v[152:155]
	v_mfma_f32_16x16x32_bf16 v[0:3], v[28:31], v[244:247], v[0:3]
	v_mfma_f32_16x16x32_bf16 v[4:7], v[180:183], v[244:247], v[4:7]
	s_setprio 1
	s_setprio 0
	v_mfma_f32_16x16x32_bf16 v[8:11], v[184:187], v[40:43], v[216:219]
	v_mfma_f32_16x16x32_bf16 v[56:59], v[204:207], v[44:47], v[8:11]
	v_mfma_f32_16x16x32_bf16 v[8:11], v[208:211], v[40:43], v[228:231]
	v_mfma_f32_16x16x32_bf16 v[60:63], v[212:215], v[44:47], v[8:11]
	v_mfma_f32_16x16x32_bf16 v[8:11], v[184:187], v[188:191], v[232:235]
	v_mfma_f32_16x16x32_bf16 v[40:43], v[204:207], v[192:195], v[8:11]
	v_mfma_f32_16x16x32_bf16 v[8:11], v[208:211], v[188:191], v[196:199]
	v_mfma_f32_16x16x32_bf16 v[44:47], v[212:215], v[192:195], v[8:11]
	v_mfma_f32_16x16x32_bf16 v[8:11], v[184:187], v[220:223], v[236:239]
	v_mfma_f32_16x16x32_bf16 v[24:27], v[204:207], v[224:227], v[8:11]
	v_mfma_f32_16x16x32_bf16 v[8:11], v[208:211], v[220:223], v[200:203]
	v_mfma_f32_16x16x32_bf16 v[28:31], v[212:215], v[224:227], v[8:11]
	v_mfma_f32_16x16x32_bf16 v[8:11], v[184:187], v[240:243], v[156:159]
	v_mfma_f32_16x16x32_bf16 v[12:15], v[208:211], v[240:243], v[176:179]
	v_mfma_f32_16x16x32_bf16 v[8:11], v[204:207], v[244:247], v[8:11]
	v_mfma_f32_16x16x32_bf16 v[12:15], v[212:215], v[244:247], v[12:15]
	s_setprio 1
	s_barrier
	s_andn2_b64 vcc, exec, s[16:17]
	s_cbranch_vccnz .LBB0_1070
	s_barrier

.LBB0_1243:
	ds_read_b128 v[144:147], v155
	ds_read_b128 v[158:161], v155 offset:1024
	ds_read_b128 v[162:165], v155 offset:2048
	ds_read_b128 v[166:169], v155 offset:3072
	ds_read_b128 v[170:173], v156
	ds_read_b128 v[174:177], v156 offset:1024
	ds_read_b128 v[178:181], v156 offset:2048
	ds_read_b128 v[182:185], v156 offset:3072
	s_add_u32 s30, s28, 0x100
	s_addc_u32 s31, s29, 0
	s_cmp_eq_u32 s61, 12
	s_cselect_b32 s39, s23, s31
	s_cselect_b32 s38, s22, s30
	s_cselect_b32 s37, s25, s21
	s_cselect_b32 s36, s24, s19
	v_lshl_add_u64 v[150:151], s[28:29], 0, v[138:139]
	s_add_i32 m0, s27, 0xc000
	ds_read_b128 v[186:189], v157
	ds_read_b128 v[190:193], v157 offset:1024
	ds_read_b128 v[194:197], v157 offset:2048
	ds_read_b128 v[198:201], v157 offset:3072
	ds_read_b128 v[202:205], v157 offset:4096
	ds_read_b128 v[206:209], v157 offset:5120
	ds_read_b128 v[210:213], v157 offset:6144
	ds_read_b128 v[214:217], v157 offset:7168
	global_load_lds_dwordx4 v[150:151], off
	v_lshl_add_u64 v[150:151], s[28:29], 0, v[136:137]
	s_add_i32 m0, s27, 0xe000
	s_nop 0
	global_load_lds_dwordx4 v[150:151], off
	s_waitcnt vmcnt(8)
	s_waitcnt lgkmcnt(0)
	s_barrier
	s_setprio 0
	s_waitcnt lgkmcnt(0)
	v_mfma_f32_16x16x32_bf16 v[124:127], v[144:147], v[186:189], v[124:127]
	v_mfma_f32_16x16x32_bf16 v[120:123], v[162:165], v[186:189], v[120:123]
	v_mfma_f32_16x16x32_bf16 v[116:119], v[144:147], v[194:197], v[116:119]
	v_mfma_f32_16x16x32_bf16 v[112:115], v[162:165], v[194:197], v[112:115]
	v_mfma_f32_16x16x32_bf16 v[108:111], v[144:147], v[202:205], v[108:111]
	v_mfma_f32_16x16x32_bf16 v[100:103], v[162:165], v[202:205], v[100:103]
	v_mfma_f32_16x16x32_bf16 v[92:95], v[144:147], v[210:213], v[92:95]
	v_mfma_f32_16x16x32_bf16 v[80:83], v[162:165], v[210:213], v[80:83]
	v_mfma_f32_16x16x32_bf16 v[124:127], v[158:161], v[190:193], v[124:127]
	v_mfma_f32_16x16x32_bf16 v[120:123], v[166:169], v[190:193], v[120:123]
	v_mfma_f32_16x16x32_bf16 v[116:119], v[158:161], v[198:201], v[116:119]
	v_mfma_f32_16x16x32_bf16 v[112:115], v[166:169], v[198:201], v[112:115]
	v_mfma_f32_16x16x32_bf16 v[108:111], v[158:161], v[206:209], v[108:111]
	v_mfma_f32_16x16x32_bf16 v[100:103], v[166:169], v[206:209], v[100:103]
	v_mfma_f32_16x16x32_bf16 v[92:95], v[158:161], v[214:217], v[92:95]
	v_mfma_f32_16x16x32_bf16 v[80:83], v[166:169], v[214:217], v[80:83]
	s_setprio 1
	s_setprio 0
	v_mfma_f32_16x16x32_bf16 v[104:107], v[170:173], v[186:189], v[104:107]
	v_mfma_f32_16x16x32_bf16 v[96:99], v[178:181], v[186:189], v[96:99]
	v_mfma_f32_16x16x32_bf16 v[88:91], v[170:173], v[194:197], v[88:91]
	v_mfma_f32_16x16x32_bf16 v[84:87], v[178:181], v[194:197], v[84:87]
	v_mfma_f32_16x16x32_bf16 v[76:79], v[170:173], v[202:205], v[76:79]
	v_mfma_f32_16x16x32_bf16 v[72:75], v[178:181], v[202:205], v[72:75]
	v_mfma_f32_16x16x32_bf16 v[68:71], v[170:173], v[210:213], v[68:71]
	v_mfma_f32_16x16x32_bf16 v[64:67], v[178:181], v[210:213], v[64:67]
	v_mfma_f32_16x16x32_bf16 v[104:107], v[174:177], v[190:193], v[104:107]
	v_mfma_f32_16x16x32_bf16 v[96:99], v[182:185], v[190:193], v[96:99]
	v_mfma_f32_16x16x32_bf16 v[88:91], v[174:177], v[198:201], v[88:91]
	v_mfma_f32_16x16x32_bf16 v[84:87], v[182:185], v[198:201], v[84:87]
	v_mfma_f32_16x16x32_bf16 v[76:79], v[174:177], v[206:209], v[76:79]
	v_mfma_f32_16x16x32_bf16 v[72:75], v[182:185], v[206:209], v[72:75]
	v_mfma_f32_16x16x32_bf16 v[68:71], v[174:177], v[214:217], v[68:71]
	v_mfma_f32_16x16x32_bf16 v[64:67], v[182:185], v[214:217], v[64:67]
	s_setprio 1
	s_barrier
	s_add_i32 s28, s57, s48
	v_lshl_add_u64 v[150:151], s[36:37], 0, v[132:133]
	s_mov_b32 m0, s28
	ds_read_b128 v[186:189], v157 offset:16384
	ds_read_b128 v[190:193], v157 offset:17408
	ds_read_b128 v[194:197], v157 offset:18432
	ds_read_b128 v[198:201], v157 offset:19456
	ds_read_b128 v[202:205], v157 offset:20480
	ds_read_b128 v[206:209], v157 offset:21504
	ds_read_b128 v[210:213], v157 offset:22528
	ds_read_b128 v[214:217], v157 offset:23552
	global_load_lds_dwordx4 v[150:151], off
	s_add_i32 m0, s28, 0x2000
	s_add_u32 s28, s36, 0x40000
	v_lshl_add_u64 v[218:219], s[36:37], 0, v[128:129]
	s_addc_u32 s29, s37, 0
	s_add_i32 s62, s58, s48
	global_load_lds_dwordx4 v[218:219], off
	v_lshl_add_u64 v[220:221], s[28:29], 0, v[132:133]
	s_mov_b32 m0, s62
	v_lshl_add_u64 v[222:223], s[38:39], 0, v[130:131]
	global_load_lds_dwordx4 v[220:221], off
	v_lshl_add_u64 v[220:221], s[28:29], 0, v[128:129]
	s_add_i32 m0, s62, 0x2000
	s_nop 0
	global_load_lds_dwordx4 v[220:221], off
	v_lshl_add_u64 v[220:221], s[38:39], 0, v[134:135]
	s_mov_b32 m0, s27
	s_nop 0
	global_load_lds_dwordx4 v[220:221], off
	s_mov_b32 m0, s50
	s_nop 0
	global_load_lds_dwordx4 v[222:223], off
	s_waitcnt vmcnt(8)
	s_waitcnt lgkmcnt(0)
	s_barrier
	s_setprio 0
	s_waitcnt lgkmcnt(0)
	v_mfma_f32_16x16x32_bf16 v[60:63], v[144:147], v[186:189], v[60:63]
	v_mfma_f32_16x16x32_bf16 v[56:59], v[162:165], v[186:189], v[56:59]
	v_mfma_f32_16x16x32_bf16 v[48:51], v[144:147], v[194:197], v[48:51]
	v_mfma_f32_16x16x32_bf16 v[40:43], v[162:165], v[194:197], v[40:43]
	v_mfma_f32_16x16x32_bf16 v[32:35], v[144:147], v[202:205], v[32:35]
	v_mfma_f32_16x16x32_bf16 v[24:27], v[162:165], v[202:205], v[24:27]
	v_mfma_f32_16x16x32_bf16 v[16:19], v[144:147], v[210:213], v[16:19]
	v_mfma_f32_16x16x32_bf16 v[8:11], v[162:165], v[210:213], v[8:11]
	v_mfma_f32_16x16x32_bf16 v[60:63], v[158:161], v[190:193], v[60:63]
	v_mfma_f32_16x16x32_bf16 v[56:59], v[166:169], v[190:193], v[56:59]
	v_mfma_f32_16x16x32_bf16 v[48:51], v[158:161], v[198:201], v[48:51]
	v_mfma_f32_16x16x32_bf16 v[40:43], v[166:169], v[198:201], v[40:43]
	v_mfma_f32_16x16x32_bf16 v[32:35], v[158:161], v[206:209], v[32:35]
	v_mfma_f32_16x16x32_bf16 v[24:27], v[166:169], v[206:209], v[24:27]
	v_mfma_f32_16x16x32_bf16 v[16:19], v[158:161], v[214:217], v[16:19]
	v_mfma_f32_16x16x32_bf16 v[8:11], v[166:169], v[214:217], v[8:11]
	s_setprio 1
	s_setprio 0
	v_mfma_f32_16x16x32_bf16 v[52:55], v[170:173], v[186:189], v[52:55]
	v_mfma_f32_16x16x32_bf16 v[44:47], v[178:181], v[186:189], v[44:47]
	v_mfma_f32_16x16x32_bf16 v[36:39], v[170:173], v[194:197], v[36:39]
	v_mfma_f32_16x16x32_bf16 v[28:31], v[178:181], v[194:197], v[28:31]
	v_mfma_f32_16x16x32_bf16 v[20:23], v[170:173], v[202:205], v[20:23]
	v_mfma_f32_16x16x32_bf16 v[12:15], v[178:181], v[202:205], v[12:15]
	v_mfma_f32_16x16x32_bf16 v[4:7], v[170:173], v[210:213], v[4:7]
	v_mfma_f32_16x16x32_bf16 v[0:3], v[178:181], v[210:213], v[0:3]
	v_mfma_f32_16x16x32_bf16 v[52:55], v[174:177], v[190:193], v[52:55]
	v_mfma_f32_16x16x32_bf16 v[44:47], v[182:185], v[190:193], v[44:47]
	v_mfma_f32_16x16x32_bf16 v[36:39], v[174:177], v[198:201], v[36:39]
	v_mfma_f32_16x16x32_bf16 v[28:31], v[182:185], v[198:201], v[28:31]
	v_mfma_f32_16x16x32_bf16 v[20:23], v[174:177], v[206:209], v[20:23]
	v_mfma_f32_16x16x32_bf16 v[12:15], v[182:185], v[206:209], v[12:15]
	v_mfma_f32_16x16x32_bf16 v[4:7], v[174:177], v[214:217], v[4:7]
	v_mfma_f32_16x16x32_bf16 v[0:3], v[182:185], v[214:217], v[0:3]
	s_setprio 1
	s_barrier
	s_add_i32 s62, 0, 0x18000
	v_add_u32_e32 v148, s62, v153
	s_add_i32 s63, 0, 0x1c000
	ds_read_b128 v[144:147], v148
	ds_read_b128 v[158:161], v148 offset:1024
	ds_read_b128 v[162:165], v148 offset:2048
	ds_read_b128 v[166:169], v148 offset:3072
	v_add_u32_e32 v148, s63, v153
	ds_read_b128 v[170:173], v148
	ds_read_b128 v[174:177], v148 offset:1024
	ds_read_b128 v[178:181], v148 offset:2048
	ds_read_b128 v[182:185], v148 offset:3072
	s_add_u32 s28, s38, 0x40000
	s_addc_u32 s29, s39, 0
	s_mov_b32 m0, s51
	v_lshl_add_u64 v[224:225], s[28:29], 0, v[134:135]
	ds_read_b128 v[186:189], v157 offset:32768
	ds_read_b128 v[190:193], v157 offset:33792
	ds_read_b128 v[194:197], v157 offset:34816
	ds_read_b128 v[198:201], v157 offset:35840
	ds_read_b128 v[202:205], v157 offset:36864
	ds_read_b128 v[206:209], v157 offset:37888
	ds_read_b128 v[210:213], v157 offset:38912
	ds_read_b128 v[214:217], v157 offset:39936
	global_load_lds_dwordx4 v[224:225], off
	v_lshl_add_u64 v[224:225], s[28:29], 0, v[130:131]
	s_mov_b32 m0, s52
	s_nop 0
	global_load_lds_dwordx4 v[224:225], off
	s_waitcnt vmcnt(8)
	s_waitcnt lgkmcnt(0)
	s_barrier
	s_setprio 0
	s_waitcnt lgkmcnt(0)
	v_mfma_f32_16x16x32_bf16 v[124:127], v[144:147], v[186:189], v[124:127]
	v_mfma_f32_16x16x32_bf16 v[120:123], v[162:165], v[186:189], v[120:123]
	v_mfma_f32_16x16x32_bf16 v[116:119], v[144:147], v[194:197], v[116:119]
	v_mfma_f32_16x16x32_bf16 v[112:115], v[162:165], v[194:197], v[112:115]
	v_mfma_f32_16x16x32_bf16 v[108:111], v[144:147], v[202:205], v[108:111]
	v_mfma_f32_16x16x32_bf16 v[100:103], v[162:165], v[202:205], v[100:103]
	v_mfma_f32_16x16x32_bf16 v[92:95], v[144:147], v[210:213], v[92:95]
	v_mfma_f32_16x16x32_bf16 v[80:83], v[162:165], v[210:213], v[80:83]
	v_mfma_f32_16x16x32_bf16 v[124:127], v[158:161], v[190:193], v[124:127]
	v_mfma_f32_16x16x32_bf16 v[120:123], v[166:169], v[190:193], v[120:123]
	v_mfma_f32_16x16x32_bf16 v[116:119], v[158:161], v[198:201], v[116:119]
	v_mfma_f32_16x16x32_bf16 v[112:115], v[166:169], v[198:201], v[112:115]
	v_mfma_f32_16x16x32_bf16 v[108:111], v[158:161], v[206:209], v[108:111]
	v_mfma_f32_16x16x32_bf16 v[100:103], v[166:169], v[206:209], v[100:103]
	v_mfma_f32_16x16x32_bf16 v[92:95], v[158:161], v[214:217], v[92:95]
	v_mfma_f32_16x16x32_bf16 v[80:83], v[166:169], v[214:217], v[80:83]
	s_setprio 1
	s_setprio 0
	v_mfma_f32_16x16x32_bf16 v[104:107], v[170:173], v[186:189], v[104:107]
	v_mfma_f32_16x16x32_bf16 v[96:99], v[178:181], v[186:189], v[96:99]
	v_mfma_f32_16x16x32_bf16 v[88:91], v[170:173], v[194:197], v[88:91]
	v_mfma_f32_16x16x32_bf16 v[84:87], v[178:181], v[194:197], v[84:87]
	v_mfma_f32_16x16x32_bf16 v[76:79], v[170:173], v[202:205], v[76:79]
	v_mfma_f32_16x16x32_bf16 v[72:75], v[178:181], v[202:205], v[72:75]
	v_mfma_f32_16x16x32_bf16 v[68:71], v[170:173], v[210:213], v[68:71]
	v_mfma_f32_16x16x32_bf16 v[64:67], v[178:181], v[210:213], v[64:67]
	v_mfma_f32_16x16x32_bf16 v[104:107], v[174:177], v[190:193], v[104:107]
	v_mfma_f32_16x16x32_bf16 v[96:99], v[182:185], v[190:193], v[96:99]
	v_mfma_f32_16x16x32_bf16 v[88:91], v[174:177], v[198:201], v[88:91]
	v_mfma_f32_16x16x32_bf16 v[84:87], v[182:185], v[198:201], v[84:87]
	v_mfma_f32_16x16x32_bf16 v[76:79], v[174:177], v[206:209], v[76:79]
	v_mfma_f32_16x16x32_bf16 v[72:75], v[182:185], v[206:209], v[72:75]
	v_mfma_f32_16x16x32_bf16 v[68:71], v[174:177], v[214:217], v[68:71]
	v_mfma_f32_16x16x32_bf16 v[64:67], v[182:185], v[214:217], v[64:67]
	s_setprio 1
	s_barrier
	s_add_i32 s28, s62, s48
	v_lshl_add_u64 v[150:151], v[150:151], 0, s[14:15]
	s_mov_b32 m0, s28
	ds_read_b128 v[186:189], v157 offset:49152
	ds_read_b128 v[190:193], v157 offset:50176
	ds_read_b128 v[194:197], v157 offset:51200
	ds_read_b128 v[198:201], v157 offset:52224
	ds_read_b128 v[202:205], v157 offset:53248
	ds_read_b128 v[206:209], v157 offset:54272
	ds_read_b128 v[210:213], v157 offset:55296
	ds_read_b128 v[214:217], v157 offset:56320
	global_load_lds_dwordx4 v[150:151], off
	s_add_i32 m0, s28, 0x2000
	s_add_u32 s28, s36, 0x40080
	v_lshl_add_u64 v[150:151], v[218:219], 0, s[14:15]
	s_addc_u32 s29, s37, 0
	s_add_i32 s36, s63, s48
	global_load_lds_dwordx4 v[150:151], off
	v_lshl_add_u64 v[150:151], s[28:29], 0, v[132:133]
	s_mov_b32 m0, s36
	s_nop 0
	global_load_lds_dwordx4 v[150:151], off
	v_lshl_add_u64 v[150:151], s[28:29], 0, v[128:129]
	s_add_i32 m0, s36, 0x2000
	s_nop 0
	global_load_lds_dwordx4 v[150:151], off
	v_lshl_add_u64 v[150:151], v[220:221], 0, s[14:15]
	s_mov_b32 m0, s53
	s_nop 0
	global_load_lds_dwordx4 v[150:151], off
	v_lshl_add_u64 v[150:151], v[222:223], 0, s[14:15]
	s_mov_b32 m0, s54
	s_nop 0
	global_load_lds_dwordx4 v[150:151], off
	s_waitcnt vmcnt(8)
	s_waitcnt lgkmcnt(0)
	s_barrier
	s_setprio 0
	s_waitcnt lgkmcnt(0)
	v_mfma_f32_16x16x32_bf16 v[60:63], v[144:147], v[186:189], v[60:63]
	v_mfma_f32_16x16x32_bf16 v[56:59], v[162:165], v[186:189], v[56:59]
	v_mfma_f32_16x16x32_bf16 v[48:51], v[144:147], v[194:197], v[48:51]
	v_mfma_f32_16x16x32_bf16 v[40:43], v[162:165], v[194:197], v[40:43]
	v_mfma_f32_16x16x32_bf16 v[32:35], v[144:147], v[202:205], v[32:35]
	v_mfma_f32_16x16x32_bf16 v[24:27], v[162:165], v[202:205], v[24:27]
	v_mfma_f32_16x16x32_bf16 v[16:19], v[144:147], v[210:213], v[16:19]
	v_mfma_f32_16x16x32_bf16 v[8:11], v[162:165], v[210:213], v[8:11]
	v_mfma_f32_16x16x32_bf16 v[60:63], v[158:161], v[190:193], v[60:63]
	v_mfma_f32_16x16x32_bf16 v[56:59], v[166:169], v[190:193], v[56:59]
	v_mfma_f32_16x16x32_bf16 v[48:51], v[158:161], v[198:201], v[48:51]
	v_mfma_f32_16x16x32_bf16 v[40:43], v[166:169], v[198:201], v[40:43]
	v_mfma_f32_16x16x32_bf16 v[32:35], v[158:161], v[206:209], v[32:35]
	v_mfma_f32_16x16x32_bf16 v[24:27], v[166:169], v[206:209], v[24:27]
	v_mfma_f32_16x16x32_bf16 v[16:19], v[158:161], v[214:217], v[16:19]
	v_mfma_f32_16x16x32_bf16 v[8:11], v[166:169], v[214:217], v[8:11]
	s_setprio 1
	s_setprio 0
	v_mfma_f32_16x16x32_bf16 v[52:55], v[170:173], v[186:189], v[52:55]
	v_mfma_f32_16x16x32_bf16 v[44:47], v[178:181], v[186:189], v[44:47]
	v_mfma_f32_16x16x32_bf16 v[36:39], v[170:173], v[194:197], v[36:39]
	v_mfma_f32_16x16x32_bf16 v[28:31], v[178:181], v[194:197], v[28:31]
	v_mfma_f32_16x16x32_bf16 v[20:23], v[170:173], v[202:205], v[20:23]
	v_mfma_f32_16x16x32_bf16 v[12:15], v[178:181], v[202:205], v[12:15]
	v_mfma_f32_16x16x32_bf16 v[4:7], v[170:173], v[210:213], v[4:7]
	v_mfma_f32_16x16x32_bf16 v[0:3], v[178:181], v[210:213], v[0:3]
	v_mfma_f32_16x16x32_bf16 v[52:55], v[174:177], v[190:193], v[52:55]
	v_mfma_f32_16x16x32_bf16 v[44:47], v[182:185], v[190:193], v[44:47]
	v_mfma_f32_16x16x32_bf16 v[36:39], v[174:177], v[198:201], v[36:39]
	v_mfma_f32_16x16x32_bf16 v[28:31], v[182:185], v[198:201], v[28:31]
	v_mfma_f32_16x16x32_bf16 v[20:23], v[174:177], v[206:209], v[20:23]
	v_mfma_f32_16x16x32_bf16 v[12:15], v[182:185], v[206:209], v[12:15]
	v_mfma_f32_16x16x32_bf16 v[4:7], v[174:177], v[214:217], v[4:7]
	v_mfma_f32_16x16x32_bf16 v[0:3], v[182:185], v[214:217], v[0:3]
	s_setprio 1
	s_barrier
	s_add_i32 s61, s61, 2
	s_add_u32 s19, s19, 0x100
	s_addc_u32 s21, s21, 0
	s_cmp_gt_u32 s61, 13
	s_mov_b64 s[28:29], s[30:31]
	s_cbranch_scc0 .LBB0_1243
	s_and_b64 vcc, exec, s[16:17]
	s_cbranch_vccz .LBB0_1246
	s_barrier

.LBB0_1405:
	ds_read_b128 v[150:153], v147
	ds_read_b128 v[154:157], v147 offset:1024
	ds_read_b128 v[158:161], v147 offset:2048
	ds_read_b128 v[162:165], v147 offset:3072
	ds_read_b128 v[166:169], v148
	ds_read_b128 v[170:173], v148 offset:1024
	ds_read_b128 v[174:177], v148 offset:2048
	ds_read_b128 v[178:181], v148 offset:3072
	s_add_u32 s22, s20, 0x100
	s_addc_u32 s23, s21, 0
	s_cmp_eq_u32 s61, 2
	s_cselect_b32 s27, s17, s23
	s_cselect_b32 s26, s16, s22
	s_cselect_b32 s25, s19, s60
	s_cselect_b32 s24, s18, s59
	v_lshl_add_u64 v[214:215], s[20:21], 0, v[138:139]
	s_add_i32 m0, s42, 0xc000
	ds_read_b128 v[182:185], v149
	ds_read_b128 v[186:189], v149 offset:1024
	ds_read_b128 v[190:193], v149 offset:2048
	ds_read_b128 v[194:197], v149 offset:3072
	ds_read_b128 v[198:201], v149 offset:4096
	ds_read_b128 v[202:205], v149 offset:5120
	ds_read_b128 v[206:209], v149 offset:6144
	ds_read_b128 v[210:213], v149 offset:7168
	global_load_lds_dwordx4 v[214:215], off
	v_lshl_add_u64 v[214:215], s[20:21], 0, v[136:137]
	s_add_i32 m0, s42, 0xe000
	s_nop 0
	global_load_lds_dwordx4 v[214:215], off
	s_waitcnt vmcnt(8)
	s_waitcnt lgkmcnt(0)
	s_barrier
	s_setprio 0
	s_waitcnt lgkmcnt(0)
	v_mfma_f32_16x16x32_bf16 v[124:127], v[150:153], v[182:185], v[124:127]
	v_mfma_f32_16x16x32_bf16 v[120:123], v[158:161], v[182:185], v[120:123]
	v_mfma_f32_16x16x32_bf16 v[112:115], v[150:153], v[190:193], v[112:115]
	v_mfma_f32_16x16x32_bf16 v[104:107], v[158:161], v[190:193], v[104:107]
	v_mfma_f32_16x16x32_bf16 v[96:99], v[150:153], v[198:201], v[96:99]
	v_mfma_f32_16x16x32_bf16 v[88:91], v[158:161], v[198:201], v[88:91]
	v_mfma_f32_16x16x32_bf16 v[80:83], v[150:153], v[206:209], v[80:83]
	v_mfma_f32_16x16x32_bf16 v[72:75], v[158:161], v[206:209], v[72:75]
	v_mfma_f32_16x16x32_bf16 v[124:127], v[154:157], v[186:189], v[124:127]
	v_mfma_f32_16x16x32_bf16 v[120:123], v[162:165], v[186:189], v[120:123]
	v_mfma_f32_16x16x32_bf16 v[112:115], v[154:157], v[194:197], v[112:115]
	v_mfma_f32_16x16x32_bf16 v[104:107], v[162:165], v[194:197], v[104:107]
	v_mfma_f32_16x16x32_bf16 v[96:99], v[154:157], v[202:205], v[96:99]
	v_mfma_f32_16x16x32_bf16 v[88:91], v[162:165], v[202:205], v[88:91]
	v_mfma_f32_16x16x32_bf16 v[80:83], v[154:157], v[210:213], v[80:83]
	v_mfma_f32_16x16x32_bf16 v[72:75], v[162:165], v[210:213], v[72:75]
	s_setprio 1
	s_setprio 0
	v_mfma_f32_16x16x32_bf16 v[116:119], v[166:169], v[182:185], v[116:119]
	v_mfma_f32_16x16x32_bf16 v[108:111], v[174:177], v[182:185], v[108:111]
	v_mfma_f32_16x16x32_bf16 v[100:103], v[166:169], v[190:193], v[100:103]
	v_mfma_f32_16x16x32_bf16 v[92:95], v[174:177], v[190:193], v[92:95]
	v_mfma_f32_16x16x32_bf16 v[84:87], v[166:169], v[198:201], v[84:87]
	v_mfma_f32_16x16x32_bf16 v[76:79], v[174:177], v[198:201], v[76:79]
	v_mfma_f32_16x16x32_bf16 v[68:71], v[166:169], v[206:209], v[68:71]
	v_mfma_f32_16x16x32_bf16 v[64:67], v[174:177], v[206:209], v[64:67]
	v_mfma_f32_16x16x32_bf16 v[116:119], v[170:173], v[186:189], v[116:119]
	v_mfma_f32_16x16x32_bf16 v[108:111], v[178:181], v[186:189], v[108:111]
	v_mfma_f32_16x16x32_bf16 v[100:103], v[170:173], v[194:197], v[100:103]
	v_mfma_f32_16x16x32_bf16 v[92:95], v[178:181], v[194:197], v[92:95]
	v_mfma_f32_16x16x32_bf16 v[84:87], v[170:173], v[202:205], v[84:87]
	v_mfma_f32_16x16x32_bf16 v[76:79], v[178:181], v[202:205], v[76:79]
	v_mfma_f32_16x16x32_bf16 v[68:71], v[170:173], v[210:213], v[68:71]
	v_mfma_f32_16x16x32_bf16 v[64:67], v[178:181], v[210:213], v[64:67]
	s_setprio 1
	s_barrier
	s_add_i32 s20, s52, s39
	v_lshl_add_u64 v[214:215], s[24:25], 0, v[132:133]
	s_mov_b32 m0, s20
	ds_read_b128 v[182:185], v149 offset:16384
	ds_read_b128 v[186:189], v149 offset:17408
	ds_read_b128 v[190:193], v149 offset:18432
	ds_read_b128 v[194:197], v149 offset:19456
	ds_read_b128 v[198:201], v149 offset:20480
	ds_read_b128 v[202:205], v149 offset:21504
	ds_read_b128 v[206:209], v149 offset:22528
	ds_read_b128 v[210:213], v149 offset:23552
	global_load_lds_dwordx4 v[214:215], off
	s_add_i32 m0, s20, 0x2000
	s_add_u32 s20, s24, 0x1800
	v_lshl_add_u64 v[216:217], s[24:25], 0, v[128:129]
	s_addc_u32 s21, s25, 0
	s_add_i32 s62, s53, s39
	global_load_lds_dwordx4 v[216:217], off
	v_lshl_add_u64 v[218:219], s[20:21], 0, v[132:133]
	s_mov_b32 m0, s62
	v_lshl_add_u64 v[220:221], s[26:27], 0, v[130:131]
	global_load_lds_dwordx4 v[218:219], off
	v_lshl_add_u64 v[218:219], s[20:21], 0, v[128:129]
	s_add_i32 m0, s62, 0x2000
	s_nop 0
	global_load_lds_dwordx4 v[218:219], off
	v_lshl_add_u64 v[218:219], s[26:27], 0, v[134:135]
	s_mov_b32 m0, s42
	s_nop 0
	global_load_lds_dwordx4 v[218:219], off
	s_mov_b32 m0, s43
	s_nop 0
	global_load_lds_dwordx4 v[220:221], off
	s_waitcnt vmcnt(8)
	s_waitcnt lgkmcnt(0)
	s_barrier
	s_setprio 0
	s_waitcnt lgkmcnt(0)
	v_mfma_f32_16x16x32_bf16 v[60:63], v[150:153], v[182:185], v[60:63]
	v_mfma_f32_16x16x32_bf16 v[56:59], v[158:161], v[182:185], v[56:59]
	v_mfma_f32_16x16x32_bf16 v[48:51], v[150:153], v[190:193], v[48:51]
	v_mfma_f32_16x16x32_bf16 v[40:43], v[158:161], v[190:193], v[40:43]
	v_mfma_f32_16x16x32_bf16 v[32:35], v[150:153], v[198:201], v[32:35]
	v_mfma_f32_16x16x32_bf16 v[24:27], v[158:161], v[198:201], v[24:27]
	v_mfma_f32_16x16x32_bf16 v[16:19], v[150:153], v[206:209], v[16:19]
	v_mfma_f32_16x16x32_bf16 v[8:11], v[158:161], v[206:209], v[8:11]
	v_mfma_f32_16x16x32_bf16 v[60:63], v[154:157], v[186:189], v[60:63]
	v_mfma_f32_16x16x32_bf16 v[56:59], v[162:165], v[186:189], v[56:59]
	v_mfma_f32_16x16x32_bf16 v[48:51], v[154:157], v[194:197], v[48:51]
	v_mfma_f32_16x16x32_bf16 v[40:43], v[162:165], v[194:197], v[40:43]
	v_mfma_f32_16x16x32_bf16 v[32:35], v[154:157], v[202:205], v[32:35]
	v_mfma_f32_16x16x32_bf16 v[24:27], v[162:165], v[202:205], v[24:27]
	v_mfma_f32_16x16x32_bf16 v[16:19], v[154:157], v[210:213], v[16:19]
	v_mfma_f32_16x16x32_bf16 v[8:11], v[162:165], v[210:213], v[8:11]
	s_setprio 1
	s_setprio 0
	v_mfma_f32_16x16x32_bf16 v[52:55], v[166:169], v[182:185], v[52:55]
	v_mfma_f32_16x16x32_bf16 v[44:47], v[174:177], v[182:185], v[44:47]
	v_mfma_f32_16x16x32_bf16 v[36:39], v[166:169], v[190:193], v[36:39]
	v_mfma_f32_16x16x32_bf16 v[28:31], v[174:177], v[190:193], v[28:31]
	v_mfma_f32_16x16x32_bf16 v[20:23], v[166:169], v[198:201], v[20:23]
	v_mfma_f32_16x16x32_bf16 v[12:15], v[174:177], v[198:201], v[12:15]
	v_mfma_f32_16x16x32_bf16 v[4:7], v[166:169], v[206:209], v[4:7]
	v_mfma_f32_16x16x32_bf16 v[0:3], v[174:177], v[206:209], v[0:3]
	v_mfma_f32_16x16x32_bf16 v[52:55], v[170:173], v[186:189], v[52:55]
	v_mfma_f32_16x16x32_bf16 v[44:47], v[178:181], v[186:189], v[44:47]
	v_mfma_f32_16x16x32_bf16 v[36:39], v[170:173], v[194:197], v[36:39]
	v_mfma_f32_16x16x32_bf16 v[28:31], v[178:181], v[194:197], v[28:31]
	v_mfma_f32_16x16x32_bf16 v[20:23], v[170:173], v[202:205], v[20:23]
	v_mfma_f32_16x16x32_bf16 v[12:15], v[178:181], v[202:205], v[12:15]
	v_mfma_f32_16x16x32_bf16 v[4:7], v[170:173], v[210:213], v[4:7]
	v_mfma_f32_16x16x32_bf16 v[0:3], v[178:181], v[210:213], v[0:3]
	s_setprio 1
	s_barrier
	s_add_i32 s62, 0, 0x18000
	s_add_i32 s63, 0, 0x1c000
	v_add_u32_e32 v162, s62, v145
	v_add_u32_e32 v178, s63, v145
	ds_read_b128 v[150:153], v162
	ds_read_b128 v[154:157], v162 offset:1024
	ds_read_b128 v[158:161], v162 offset:2048
	ds_read_b128 v[162:165], v162 offset:3072
	ds_read_b128 v[166:169], v178
	ds_read_b128 v[170:173], v178 offset:1024
	ds_read_b128 v[174:177], v178 offset:2048
	ds_read_b128 v[178:181], v178 offset:3072
	s_add_u32 s20, s26, 0x30000
	s_addc_u32 s21, s27, 0
	s_mov_b32 m0, s46
	v_lshl_add_u64 v[222:223], s[20:21], 0, v[134:135]
	ds_read_b128 v[182:185], v149 offset:32768
	ds_read_b128 v[186:189], v149 offset:33792
	ds_read_b128 v[190:193], v149 offset:34816
	ds_read_b128 v[194:197], v149 offset:35840
	ds_read_b128 v[198:201], v149 offset:36864
	ds_read_b128 v[202:205], v149 offset:37888
	ds_read_b128 v[206:209], v149 offset:38912
	ds_read_b128 v[210:213], v149 offset:39936
	global_load_lds_dwordx4 v[222:223], off
	v_lshl_add_u64 v[222:223], s[20:21], 0, v[130:131]
	s_mov_b32 m0, s47
	s_nop 0
	global_load_lds_dwordx4 v[222:223], off
	s_waitcnt vmcnt(8)
	s_waitcnt lgkmcnt(0)
	s_barrier
	s_setprio 0
	s_waitcnt lgkmcnt(0)
	v_mfma_f32_16x16x32_bf16 v[124:127], v[150:153], v[182:185], v[124:127]
	v_mfma_f32_16x16x32_bf16 v[120:123], v[158:161], v[182:185], v[120:123]
	v_mfma_f32_16x16x32_bf16 v[112:115], v[150:153], v[190:193], v[112:115]
	v_mfma_f32_16x16x32_bf16 v[104:107], v[158:161], v[190:193], v[104:107]
	v_mfma_f32_16x16x32_bf16 v[96:99], v[150:153], v[198:201], v[96:99]
	v_mfma_f32_16x16x32_bf16 v[88:91], v[158:161], v[198:201], v[88:91]
	v_mfma_f32_16x16x32_bf16 v[80:83], v[150:153], v[206:209], v[80:83]
	v_mfma_f32_16x16x32_bf16 v[72:75], v[158:161], v[206:209], v[72:75]
	v_mfma_f32_16x16x32_bf16 v[124:127], v[154:157], v[186:189], v[124:127]
	v_mfma_f32_16x16x32_bf16 v[120:123], v[162:165], v[186:189], v[120:123]
	v_mfma_f32_16x16x32_bf16 v[112:115], v[154:157], v[194:197], v[112:115]
	v_mfma_f32_16x16x32_bf16 v[104:107], v[162:165], v[194:197], v[104:107]
	v_mfma_f32_16x16x32_bf16 v[96:99], v[154:157], v[202:205], v[96:99]
	v_mfma_f32_16x16x32_bf16 v[88:91], v[162:165], v[202:205], v[88:91]
	v_mfma_f32_16x16x32_bf16 v[80:83], v[154:157], v[210:213], v[80:83]
	v_mfma_f32_16x16x32_bf16 v[72:75], v[162:165], v[210:213], v[72:75]
	s_setprio 1
	s_setprio 0
	v_mfma_f32_16x16x32_bf16 v[116:119], v[166:169], v[182:185], v[116:119]
	v_mfma_f32_16x16x32_bf16 v[108:111], v[174:177], v[182:185], v[108:111]
	v_mfma_f32_16x16x32_bf16 v[100:103], v[166:169], v[190:193], v[100:103]
	v_mfma_f32_16x16x32_bf16 v[92:95], v[174:177], v[190:193], v[92:95]
	v_mfma_f32_16x16x32_bf16 v[84:87], v[166:169], v[198:201], v[84:87]
	v_mfma_f32_16x16x32_bf16 v[76:79], v[174:177], v[198:201], v[76:79]
	v_mfma_f32_16x16x32_bf16 v[68:71], v[166:169], v[206:209], v[68:71]
	v_mfma_f32_16x16x32_bf16 v[64:67], v[174:177], v[206:209], v[64:67]
	v_mfma_f32_16x16x32_bf16 v[116:119], v[170:173], v[186:189], v[116:119]
	v_mfma_f32_16x16x32_bf16 v[108:111], v[178:181], v[186:189], v[108:111]
	v_mfma_f32_16x16x32_bf16 v[100:103], v[170:173], v[194:197], v[100:103]
	v_mfma_f32_16x16x32_bf16 v[92:95], v[178:181], v[194:197], v[92:95]
	v_mfma_f32_16x16x32_bf16 v[84:87], v[170:173], v[202:205], v[84:87]
	v_mfma_f32_16x16x32_bf16 v[76:79], v[178:181], v[202:205], v[76:79]
	v_mfma_f32_16x16x32_bf16 v[68:71], v[170:173], v[210:213], v[68:71]
	v_mfma_f32_16x16x32_bf16 v[64:67], v[178:181], v[210:213], v[64:67]
	s_setprio 1
	s_barrier
	s_add_i32 s20, s62, s39
	v_lshl_add_u64 v[214:215], v[214:215], 0, s[12:13]
	s_mov_b32 m0, s20
	ds_read_b128 v[182:185], v149 offset:49152
	ds_read_b128 v[186:189], v149 offset:50176
	ds_read_b128 v[190:193], v149 offset:51200
	ds_read_b128 v[194:197], v149 offset:52224
	ds_read_b128 v[198:201], v149 offset:53248
	ds_read_b128 v[202:205], v149 offset:54272
	ds_read_b128 v[206:209], v149 offset:55296
	ds_read_b128 v[210:213], v149 offset:56320
	global_load_lds_dwordx4 v[214:215], off
	s_add_i32 m0, s20, 0x2000
	s_add_u32 s20, s24, 0x1880
	v_lshl_add_u64 v[214:215], v[216:217], 0, s[12:13]
	s_addc_u32 s21, s25, 0
	s_add_i32 s24, s63, s39
	global_load_lds_dwordx4 v[214:215], off
	v_lshl_add_u64 v[214:215], s[20:21], 0, v[132:133]
	s_mov_b32 m0, s24
	s_nop 0
	global_load_lds_dwordx4 v[214:215], off
	v_lshl_add_u64 v[214:215], s[20:21], 0, v[128:129]
	s_add_i32 m0, s24, 0x2000
	s_nop 0
	global_load_lds_dwordx4 v[214:215], off
	v_lshl_add_u64 v[214:215], v[218:219], 0, s[12:13]
	s_mov_b32 m0, s48
	s_nop 0
	global_load_lds_dwordx4 v[214:215], off
	v_lshl_add_u64 v[214:215], v[220:221], 0, s[12:13]
	s_mov_b32 m0, s49
	s_nop 0
	global_load_lds_dwordx4 v[214:215], off
	s_waitcnt vmcnt(8)
	s_waitcnt lgkmcnt(0)
	s_barrier
	s_setprio 0
	s_waitcnt lgkmcnt(0)
	v_mfma_f32_16x16x32_bf16 v[60:63], v[150:153], v[182:185], v[60:63]
	v_mfma_f32_16x16x32_bf16 v[56:59], v[158:161], v[182:185], v[56:59]
	v_mfma_f32_16x16x32_bf16 v[48:51], v[150:153], v[190:193], v[48:51]
	v_mfma_f32_16x16x32_bf16 v[40:43], v[158:161], v[190:193], v[40:43]
	v_mfma_f32_16x16x32_bf16 v[32:35], v[150:153], v[198:201], v[32:35]
	v_mfma_f32_16x16x32_bf16 v[24:27], v[158:161], v[198:201], v[24:27]
	v_mfma_f32_16x16x32_bf16 v[16:19], v[150:153], v[206:209], v[16:19]
	v_mfma_f32_16x16x32_bf16 v[8:11], v[158:161], v[206:209], v[8:11]
	v_mfma_f32_16x16x32_bf16 v[60:63], v[154:157], v[186:189], v[60:63]
	v_mfma_f32_16x16x32_bf16 v[56:59], v[162:165], v[186:189], v[56:59]
	v_mfma_f32_16x16x32_bf16 v[48:51], v[154:157], v[194:197], v[48:51]
	v_mfma_f32_16x16x32_bf16 v[40:43], v[162:165], v[194:197], v[40:43]
	v_mfma_f32_16x16x32_bf16 v[32:35], v[154:157], v[202:205], v[32:35]
	v_mfma_f32_16x16x32_bf16 v[24:27], v[162:165], v[202:205], v[24:27]
	v_mfma_f32_16x16x32_bf16 v[16:19], v[154:157], v[210:213], v[16:19]
	v_mfma_f32_16x16x32_bf16 v[8:11], v[162:165], v[210:213], v[8:11]
	s_setprio 1
	s_setprio 0
	v_mfma_f32_16x16x32_bf16 v[52:55], v[166:169], v[182:185], v[52:55]
	v_mfma_f32_16x16x32_bf16 v[44:47], v[174:177], v[182:185], v[44:47]
	v_mfma_f32_16x16x32_bf16 v[36:39], v[166:169], v[190:193], v[36:39]
	v_mfma_f32_16x16x32_bf16 v[28:31], v[174:177], v[190:193], v[28:31]
	v_mfma_f32_16x16x32_bf16 v[20:23], v[166:169], v[198:201], v[20:23]
	v_mfma_f32_16x16x32_bf16 v[12:15], v[174:177], v[198:201], v[12:15]
	v_mfma_f32_16x16x32_bf16 v[4:7], v[166:169], v[206:209], v[4:7]
	v_mfma_f32_16x16x32_bf16 v[0:3], v[174:177], v[206:209], v[0:3]
	v_mfma_f32_16x16x32_bf16 v[52:55], v[170:173], v[186:189], v[52:55]
	v_mfma_f32_16x16x32_bf16 v[44:47], v[178:181], v[186:189], v[44:47]
	v_mfma_f32_16x16x32_bf16 v[36:39], v[170:173], v[194:197], v[36:39]
	v_mfma_f32_16x16x32_bf16 v[28:31], v[178:181], v[194:197], v[28:31]
	v_mfma_f32_16x16x32_bf16 v[20:23], v[170:173], v[202:205], v[20:23]
	v_mfma_f32_16x16x32_bf16 v[12:15], v[178:181], v[202:205], v[12:15]
	v_mfma_f32_16x16x32_bf16 v[4:7], v[170:173], v[210:213], v[4:7]
	v_mfma_f32_16x16x32_bf16 v[0:3], v[178:181], v[210:213], v[0:3]
	s_setprio 1
	s_barrier
	s_add_i32 s61, s61, 2
	s_add_u32 s59, s59, 0x100
	s_addc_u32 s60, s60, 0
	s_cmp_gt_u32 s61, 3
	s_mov_b64 s[20:21], s[22:23]
	s_cbranch_scc0 .LBB0_1405
	s_and_b64 vcc, exec, s[14:15]
	s_cbranch_vccz .LBB0_1408
	s_barrier

.LBB0_1429:
	s_add_u32 s40, s22, s17
	s_addc_u32 s41, s23, 0
	s_add_u32 s36, s40, 0x100
	s_addc_u32 s37, s41, 0
	s_and_b64 s[30:31], s[28:29], exec
	s_cselect_b32 s37, s19, s37
	s_cselect_b32 s36, s18, s36
	s_add_u32 s17, s24, s17
	s_addc_u32 s30, s25, 0
	s_add_u32 s17, s17, 0x100
	s_addc_u32 s30, s30, 0
	s_and_b64 s[28:29], s[28:29], exec
	s_cselect_b32 s39, s21, s30
	s_cselect_b32 s38, s20, s17
	s_add_u32 s42, s40, 0x30080
	ds_read_b128 v[146:149], v143
	ds_read_b128 v[150:153], v143 offset:1024
	ds_read_b128 v[154:157], v143 offset:2048
	ds_read_b128 v[158:161], v143 offset:3072
	ds_read_b128 v[162:165], v144
	ds_read_b128 v[166:169], v144 offset:1024
	ds_read_b128 v[170:173], v144 offset:2048
	ds_read_b128 v[174:177], v144 offset:3072
	s_addc_u32 s43, s41, 0
	s_add_i32 s76, s62, s53
	s_add_i32 m0, s54, 0xc000
	s_add_i32 s79, s54, 0xe000
	s_add_i32 s73, s76, 0x2000
	s_add_u32 s40, s38, 0x1000
	s_addc_u32 s41, s39, 0
	s_add_i32 s75, s63, s53
	s_add_i32 s74, s75, 0x2000
	s_add_i32 s72, 0, 0x18000
	s_add_i32 s71, 0, 0x1c000
	s_add_u32 s30, s36, 0x30000
	s_addc_u32 s31, s37, 0
	s_add_i32 s70, s72, s53
	s_add_i32 s17, s70, 0x2000
	s_add_u32 s28, s38, 0x1080
	s_addc_u32 s29, s39, 0
	s_add_i32 s78, s71, s53
	s_add_i32 s77, s78, 0x2000
	v_lshl_add_u64 v[210:211], s[42:43], 0, v[128:129]
	ds_read_b128 v[178:181], v145
	ds_read_b128 v[182:185], v145 offset:1024
	ds_read_b128 v[186:189], v145 offset:2048
	ds_read_b128 v[190:193], v145 offset:3072
	ds_read_b128 v[194:197], v145 offset:4096
	ds_read_b128 v[198:201], v145 offset:5120
	ds_read_b128 v[202:205], v145 offset:6144
	ds_read_b128 v[206:209], v145 offset:7168
	global_load_lds_dwordx4 v[210:211], off
	v_lshl_add_u64 v[210:211], s[42:43], 0, v[132:133]
	s_mov_b32 m0, s79
	s_nop 0
	global_load_lds_dwordx4 v[210:211], off
	s_waitcnt vmcnt(8)
	s_waitcnt lgkmcnt(0)
	s_barrier
	s_setprio 0
	s_waitcnt lgkmcnt(0)
	v_mfma_f32_16x16x32_bf16 v[124:127], v[146:149], v[178:181], v[124:127]
	v_mfma_f32_16x16x32_bf16 v[120:123], v[154:157], v[178:181], v[120:123]
	v_mfma_f32_16x16x32_bf16 v[108:111], v[146:149], v[186:189], v[108:111]
	v_mfma_f32_16x16x32_bf16 v[104:107], v[154:157], v[186:189], v[104:107]
	v_mfma_f32_16x16x32_bf16 v[92:95], v[146:149], v[194:197], v[92:95]
	v_mfma_f32_16x16x32_bf16 v[88:91], v[154:157], v[194:197], v[88:91]
	v_mfma_f32_16x16x32_bf16 v[76:79], v[146:149], v[202:205], v[76:79]
	v_mfma_f32_16x16x32_bf16 v[72:75], v[154:157], v[202:205], v[72:75]
	v_mfma_f32_16x16x32_bf16 v[124:127], v[150:153], v[182:185], v[124:127]
	v_mfma_f32_16x16x32_bf16 v[120:123], v[158:161], v[182:185], v[120:123]
	v_mfma_f32_16x16x32_bf16 v[108:111], v[150:153], v[190:193], v[108:111]
	v_mfma_f32_16x16x32_bf16 v[104:107], v[158:161], v[190:193], v[104:107]
	v_mfma_f32_16x16x32_bf16 v[92:95], v[150:153], v[198:201], v[92:95]
	v_mfma_f32_16x16x32_bf16 v[88:91], v[158:161], v[198:201], v[88:91]
	v_mfma_f32_16x16x32_bf16 v[76:79], v[150:153], v[206:209], v[76:79]
	v_mfma_f32_16x16x32_bf16 v[72:75], v[158:161], v[206:209], v[72:75]
	s_setprio 1
	s_setprio 0
	v_mfma_f32_16x16x32_bf16 v[116:119], v[162:165], v[178:181], v[116:119]
	v_mfma_f32_16x16x32_bf16 v[112:115], v[170:173], v[178:181], v[112:115]
	v_mfma_f32_16x16x32_bf16 v[100:103], v[162:165], v[186:189], v[100:103]
	v_mfma_f32_16x16x32_bf16 v[96:99], v[170:173], v[186:189], v[96:99]
	v_mfma_f32_16x16x32_bf16 v[84:87], v[162:165], v[194:197], v[84:87]
	v_mfma_f32_16x16x32_bf16 v[80:83], v[170:173], v[194:197], v[80:83]
	v_mfma_f32_16x16x32_bf16 v[68:71], v[162:165], v[202:205], v[68:71]
	v_mfma_f32_16x16x32_bf16 v[64:67], v[170:173], v[202:205], v[64:67]
	v_mfma_f32_16x16x32_bf16 v[116:119], v[166:169], v[182:185], v[116:119]
	v_mfma_f32_16x16x32_bf16 v[112:115], v[174:177], v[182:185], v[112:115]
	v_mfma_f32_16x16x32_bf16 v[100:103], v[166:169], v[190:193], v[100:103]
	v_mfma_f32_16x16x32_bf16 v[96:99], v[174:177], v[190:193], v[96:99]
	v_mfma_f32_16x16x32_bf16 v[84:87], v[166:169], v[198:201], v[84:87]
	v_mfma_f32_16x16x32_bf16 v[80:83], v[174:177], v[198:201], v[80:83]
	v_mfma_f32_16x16x32_bf16 v[68:71], v[166:169], v[206:209], v[68:71]
	v_mfma_f32_16x16x32_bf16 v[64:67], v[174:177], v[206:209], v[64:67]
	s_setprio 1
	s_barrier
	s_mov_b32 m0, s76
	v_lshl_add_u64 v[210:211], s[38:39], 0, v[130:131]
	ds_read_b128 v[178:181], v145 offset:16384
	ds_read_b128 v[182:185], v145 offset:17408
	ds_read_b128 v[186:189], v145 offset:18432
	ds_read_b128 v[190:193], v145 offset:19456
	ds_read_b128 v[194:197], v145 offset:20480
	ds_read_b128 v[198:201], v145 offset:21504
	ds_read_b128 v[202:205], v145 offset:22528
	ds_read_b128 v[206:209], v145 offset:23552
	global_load_lds_dwordx4 v[210:211], off
	v_lshl_add_u64 v[212:213], s[38:39], 0, v[134:135]
	s_mov_b32 m0, s73
	v_lshl_add_u64 v[214:215], s[40:41], 0, v[130:131]
	global_load_lds_dwordx4 v[212:213], off
	s_mov_b32 m0, s75
	v_lshl_add_u64 v[216:217], s[36:37], 0, v[132:133]
	global_load_lds_dwordx4 v[214:215], off
	v_lshl_add_u64 v[214:215], s[40:41], 0, v[134:135]
	s_mov_b32 m0, s74
	s_nop 0
	global_load_lds_dwordx4 v[214:215], off
	v_lshl_add_u64 v[214:215], s[36:37], 0, v[128:129]
	s_mov_b32 m0, s54
	s_nop 0
	global_load_lds_dwordx4 v[214:215], off
	s_mov_b32 m0, s55
	s_nop 0
	global_load_lds_dwordx4 v[216:217], off
	s_waitcnt vmcnt(8)
	s_waitcnt lgkmcnt(0)
	s_barrier
	s_setprio 0
	s_waitcnt lgkmcnt(0)
	v_mfma_f32_16x16x32_bf16 v[60:63], v[146:149], v[178:181], v[60:63]
	v_mfma_f32_16x16x32_bf16 v[56:59], v[154:157], v[178:181], v[56:59]
	v_mfma_f32_16x16x32_bf16 v[48:51], v[146:149], v[186:189], v[48:51]
	v_mfma_f32_16x16x32_bf16 v[40:43], v[154:157], v[186:189], v[40:43]
	v_mfma_f32_16x16x32_bf16 v[32:35], v[146:149], v[194:197], v[32:35]
	v_mfma_f32_16x16x32_bf16 v[24:27], v[154:157], v[194:197], v[24:27]
	v_mfma_f32_16x16x32_bf16 v[16:19], v[146:149], v[202:205], v[16:19]
	v_mfma_f32_16x16x32_bf16 v[8:11], v[154:157], v[202:205], v[8:11]
	v_mfma_f32_16x16x32_bf16 v[60:63], v[150:153], v[182:185], v[60:63]
	v_mfma_f32_16x16x32_bf16 v[56:59], v[158:161], v[182:185], v[56:59]
	v_mfma_f32_16x16x32_bf16 v[48:51], v[150:153], v[190:193], v[48:51]
	v_mfma_f32_16x16x32_bf16 v[40:43], v[158:161], v[190:193], v[40:43]
	v_mfma_f32_16x16x32_bf16 v[32:35], v[150:153], v[198:201], v[32:35]
	v_mfma_f32_16x16x32_bf16 v[24:27], v[158:161], v[198:201], v[24:27]
	v_mfma_f32_16x16x32_bf16 v[16:19], v[150:153], v[206:209], v[16:19]
	v_mfma_f32_16x16x32_bf16 v[8:11], v[158:161], v[206:209], v[8:11]
	s_setprio 1
	s_setprio 0
	v_mfma_f32_16x16x32_bf16 v[52:55], v[162:165], v[178:181], v[52:55]
	v_mfma_f32_16x16x32_bf16 v[44:47], v[170:173], v[178:181], v[44:47]
	v_mfma_f32_16x16x32_bf16 v[36:39], v[162:165], v[186:189], v[36:39]
	v_mfma_f32_16x16x32_bf16 v[28:31], v[170:173], v[186:189], v[28:31]
	v_mfma_f32_16x16x32_bf16 v[20:23], v[162:165], v[194:197], v[20:23]
	v_mfma_f32_16x16x32_bf16 v[12:15], v[170:173], v[194:197], v[12:15]
	v_mfma_f32_16x16x32_bf16 v[4:7], v[162:165], v[202:205], v[4:7]
	v_mfma_f32_16x16x32_bf16 v[0:3], v[170:173], v[202:205], v[0:3]
	v_mfma_f32_16x16x32_bf16 v[52:55], v[166:169], v[182:185], v[52:55]
	v_mfma_f32_16x16x32_bf16 v[44:47], v[174:177], v[182:185], v[44:47]
	v_mfma_f32_16x16x32_bf16 v[36:39], v[166:169], v[190:193], v[36:39]
	v_mfma_f32_16x16x32_bf16 v[28:31], v[174:177], v[190:193], v[28:31]
	v_mfma_f32_16x16x32_bf16 v[20:23], v[166:169], v[198:201], v[20:23]
	v_mfma_f32_16x16x32_bf16 v[12:15], v[174:177], v[198:201], v[12:15]
	v_mfma_f32_16x16x32_bf16 v[4:7], v[166:169], v[206:209], v[4:7]
	v_mfma_f32_16x16x32_bf16 v[0:3], v[174:177], v[206:209], v[0:3]
	s_setprio 1
	s_barrier
	v_add_u32_e32 v158, s72, v141
	v_add_u32_e32 v174, s71, v141
	ds_read_b128 v[146:149], v158
	ds_read_b128 v[150:153], v158 offset:1024
	ds_read_b128 v[154:157], v158 offset:2048
	ds_read_b128 v[158:161], v158 offset:3072
	ds_read_b128 v[162:165], v174
	ds_read_b128 v[166:169], v174 offset:1024
	ds_read_b128 v[170:173], v174 offset:2048
	ds_read_b128 v[174:177], v174 offset:3072
	s_mov_b32 m0, s56
	v_lshl_add_u64 v[218:219], s[30:31], 0, v[128:129]
	ds_read_b128 v[178:181], v145 offset:32768
	ds_read_b128 v[182:185], v145 offset:33792
	ds_read_b128 v[186:189], v145 offset:34816
	ds_read_b128 v[190:193], v145 offset:35840
	ds_read_b128 v[194:197], v145 offset:36864
	ds_read_b128 v[198:201], v145 offset:37888
	ds_read_b128 v[202:205], v145 offset:38912
	ds_read_b128 v[206:209], v145 offset:39936
	global_load_lds_dwordx4 v[218:219], off
	v_lshl_add_u64 v[218:219], s[30:31], 0, v[132:133]
	s_mov_b32 m0, s57
	s_nop 0
	global_load_lds_dwordx4 v[218:219], off
	s_waitcnt vmcnt(8)
	s_waitcnt lgkmcnt(0)
	s_barrier
	s_setprio 0
	s_waitcnt lgkmcnt(0)
	v_mfma_f32_16x16x32_bf16 v[124:127], v[146:149], v[178:181], v[124:127]
	v_mfma_f32_16x16x32_bf16 v[120:123], v[154:157], v[178:181], v[120:123]
	v_mfma_f32_16x16x32_bf16 v[108:111], v[146:149], v[186:189], v[108:111]
	v_mfma_f32_16x16x32_bf16 v[104:107], v[154:157], v[186:189], v[104:107]
	v_mfma_f32_16x16x32_bf16 v[92:95], v[146:149], v[194:197], v[92:95]
	v_mfma_f32_16x16x32_bf16 v[88:91], v[154:157], v[194:197], v[88:91]
	v_mfma_f32_16x16x32_bf16 v[76:79], v[146:149], v[202:205], v[76:79]
	v_mfma_f32_16x16x32_bf16 v[72:75], v[154:157], v[202:205], v[72:75]
	v_mfma_f32_16x16x32_bf16 v[124:127], v[150:153], v[182:185], v[124:127]
	v_mfma_f32_16x16x32_bf16 v[120:123], v[158:161], v[182:185], v[120:123]
	v_mfma_f32_16x16x32_bf16 v[108:111], v[150:153], v[190:193], v[108:111]
	v_mfma_f32_16x16x32_bf16 v[104:107], v[158:161], v[190:193], v[104:107]
	v_mfma_f32_16x16x32_bf16 v[92:95], v[150:153], v[198:201], v[92:95]
	v_mfma_f32_16x16x32_bf16 v[88:91], v[158:161], v[198:201], v[88:91]
	v_mfma_f32_16x16x32_bf16 v[76:79], v[150:153], v[206:209], v[76:79]
	v_mfma_f32_16x16x32_bf16 v[72:75], v[158:161], v[206:209], v[72:75]
	s_setprio 1
	s_setprio 0
	v_mfma_f32_16x16x32_bf16 v[116:119], v[162:165], v[178:181], v[116:119]
	v_mfma_f32_16x16x32_bf16 v[112:115], v[170:173], v[178:181], v[112:115]
	v_mfma_f32_16x16x32_bf16 v[100:103], v[162:165], v[186:189], v[100:103]
	v_mfma_f32_16x16x32_bf16 v[96:99], v[170:173], v[186:189], v[96:99]
	v_mfma_f32_16x16x32_bf16 v[84:87], v[162:165], v[194:197], v[84:87]
	v_mfma_f32_16x16x32_bf16 v[80:83], v[170:173], v[194:197], v[80:83]
	v_mfma_f32_16x16x32_bf16 v[68:71], v[162:165], v[202:205], v[68:71]
	v_mfma_f32_16x16x32_bf16 v[64:67], v[170:173], v[202:205], v[64:67]
	v_mfma_f32_16x16x32_bf16 v[116:119], v[166:169], v[182:185], v[116:119]
	v_mfma_f32_16x16x32_bf16 v[112:115], v[174:177], v[182:185], v[112:115]
	v_mfma_f32_16x16x32_bf16 v[100:103], v[166:169], v[190:193], v[100:103]
	v_mfma_f32_16x16x32_bf16 v[96:99], v[174:177], v[190:193], v[96:99]
	v_mfma_f32_16x16x32_bf16 v[84:87], v[166:169], v[198:201], v[84:87]
	v_mfma_f32_16x16x32_bf16 v[80:83], v[174:177], v[198:201], v[80:83]
	v_mfma_f32_16x16x32_bf16 v[68:71], v[166:169], v[206:209], v[68:71]
	v_mfma_f32_16x16x32_bf16 v[64:67], v[174:177], v[206:209], v[64:67]
	s_setprio 1
	s_barrier
	s_mov_b32 m0, s70
	v_lshl_add_u64 v[210:211], v[210:211], 0, s[12:13]
	ds_read_b128 v[178:181], v145 offset:49152
	ds_read_b128 v[182:185], v145 offset:50176
	ds_read_b128 v[186:189], v145 offset:51200
	ds_read_b128 v[190:193], v145 offset:52224
	ds_read_b128 v[194:197], v145 offset:53248
	ds_read_b128 v[198:201], v145 offset:54272
	ds_read_b128 v[202:205], v145 offset:55296
	ds_read_b128 v[206:209], v145 offset:56320
	global_load_lds_dwordx4 v[210:211], off
	v_lshl_add_u64 v[210:211], v[212:213], 0, s[12:13]
	s_mov_b32 m0, s17
	s_nop 0
	global_load_lds_dwordx4 v[210:211], off
	v_lshl_add_u64 v[210:211], s[28:29], 0, v[130:131]
	s_mov_b32 m0, s78
	s_nop 0
	global_load_lds_dwordx4 v[210:211], off
	v_lshl_add_u64 v[210:211], s[28:29], 0, v[134:135]
	s_mov_b32 m0, s77
	s_nop 0
	global_load_lds_dwordx4 v[210:211], off
	v_lshl_add_u64 v[210:211], v[214:215], 0, s[12:13]
	s_mov_b32 m0, s59
	s_nop 0
	global_load_lds_dwordx4 v[210:211], off
	v_lshl_add_u64 v[210:211], v[216:217], 0, s[12:13]
	s_mov_b32 m0, s60
	s_nop 0
	global_load_lds_dwordx4 v[210:211], off
	s_waitcnt vmcnt(8)
	s_waitcnt lgkmcnt(0)
	s_barrier
	s_setprio 0
	s_waitcnt lgkmcnt(0)
	v_mfma_f32_16x16x32_bf16 v[60:63], v[146:149], v[178:181], v[60:63]
	v_mfma_f32_16x16x32_bf16 v[56:59], v[154:157], v[178:181], v[56:59]
	v_mfma_f32_16x16x32_bf16 v[48:51], v[146:149], v[186:189], v[48:51]
	v_mfma_f32_16x16x32_bf16 v[40:43], v[154:157], v[186:189], v[40:43]
	v_mfma_f32_16x16x32_bf16 v[32:35], v[146:149], v[194:197], v[32:35]
	v_mfma_f32_16x16x32_bf16 v[24:27], v[154:157], v[194:197], v[24:27]
	v_mfma_f32_16x16x32_bf16 v[16:19], v[146:149], v[202:205], v[16:19]
	v_mfma_f32_16x16x32_bf16 v[8:11], v[154:157], v[202:205], v[8:11]
	v_mfma_f32_16x16x32_bf16 v[60:63], v[150:153], v[182:185], v[60:63]
	v_mfma_f32_16x16x32_bf16 v[56:59], v[158:161], v[182:185], v[56:59]
	v_mfma_f32_16x16x32_bf16 v[48:51], v[150:153], v[190:193], v[48:51]
	v_mfma_f32_16x16x32_bf16 v[40:43], v[158:161], v[190:193], v[40:43]
	v_mfma_f32_16x16x32_bf16 v[32:35], v[150:153], v[198:201], v[32:35]
	v_mfma_f32_16x16x32_bf16 v[24:27], v[158:161], v[198:201], v[24:27]
	v_mfma_f32_16x16x32_bf16 v[16:19], v[150:153], v[206:209], v[16:19]
	v_mfma_f32_16x16x32_bf16 v[8:11], v[158:161], v[206:209], v[8:11]
	s_setprio 1
	s_setprio 0
	v_mfma_f32_16x16x32_bf16 v[52:55], v[162:165], v[178:181], v[52:55]
	v_mfma_f32_16x16x32_bf16 v[44:47], v[170:173], v[178:181], v[44:47]
	v_mfma_f32_16x16x32_bf16 v[36:39], v[162:165], v[186:189], v[36:39]
	v_mfma_f32_16x16x32_bf16 v[28:31], v[170:173], v[186:189], v[28:31]
	v_mfma_f32_16x16x32_bf16 v[20:23], v[162:165], v[194:197], v[20:23]
	v_mfma_f32_16x16x32_bf16 v[12:15], v[170:173], v[194:197], v[12:15]
	v_mfma_f32_16x16x32_bf16 v[4:7], v[162:165], v[202:205], v[4:7]
	v_mfma_f32_16x16x32_bf16 v[0:3], v[170:173], v[202:205], v[0:3]
	v_mfma_f32_16x16x32_bf16 v[52:55], v[166:169], v[182:185], v[52:55]
	v_mfma_f32_16x16x32_bf16 v[44:47], v[174:177], v[182:185], v[44:47]
	v_mfma_f32_16x16x32_bf16 v[36:39], v[166:169], v[190:193], v[36:39]
	v_mfma_f32_16x16x32_bf16 v[28:31], v[174:177], v[190:193], v[28:31]
	v_mfma_f32_16x16x32_bf16 v[20:23], v[166:169], v[198:201], v[20:23]
	v_mfma_f32_16x16x32_bf16 v[12:15], v[174:177], v[198:201], v[12:15]
	v_mfma_f32_16x16x32_bf16 v[4:7], v[166:169], v[206:209], v[4:7]
	v_mfma_f32_16x16x32_bf16 v[0:3], v[174:177], v[206:209], v[0:3]
	s_setprio 1
	s_barrier
	s_movk_i32 s17, 0x100
	s_andn2_b64 vcc, exec, s[26:27]
	s_mov_b64 s[28:29], -1
	s_mov_b64 s[26:27], 0
	s_cbranch_vccz .LBB0_1429
	s_and_b64 vcc, exec, s[14:15]
	s_cbranch_vccz .LBB0_1432
	s_barrier

.LBB0_4355:
	ds_read_b128 v[160:163], v152
	ds_read_b128 v[164:167], v152 offset:1024
	ds_read_b128 v[168:171], v152 offset:2048
	ds_read_b128 v[172:175], v152 offset:3072
	ds_read_b128 v[176:179], v153
	ds_read_b128 v[180:183], v153 offset:1024
	ds_read_b128 v[184:187], v153 offset:2048
	ds_read_b128 v[188:191], v153 offset:3072
	s_add_u32 s38, s30, s36
	s_addc_u32 s39, s31, s37
	s_add_u32 s40, s38, 0x100
	s_addc_u32 s41, s39, 0
	s_add_u32 s67, s23, s36
	s_addc_u32 s68, s65, s37
	s_cmpk_eq_i32 s36, 0x700
	s_cselect_b64 vcc, -1, 0
	s_and_b64 s[38:39], vcc, exec
	v_cndmask_b32_e32 v132, v138, v157, vcc
	s_cselect_b32 s41, s27, s41
	s_cselect_b32 s40, s26, s40
	v_cndmask_b32_e32 v224, v136, v156, vcc
	v_cndmask_b32_e32 v135, v134, v155, vcc
	v_cndmask_b32_e32 v141, v140, v158, vcc
	s_cselect_b32 s39, s25, s68
	s_cselect_b32 s38, s24, s67
	s_mov_b32 m0, s59
	v_lshl_add_u64 v[226:227], v[144:145], 0, s[36:37]
	ds_read_b128 v[192:195], v154
	ds_read_b128 v[196:199], v154 offset:1024
	ds_read_b128 v[200:203], v154 offset:2048
	ds_read_b128 v[204:207], v154 offset:3072
	ds_read_b128 v[208:211], v154 offset:4096
	ds_read_b128 v[212:215], v154 offset:5120
	ds_read_b128 v[216:219], v154 offset:6144
	ds_read_b128 v[220:223], v154 offset:7168
	global_load_lds_dwordx4 v[226:227], off
	v_lshl_add_u64 v[226:227], v[142:143], 0, s[36:37]
	s_add_i32 m0, s49, 0xe000
	s_nop 0
	global_load_lds_dwordx4 v[226:227], off
	s_waitcnt vmcnt(8)
	s_waitcnt lgkmcnt(0)
	s_barrier
	s_setprio 0
	s_waitcnt lgkmcnt(0)
	v_mfma_f32_16x16x32_bf16 v[116:119], v[160:163], v[192:195], v[116:119]
	v_mfma_f32_16x16x32_bf16 v[112:115], v[168:171], v[192:195], v[112:115]
	v_mfma_f32_16x16x32_bf16 v[108:111], v[160:163], v[200:203], v[108:111]
	v_mfma_f32_16x16x32_bf16 v[104:107], v[168:171], v[200:203], v[104:107]
	v_mfma_f32_16x16x32_bf16 v[92:95], v[160:163], v[208:211], v[92:95]
	v_mfma_f32_16x16x32_bf16 v[88:91], v[168:171], v[208:211], v[88:91]
	v_mfma_f32_16x16x32_bf16 v[76:79], v[160:163], v[216:219], v[76:79]
	v_mfma_f32_16x16x32_bf16 v[72:75], v[168:171], v[216:219], v[72:75]
	v_mfma_f32_16x16x32_bf16 v[116:119], v[164:167], v[196:199], v[116:119]
	v_mfma_f32_16x16x32_bf16 v[112:115], v[172:175], v[196:199], v[112:115]
	v_mfma_f32_16x16x32_bf16 v[108:111], v[164:167], v[204:207], v[108:111]
	v_mfma_f32_16x16x32_bf16 v[104:107], v[172:175], v[204:207], v[104:107]
	v_mfma_f32_16x16x32_bf16 v[92:95], v[164:167], v[212:215], v[92:95]
	v_mfma_f32_16x16x32_bf16 v[88:91], v[172:175], v[212:215], v[88:91]
	v_mfma_f32_16x16x32_bf16 v[76:79], v[164:167], v[220:223], v[76:79]
	v_mfma_f32_16x16x32_bf16 v[72:75], v[172:175], v[220:223], v[72:75]
	s_setprio 1
	s_setprio 0
	v_mfma_f32_16x16x32_bf16 v[124:127], v[176:179], v[192:195], v[124:127]
	v_mfma_f32_16x16x32_bf16 v[120:123], v[184:187], v[192:195], v[120:123]
	v_mfma_f32_16x16x32_bf16 v[100:103], v[176:179], v[200:203], v[100:103]
	v_mfma_f32_16x16x32_bf16 v[96:99], v[184:187], v[200:203], v[96:99]
	v_mfma_f32_16x16x32_bf16 v[84:87], v[176:179], v[208:211], v[84:87]
	v_mfma_f32_16x16x32_bf16 v[80:83], v[184:187], v[208:211], v[80:83]
	v_mfma_f32_16x16x32_bf16 v[68:71], v[176:179], v[216:219], v[68:71]
	v_mfma_f32_16x16x32_bf16 v[64:67], v[184:187], v[216:219], v[64:67]
	v_mfma_f32_16x16x32_bf16 v[124:127], v[180:183], v[196:199], v[124:127]
	v_mfma_f32_16x16x32_bf16 v[120:123], v[188:191], v[196:199], v[120:123]
	v_mfma_f32_16x16x32_bf16 v[100:103], v[180:183], v[204:207], v[100:103]
	v_mfma_f32_16x16x32_bf16 v[96:99], v[188:191], v[204:207], v[96:99]
	v_mfma_f32_16x16x32_bf16 v[84:87], v[180:183], v[212:215], v[84:87]
	v_mfma_f32_16x16x32_bf16 v[80:83], v[188:191], v[212:215], v[80:83]
	v_mfma_f32_16x16x32_bf16 v[68:71], v[180:183], v[220:223], v[68:71]
	v_mfma_f32_16x16x32_bf16 v[64:67], v[188:191], v[220:223], v[64:67]
	s_setprio 1
	s_barrier
	s_add_i32 s67, s56, s29
	v_lshl_add_u64 v[226:227], s[38:39], 0, v[128:129]
	s_mov_b32 m0, s67
	ds_read_b128 v[192:195], v154 offset:16384
	ds_read_b128 v[196:199], v154 offset:17408
	ds_read_b128 v[200:203], v154 offset:18432
	ds_read_b128 v[204:207], v154 offset:19456
	ds_read_b128 v[208:211], v154 offset:20480
	ds_read_b128 v[212:215], v154 offset:21504
	ds_read_b128 v[216:219], v154 offset:22528
	ds_read_b128 v[220:223], v154 offset:23552
	global_load_lds_dwordx4 v[226:227], off
	s_add_i32 m0, s67, 0x2000
	s_add_u32 s68, s38, 0x40000
	v_lshl_add_u64 v[228:229], s[38:39], 0, v[130:131]
	s_addc_u32 s69, s39, 0
	s_add_i32 s67, s57, s29
	global_load_lds_dwordx4 v[228:229], off
	v_lshl_add_u64 v[230:231], s[68:69], 0, v[128:129]
	s_mov_b32 m0, s67
	v_mov_b32_e32 v225, v133
	global_load_lds_dwordx4 v[230:231], off
	v_lshl_add_u64 v[230:231], s[68:69], 0, v[130:131]
	s_add_i32 m0, s67, 0x2000
	s_nop 0
	global_load_lds_dwordx4 v[230:231], off
	s_mov_b32 m0, s49
	v_lshl_add_u64 v[230:231], s[40:41], 0, v[132:133]
	global_load_lds_dwordx4 v132, s[40:41]
	s_mov_b32 m0, s50
	s_nop 0
	global_load_lds_dwordx4 v224, s[40:41]
	s_waitcnt vmcnt(8)
	s_waitcnt lgkmcnt(0)
	v_lshl_add_u64 v[224:225], s[40:41], 0, v[224:225]
	s_barrier
	s_setprio 0
	s_waitcnt lgkmcnt(0)
	v_mfma_f32_16x16x32_bf16 v[60:63], v[160:163], v[192:195], v[60:63]
	v_mfma_f32_16x16x32_bf16 v[56:59], v[168:171], v[192:195], v[56:59]
	v_mfma_f32_16x16x32_bf16 v[44:47], v[160:163], v[200:203], v[44:47]
	v_mfma_f32_16x16x32_bf16 v[40:43], v[168:171], v[200:203], v[40:43]
	v_mfma_f32_16x16x32_bf16 v[28:31], v[160:163], v[208:211], v[28:31]
	v_mfma_f32_16x16x32_bf16 v[24:27], v[168:171], v[208:211], v[24:27]
	v_mfma_f32_16x16x32_bf16 v[12:15], v[160:163], v[216:219], v[12:15]
	v_mfma_f32_16x16x32_bf16 v[8:11], v[168:171], v[216:219], v[8:11]
	v_mfma_f32_16x16x32_bf16 v[60:63], v[164:167], v[196:199], v[60:63]
	v_mfma_f32_16x16x32_bf16 v[56:59], v[172:175], v[196:199], v[56:59]
	v_mfma_f32_16x16x32_bf16 v[44:47], v[164:167], v[204:207], v[44:47]
	v_mfma_f32_16x16x32_bf16 v[40:43], v[172:175], v[204:207], v[40:43]
	v_mfma_f32_16x16x32_bf16 v[28:31], v[164:167], v[212:215], v[28:31]
	v_mfma_f32_16x16x32_bf16 v[24:27], v[172:175], v[212:215], v[24:27]
	v_mfma_f32_16x16x32_bf16 v[12:15], v[164:167], v[220:223], v[12:15]
	v_mfma_f32_16x16x32_bf16 v[8:11], v[172:175], v[220:223], v[8:11]
	s_setprio 1
	s_setprio 0
	v_mfma_f32_16x16x32_bf16 v[52:55], v[176:179], v[192:195], v[52:55]
	v_mfma_f32_16x16x32_bf16 v[48:51], v[184:187], v[192:195], v[48:51]
	v_mfma_f32_16x16x32_bf16 v[36:39], v[176:179], v[200:203], v[36:39]
	v_mfma_f32_16x16x32_bf16 v[32:35], v[184:187], v[200:203], v[32:35]
	v_mfma_f32_16x16x32_bf16 v[20:23], v[176:179], v[208:211], v[20:23]
	v_mfma_f32_16x16x32_bf16 v[16:19], v[184:187], v[208:211], v[16:19]
	v_mfma_f32_16x16x32_bf16 v[4:7], v[176:179], v[216:219], v[4:7]
	v_mfma_f32_16x16x32_bf16 v[0:3], v[184:187], v[216:219], v[0:3]
	v_mfma_f32_16x16x32_bf16 v[52:55], v[180:183], v[196:199], v[52:55]
	v_mfma_f32_16x16x32_bf16 v[48:51], v[188:191], v[196:199], v[48:51]
	v_mfma_f32_16x16x32_bf16 v[36:39], v[180:183], v[204:207], v[36:39]
	v_mfma_f32_16x16x32_bf16 v[32:35], v[188:191], v[204:207], v[32:35]
	v_mfma_f32_16x16x32_bf16 v[20:23], v[180:183], v[212:215], v[20:23]
	v_mfma_f32_16x16x32_bf16 v[16:19], v[188:191], v[212:215], v[16:19]
	v_mfma_f32_16x16x32_bf16 v[4:7], v[180:183], v[220:223], v[4:7]
	v_mfma_f32_16x16x32_bf16 v[0:3], v[188:191], v[220:223], v[0:3]
	s_setprio 1
	s_barrier
	s_add_i32 s67, 0, 0x18000
	v_add_u32_e32 v132, s67, v139
	s_add_i32 s68, 0, 0x1c000
	ds_read_b128 v[160:163], v132
	ds_read_b128 v[164:167], v132 offset:1024
	ds_read_b128 v[168:171], v132 offset:2048
	ds_read_b128 v[172:175], v132 offset:3072
	v_add_u32_e32 v132, s68, v139
	ds_read_b128 v[176:179], v132
	ds_read_b128 v[180:183], v132 offset:1024
	ds_read_b128 v[184:187], v132 offset:2048
	ds_read_b128 v[188:191], v132 offset:3072
	s_mov_b32 m0, s51
	ds_read_b128 v[192:195], v154 offset:32768
	ds_read_b128 v[196:199], v154 offset:33792
	ds_read_b128 v[200:203], v154 offset:34816
	ds_read_b128 v[204:207], v154 offset:35840
	ds_read_b128 v[208:211], v154 offset:36864
	ds_read_b128 v[212:215], v154 offset:37888
	ds_read_b128 v[216:219], v154 offset:38912
	ds_read_b128 v[220:223], v154 offset:39936
	global_load_lds_dwordx4 v135, s[40:41]
	s_mov_b32 m0, s52
	s_nop 0
	global_load_lds_dwordx4 v141, s[40:41]
	s_waitcnt vmcnt(8)
	s_waitcnt lgkmcnt(0)
	s_barrier
	s_setprio 0
	s_waitcnt lgkmcnt(0)
	v_mfma_f32_16x16x32_bf16 v[116:119], v[160:163], v[192:195], v[116:119]
	v_mfma_f32_16x16x32_bf16 v[112:115], v[168:171], v[192:195], v[112:115]
	v_mfma_f32_16x16x32_bf16 v[108:111], v[160:163], v[200:203], v[108:111]
	v_mfma_f32_16x16x32_bf16 v[104:107], v[168:171], v[200:203], v[104:107]
	v_mfma_f32_16x16x32_bf16 v[92:95], v[160:163], v[208:211], v[92:95]
	v_mfma_f32_16x16x32_bf16 v[88:91], v[168:171], v[208:211], v[88:91]
	v_mfma_f32_16x16x32_bf16 v[76:79], v[160:163], v[216:219], v[76:79]
	v_mfma_f32_16x16x32_bf16 v[72:75], v[168:171], v[216:219], v[72:75]
	v_mfma_f32_16x16x32_bf16 v[116:119], v[164:167], v[196:199], v[116:119]
	v_mfma_f32_16x16x32_bf16 v[112:115], v[172:175], v[196:199], v[112:115]
	v_mfma_f32_16x16x32_bf16 v[108:111], v[164:167], v[204:207], v[108:111]
	v_mfma_f32_16x16x32_bf16 v[104:107], v[172:175], v[204:207], v[104:107]
	v_mfma_f32_16x16x32_bf16 v[92:95], v[164:167], v[212:215], v[92:95]
	v_mfma_f32_16x16x32_bf16 v[88:91], v[172:175], v[212:215], v[88:91]
	v_mfma_f32_16x16x32_bf16 v[76:79], v[164:167], v[220:223], v[76:79]
	v_mfma_f32_16x16x32_bf16 v[72:75], v[172:175], v[220:223], v[72:75]
	s_setprio 1
	s_setprio 0
	v_mfma_f32_16x16x32_bf16 v[124:127], v[176:179], v[192:195], v[124:127]
	v_mfma_f32_16x16x32_bf16 v[120:123], v[184:187], v[192:195], v[120:123]
	v_mfma_f32_16x16x32_bf16 v[100:103], v[176:179], v[200:203], v[100:103]
	v_mfma_f32_16x16x32_bf16 v[96:99], v[184:187], v[200:203], v[96:99]
	v_mfma_f32_16x16x32_bf16 v[84:87], v[176:179], v[208:211], v[84:87]
	v_mfma_f32_16x16x32_bf16 v[80:83], v[184:187], v[208:211], v[80:83]
	v_mfma_f32_16x16x32_bf16 v[68:71], v[176:179], v[216:219], v[68:71]
	v_mfma_f32_16x16x32_bf16 v[64:67], v[184:187], v[216:219], v[64:67]
	v_mfma_f32_16x16x32_bf16 v[124:127], v[180:183], v[196:199], v[124:127]
	v_mfma_f32_16x16x32_bf16 v[120:123], v[188:191], v[196:199], v[120:123]
	v_mfma_f32_16x16x32_bf16 v[100:103], v[180:183], v[204:207], v[100:103]
	v_mfma_f32_16x16x32_bf16 v[96:99], v[188:191], v[204:207], v[96:99]
	v_mfma_f32_16x16x32_bf16 v[84:87], v[180:183], v[212:215], v[84:87]
	v_mfma_f32_16x16x32_bf16 v[80:83], v[188:191], v[212:215], v[80:83]
	v_mfma_f32_16x16x32_bf16 v[68:71], v[180:183], v[220:223], v[68:71]
	v_mfma_f32_16x16x32_bf16 v[64:67], v[188:191], v[220:223], v[64:67]
	s_setprio 1
	s_barrier
	s_add_i32 s40, s67, s29
	v_lshl_add_u64 v[226:227], v[226:227], 0, s[18:19]
	s_mov_b32 m0, s40
	ds_read_b128 v[192:195], v154 offset:49152
	ds_read_b128 v[196:199], v154 offset:50176
	ds_read_b128 v[200:203], v154 offset:51200
	ds_read_b128 v[204:207], v154 offset:52224
	ds_read_b128 v[208:211], v154 offset:53248
	ds_read_b128 v[212:215], v154 offset:54272
	ds_read_b128 v[216:219], v154 offset:55296
	ds_read_b128 v[220:223], v154 offset:56320
	global_load_lds_dwordx4 v[226:227], off
	s_add_i32 m0, s40, 0x2000
	s_add_u32 s38, s38, 0x40080
	v_lshl_add_u64 v[226:227], v[228:229], 0, s[18:19]
	s_addc_u32 s39, s39, 0
	s_add_i32 s40, s68, s29
	global_load_lds_dwordx4 v[226:227], off
	v_lshl_add_u64 v[226:227], s[38:39], 0, v[128:129]
	s_mov_b32 m0, s40
	v_lshl_add_u64 v[224:225], v[224:225], 0, s[18:19]
	global_load_lds_dwordx4 v[226:227], off
	v_lshl_add_u64 v[226:227], s[38:39], 0, v[130:131]
	s_add_i32 m0, s40, 0x2000
	s_nop 0
	global_load_lds_dwordx4 v[226:227], off
	v_lshl_add_u64 v[226:227], v[230:231], 0, s[18:19]
	s_mov_b32 m0, s54
	s_nop 0
	global_load_lds_dwordx4 v[226:227], off
	s_mov_b32 m0, s55
	s_nop 0
	global_load_lds_dwordx4 v[224:225], off
	s_waitcnt vmcnt(8)
	s_waitcnt lgkmcnt(0)
	s_barrier
	s_setprio 0
	s_waitcnt lgkmcnt(0)
	v_mfma_f32_16x16x32_bf16 v[60:63], v[160:163], v[192:195], v[60:63]
	v_mfma_f32_16x16x32_bf16 v[56:59], v[168:171], v[192:195], v[56:59]
	v_mfma_f32_16x16x32_bf16 v[44:47], v[160:163], v[200:203], v[44:47]
	v_mfma_f32_16x16x32_bf16 v[40:43], v[168:171], v[200:203], v[40:43]
	v_mfma_f32_16x16x32_bf16 v[28:31], v[160:163], v[208:211], v[28:31]
	v_mfma_f32_16x16x32_bf16 v[24:27], v[168:171], v[208:211], v[24:27]
	v_mfma_f32_16x16x32_bf16 v[12:15], v[160:163], v[216:219], v[12:15]
	v_mfma_f32_16x16x32_bf16 v[8:11], v[168:171], v[216:219], v[8:11]
	v_mfma_f32_16x16x32_bf16 v[60:63], v[164:167], v[196:199], v[60:63]
	v_mfma_f32_16x16x32_bf16 v[56:59], v[172:175], v[196:199], v[56:59]
	v_mfma_f32_16x16x32_bf16 v[44:47], v[164:167], v[204:207], v[44:47]
	v_mfma_f32_16x16x32_bf16 v[40:43], v[172:175], v[204:207], v[40:43]
	v_mfma_f32_16x16x32_bf16 v[28:31], v[164:167], v[212:215], v[28:31]
	v_mfma_f32_16x16x32_bf16 v[24:27], v[172:175], v[212:215], v[24:27]
	v_mfma_f32_16x16x32_bf16 v[12:15], v[164:167], v[220:223], v[12:15]
	v_mfma_f32_16x16x32_bf16 v[8:11], v[172:175], v[220:223], v[8:11]
	s_setprio 1
	s_setprio 0
	v_mfma_f32_16x16x32_bf16 v[52:55], v[176:179], v[192:195], v[52:55]
	v_mfma_f32_16x16x32_bf16 v[48:51], v[184:187], v[192:195], v[48:51]
	v_mfma_f32_16x16x32_bf16 v[36:39], v[176:179], v[200:203], v[36:39]
	v_mfma_f32_16x16x32_bf16 v[32:35], v[184:187], v[200:203], v[32:35]
	v_mfma_f32_16x16x32_bf16 v[20:23], v[176:179], v[208:211], v[20:23]
	v_mfma_f32_16x16x32_bf16 v[16:19], v[184:187], v[208:211], v[16:19]
	v_mfma_f32_16x16x32_bf16 v[4:7], v[176:179], v[216:219], v[4:7]
	v_mfma_f32_16x16x32_bf16 v[0:3], v[184:187], v[216:219], v[0:3]
	v_mfma_f32_16x16x32_bf16 v[52:55], v[180:183], v[196:199], v[52:55]
	v_mfma_f32_16x16x32_bf16 v[48:51], v[188:191], v[196:199], v[48:51]
	v_mfma_f32_16x16x32_bf16 v[36:39], v[180:183], v[204:207], v[36:39]
	v_mfma_f32_16x16x32_bf16 v[32:35], v[188:191], v[204:207], v[32:35]
	v_mfma_f32_16x16x32_bf16 v[20:23], v[180:183], v[212:215], v[20:23]
	v_mfma_f32_16x16x32_bf16 v[16:19], v[188:191], v[212:215], v[16:19]
	v_mfma_f32_16x16x32_bf16 v[4:7], v[180:183], v[220:223], v[4:7]
	v_mfma_f32_16x16x32_bf16 v[0:3], v[188:191], v[220:223], v[0:3]
	s_setprio 1
	s_barrier
	s_add_i32 s66, s66, 2
	s_add_u32 s36, s36, 0x100
	s_addc_u32 s37, s37, 0
	s_cmp_gt_u32 s66, 13
	s_cbranch_scc0 .LBB0_4355
	s_and_b64 vcc, exec, s[20:21]
	s_cbranch_vccz .LBB0_4358
	s_barrier

.LBB0_4459:
	ds_read_b128 v[8:11], v149
	ds_read_b128 v[12:15], v149 offset:1024
	ds_read_b128 v[16:19], v149 offset:2048
	ds_read_b128 v[20:23], v149 offset:3072
	ds_read_b128 v[24:27], v150
	ds_read_b128 v[28:31], v150 offset:1024
	ds_read_b128 v[32:35], v150 offset:2048
	ds_read_b128 v[36:39], v150 offset:3072
	s_add_u32 s68, s36, 0x18080
	s_addc_u32 s69, s37, 0
	s_mov_b32 m0, s61
	v_lshl_add_u64 v[64:65], s[68:69], 0, v[128:129]
	ds_read_b128 v[0:3], v140
	ds_read_b128 v[4:7], v140 offset:1024
	ds_read_b128 v[40:43], v140 offset:2048
	ds_read_b128 v[44:47], v140 offset:3072
	ds_read_b128 v[48:51], v140 offset:4096
	ds_read_b128 v[52:55], v140 offset:5120
	ds_read_b128 v[56:59], v140 offset:6144
	ds_read_b128 v[60:63], v140 offset:7168
	global_load_lds_dwordx4 v[64:65], off
	v_lshl_add_u64 v[64:65], s[68:69], 0, v[132:133]
	s_mov_b32 m0, s62
	s_nop 0
	global_load_lds_dwordx4 v[64:65], off
	s_waitcnt vmcnt(8)
	s_waitcnt lgkmcnt(0)
	s_barrier
	s_setprio 0
	s_waitcnt lgkmcnt(0)
	v_mfma_f32_16x16x32_bf16 v[64:67], v[8:11], v[0:3], 0
	v_mfma_f32_16x16x32_bf16 v[68:71], v[16:19], v[0:3], 0
	v_mfma_f32_16x16x32_bf16 v[72:75], v[8:11], v[40:43], 0
	v_mfma_f32_16x16x32_bf16 v[76:79], v[16:19], v[40:43], 0
	v_mfma_f32_16x16x32_bf16 v[80:83], v[8:11], v[48:51], 0
	v_mfma_f32_16x16x32_bf16 v[84:87], v[16:19], v[48:51], 0
	v_mfma_f32_16x16x32_bf16 v[88:91], v[8:11], v[56:59], 0
	v_mfma_f32_16x16x32_bf16 v[92:95], v[16:19], v[56:59], 0
	v_mfma_f32_16x16x32_bf16 v[64:67], v[12:15], v[4:7], v[64:67]
	v_mfma_f32_16x16x32_bf16 v[68:71], v[20:23], v[4:7], v[68:71]
	v_mfma_f32_16x16x32_bf16 v[72:75], v[12:15], v[44:47], v[72:75]
	v_mfma_f32_16x16x32_bf16 v[76:79], v[20:23], v[44:47], v[76:79]
	v_mfma_f32_16x16x32_bf16 v[80:83], v[12:15], v[52:55], v[80:83]
	v_mfma_f32_16x16x32_bf16 v[84:87], v[20:23], v[52:55], v[84:87]
	v_mfma_f32_16x16x32_bf16 v[88:91], v[12:15], v[60:63], v[88:91]
	v_mfma_f32_16x16x32_bf16 v[92:95], v[20:23], v[60:63], v[92:95]
	s_setprio 1
	s_setprio 0
	v_mfma_f32_16x16x32_bf16 v[96:99], v[24:27], v[0:3], 0
	v_mfma_f32_16x16x32_bf16 v[0:3], v[32:35], v[0:3], 0
	v_mfma_f32_16x16x32_bf16 v[100:103], v[36:39], v[4:7], v[0:3]
	v_mfma_f32_16x16x32_bf16 v[0:3], v[24:27], v[40:43], 0
	v_mfma_f32_16x16x32_bf16 v[104:107], v[28:31], v[44:47], v[0:3]
	v_mfma_f32_16x16x32_bf16 v[0:3], v[32:35], v[40:43], 0
	v_mfma_f32_16x16x32_bf16 v[40:43], v[36:39], v[44:47], v[0:3]
	v_mfma_f32_16x16x32_bf16 v[0:3], v[24:27], v[48:51], 0
	v_mfma_f32_16x16x32_bf16 v[44:47], v[28:31], v[52:55], v[0:3]
	v_mfma_f32_16x16x32_bf16 v[0:3], v[32:35], v[48:51], 0
	v_mfma_f32_16x16x32_bf16 v[48:51], v[36:39], v[52:55], v[0:3]
	v_mfma_f32_16x16x32_bf16 v[0:3], v[24:27], v[56:59], 0
	v_mfma_f32_16x16x32_bf16 v[52:55], v[28:31], v[60:63], v[0:3]
	v_mfma_f32_16x16x32_bf16 v[0:3], v[32:35], v[56:59], 0
	v_mfma_f32_16x16x32_bf16 v[96:99], v[28:31], v[4:7], v[96:99]
	v_mfma_f32_16x16x32_bf16 v[56:59], v[36:39], v[60:63], v[0:3]
	s_setprio 1
	s_barrier
	s_nop 3
	v_lshl_add_u64 v[0:1], s[38:39], 0, v[130:131]
	s_add_i32 s70, s59, s45
	v_lshl_add_u64 v[2:3], v[0:1], 0, s[18:19]
	s_mov_b32 m0, s70
	s_add_i32 s67, s70, 0x2000
	ds_read_b128 v[60:63], v140 offset:16384
	ds_read_b128 v[108:111], v140 offset:17408
	ds_read_b128 v[112:115], v140 offset:18432
	ds_read_b128 v[116:119], v140 offset:19456
	ds_read_b128 v[120:123], v140 offset:20480
	ds_read_b128 v[124:127], v140 offset:21504
	ds_read_b128 v[152:155], v140 offset:22528
	ds_read_b128 v[156:159], v140 offset:23552
	global_load_lds_dwordx4 v[2:3], off
	v_lshl_add_u64 v[2:3], s[38:39], 0, v[134:135]
	s_add_u32 s72, s38, 0x1900
	v_lshl_add_u64 v[4:5], v[2:3], 0, s[18:19]
	s_mov_b32 m0, s67
	s_addc_u32 s73, s39, 0
	s_add_i32 s68, s60, s45
	global_load_lds_dwordx4 v[4:5], off
	v_lshl_add_u64 v[4:5], s[72:73], 0, v[130:131]
	s_mov_b32 m0, s68
	s_add_i32 s69, s68, 0x2000
	global_load_lds_dwordx4 v[4:5], off
	v_lshl_add_u64 v[4:5], s[72:73], 0, v[134:135]
	s_mov_b32 m0, s69
	s_nop 0
	global_load_lds_dwordx4 v[4:5], off
	v_lshl_add_u64 v[4:5], s[36:37], 0, v[128:129]
	v_lshl_add_u64 v[6:7], v[4:5], 0, s[18:19]
	s_mov_b32 m0, s46
	s_nop 0
	global_load_lds_dwordx4 v[6:7], off
	v_lshl_add_u64 v[6:7], s[36:37], 0, v[132:133]
	v_lshl_add_u64 v[136:137], v[6:7], 0, s[18:19]
	s_mov_b32 m0, s47
	s_nop 0
	global_load_lds_dwordx4 v[136:137], off
	s_waitcnt vmcnt(8)
	s_waitcnt lgkmcnt(0)
	s_barrier
	s_setprio 0
	s_waitcnt lgkmcnt(0)
	v_mfma_f32_16x16x32_bf16 v[160:163], v[8:11], v[60:63], 0
	v_mfma_f32_16x16x32_bf16 v[168:171], v[8:11], v[112:115], 0
	v_mfma_f32_16x16x32_bf16 v[176:179], v[8:11], v[120:123], 0
	v_mfma_f32_16x16x32_bf16 v[8:11], v[8:11], v[152:155], 0
	v_mfma_f32_16x16x32_bf16 v[160:163], v[12:15], v[108:111], v[160:163]
	v_mfma_f32_16x16x32_bf16 v[164:167], v[16:19], v[60:63], 0
	v_mfma_f32_16x16x32_bf16 v[168:171], v[12:15], v[116:119], v[168:171]
	v_mfma_f32_16x16x32_bf16 v[172:175], v[16:19], v[112:115], 0
	v_mfma_f32_16x16x32_bf16 v[176:179], v[12:15], v[124:127], v[176:179]
	v_mfma_f32_16x16x32_bf16 v[180:183], v[16:19], v[120:123], 0
	v_mfma_f32_16x16x32_bf16 v[10:13], v[12:15], v[156:159], v[8:11]
	v_mfma_f32_16x16x32_bf16 v[14:17], v[16:19], v[152:155], 0
	v_mfma_f32_16x16x32_bf16 v[14:17], v[20:23], v[156:159], v[14:17]
	v_mfma_f32_16x16x32_bf16 v[164:167], v[20:23], v[108:111], v[164:167]
	v_mfma_f32_16x16x32_bf16 v[172:175], v[20:23], v[116:119], v[172:175]
	v_mfma_f32_16x16x32_bf16 v[180:183], v[20:23], v[124:127], v[180:183]
	s_setprio 1
	s_setprio 0
	v_mfma_f32_16x16x32_bf16 v[18:21], v[24:27], v[60:63], 0
	v_mfma_f32_16x16x32_bf16 v[60:63], v[32:35], v[60:63], 0
	v_mfma_f32_16x16x32_bf16 v[18:21], v[28:31], v[108:111], v[18:21]
	v_mfma_f32_16x16x32_bf16 v[60:63], v[36:39], v[108:111], v[60:63]
	v_mfma_f32_16x16x32_bf16 v[108:111], v[24:27], v[112:115], 0
	v_mfma_f32_16x16x32_bf16 v[112:115], v[32:35], v[112:115], 0
	v_mfma_f32_16x16x32_bf16 v[108:111], v[28:31], v[116:119], v[108:111]
	v_mfma_f32_16x16x32_bf16 v[112:115], v[36:39], v[116:119], v[112:115]
	v_mfma_f32_16x16x32_bf16 v[116:119], v[24:27], v[120:123], 0
	v_mfma_f32_16x16x32_bf16 v[22:25], v[24:27], v[152:155], 0
	v_mfma_f32_16x16x32_bf16 v[116:119], v[28:31], v[124:127], v[116:119]
	v_mfma_f32_16x16x32_bf16 v[120:123], v[32:35], v[120:123], 0
	v_mfma_f32_16x16x32_bf16 v[22:25], v[28:31], v[156:159], v[22:25]
	v_mfma_f32_16x16x32_bf16 v[26:29], v[32:35], v[152:155], 0
	v_mfma_f32_16x16x32_bf16 v[120:123], v[36:39], v[124:127], v[120:123]
	v_mfma_f32_16x16x32_bf16 v[26:29], v[36:39], v[156:159], v[26:29]
	s_setprio 1
	s_barrier
	s_add_i32 s74, 0, 0x18000
	s_add_i32 s75, 0, 0x1c000
	v_add_u32_e32 v8, s74, v139
	v_add_u32_e32 v9, s75, v139
	ds_read_b128 v[30:33], v8
	ds_read_b128 v[34:37], v8 offset:1024
	ds_read_b128 v[124:127], v8 offset:2048
	ds_read_b128 v[152:155], v8 offset:3072
	ds_read_b128 v[156:159], v9
	ds_read_b128 v[184:187], v9 offset:1024
	ds_read_b128 v[188:191], v9 offset:2048
	ds_read_b128 v[192:195], v9 offset:3072
	s_add_u32 s72, s36, 0x18100
	s_addc_u32 s73, s37, 0
	s_mov_b32 m0, s49
	v_lshl_add_u64 v[38:39], s[72:73], 0, v[128:129]
	ds_read_b128 v[196:199], v140 offset:32768
	ds_read_b128 v[200:203], v140 offset:33792
	ds_read_b128 v[204:207], v140 offset:34816
	ds_read_b128 v[208:211], v140 offset:35840
	ds_read_b128 v[212:215], v140 offset:36864
	ds_read_b128 v[216:219], v140 offset:37888
	ds_read_b128 v[220:223], v140 offset:38912
	ds_read_b128 v[224:227], v140 offset:39936
	global_load_lds_dwordx4 v[38:39], off
	v_lshl_add_u64 v[38:39], s[72:73], 0, v[132:133]
	s_mov_b32 m0, s50
	s_nop 0
	global_load_lds_dwordx4 v[38:39], off
	s_waitcnt vmcnt(8)
	s_waitcnt lgkmcnt(0)
	s_barrier
	s_setprio 0
	s_waitcnt lgkmcnt(0)
	v_mfma_f32_16x16x32_bf16 v[64:67], v[30:33], v[196:199], v[64:67]
	v_mfma_f32_16x16x32_bf16 v[68:71], v[124:127], v[196:199], v[68:71]
	v_mfma_f32_16x16x32_bf16 v[72:75], v[30:33], v[204:207], v[72:75]
	v_mfma_f32_16x16x32_bf16 v[76:79], v[124:127], v[204:207], v[76:79]
	v_mfma_f32_16x16x32_bf16 v[80:83], v[30:33], v[212:215], v[80:83]
	v_mfma_f32_16x16x32_bf16 v[84:87], v[124:127], v[212:215], v[84:87]
	v_mfma_f32_16x16x32_bf16 v[88:91], v[30:33], v[220:223], v[88:91]
	v_mfma_f32_16x16x32_bf16 v[92:95], v[124:127], v[220:223], v[92:95]
	v_mfma_f32_16x16x32_bf16 v[64:67], v[34:37], v[200:203], v[64:67]
	v_mfma_f32_16x16x32_bf16 v[68:71], v[152:155], v[200:203], v[68:71]
	v_mfma_f32_16x16x32_bf16 v[72:75], v[34:37], v[208:211], v[72:75]
	v_mfma_f32_16x16x32_bf16 v[76:79], v[152:155], v[208:211], v[76:79]
	v_mfma_f32_16x16x32_bf16 v[80:83], v[34:37], v[216:219], v[80:83]
	v_mfma_f32_16x16x32_bf16 v[84:87], v[152:155], v[216:219], v[84:87]
	v_mfma_f32_16x16x32_bf16 v[88:91], v[34:37], v[224:227], v[88:91]
	v_mfma_f32_16x16x32_bf16 v[92:95], v[152:155], v[224:227], v[92:95]
	s_setprio 1
	s_setprio 0
	v_mfma_f32_16x16x32_bf16 v[96:99], v[156:159], v[196:199], v[96:99]
	v_mfma_f32_16x16x32_bf16 v[100:103], v[188:191], v[196:199], v[100:103]
	v_mfma_f32_16x16x32_bf16 v[104:107], v[156:159], v[204:207], v[104:107]
	v_mfma_f32_16x16x32_bf16 v[38:41], v[188:191], v[204:207], v[40:43]
	v_mfma_f32_16x16x32_bf16 v[42:45], v[156:159], v[212:215], v[44:47]
	v_mfma_f32_16x16x32_bf16 v[46:49], v[188:191], v[212:215], v[48:51]
	v_mfma_f32_16x16x32_bf16 v[50:53], v[156:159], v[220:223], v[52:55]
	v_mfma_f32_16x16x32_bf16 v[54:57], v[188:191], v[220:223], v[56:59]
	v_mfma_f32_16x16x32_bf16 v[96:99], v[184:187], v[200:203], v[96:99]
	v_mfma_f32_16x16x32_bf16 v[100:103], v[192:195], v[200:203], v[100:103]
	v_mfma_f32_16x16x32_bf16 v[104:107], v[184:187], v[208:211], v[104:107]
	v_mfma_f32_16x16x32_bf16 v[38:41], v[192:195], v[208:211], v[38:41]
	v_mfma_f32_16x16x32_bf16 v[42:45], v[184:187], v[216:219], v[42:45]
	v_mfma_f32_16x16x32_bf16 v[46:49], v[192:195], v[216:219], v[46:49]
	v_mfma_f32_16x16x32_bf16 v[50:53], v[184:187], v[224:227], v[50:53]
	v_mfma_f32_16x16x32_bf16 v[54:57], v[192:195], v[224:227], v[54:57]
	s_setprio 1
	s_barrier
	s_add_i32 s74, s74, s45
	s_add_i32 s71, s74, 0x2000
	v_lshl_add_u64 v[58:59], v[0:1], 0, s[20:21]
	s_mov_b32 m0, s74
	s_add_u32 s76, s38, 0x1980
	ds_read_b128 v[196:199], v140 offset:49152
	ds_read_b128 v[200:203], v140 offset:50176
	ds_read_b128 v[204:207], v140 offset:51200
	ds_read_b128 v[208:211], v140 offset:52224
	ds_read_b128 v[212:215], v140 offset:53248
	ds_read_b128 v[216:219], v140 offset:54272
	ds_read_b128 v[220:223], v140 offset:55296
	ds_read_b128 v[224:227], v140 offset:56320
	global_load_lds_dwordx4 v[58:59], off
	v_lshl_add_u64 v[58:59], v[2:3], 0, s[20:21]
	s_mov_b32 m0, s71
	s_addc_u32 s77, s39, 0
	s_add_i32 s72, s75, s45
	global_load_lds_dwordx4 v[58:59], off
	v_lshl_add_u64 v[58:59], s[76:77], 0, v[130:131]
	s_mov_b32 m0, s72
	s_add_i32 s73, s72, 0x2000
	global_load_lds_dwordx4 v[58:59], off
	v_lshl_add_u64 v[58:59], s[76:77], 0, v[134:135]
	s_mov_b32 m0, s73
	s_nop 0
	global_load_lds_dwordx4 v[58:59], off
	v_lshl_add_u64 v[58:59], v[4:5], 0, s[20:21]
	s_mov_b32 m0, s52
	s_nop 0
	global_load_lds_dwordx4 v[58:59], off
	v_lshl_add_u64 v[58:59], v[6:7], 0, s[20:21]
	s_mov_b32 m0, s53
	s_nop 0
	global_load_lds_dwordx4 v[58:59], off
	s_waitcnt vmcnt(8)
	s_waitcnt lgkmcnt(0)
	s_barrier
	s_setprio 0
	s_waitcnt lgkmcnt(0)
	v_mfma_f32_16x16x32_bf16 v[10:13], v[30:33], v[220:223], v[10:13]
	v_mfma_f32_16x16x32_bf16 v[14:17], v[124:127], v[220:223], v[14:17]
	v_mfma_f32_16x16x32_bf16 v[160:163], v[30:33], v[196:199], v[160:163]
	v_mfma_f32_16x16x32_bf16 v[164:167], v[124:127], v[196:199], v[164:167]
	v_mfma_f32_16x16x32_bf16 v[168:171], v[30:33], v[204:207], v[168:171]
	v_mfma_f32_16x16x32_bf16 v[172:175], v[124:127], v[204:207], v[172:175]
	v_mfma_f32_16x16x32_bf16 v[176:179], v[30:33], v[212:215], v[176:179]
	v_mfma_f32_16x16x32_bf16 v[180:183], v[124:127], v[212:215], v[180:183]
	v_mfma_f32_16x16x32_bf16 v[10:13], v[34:37], v[224:227], v[10:13]
	v_mfma_f32_16x16x32_bf16 v[14:17], v[152:155], v[224:227], v[14:17]
	v_mfma_f32_16x16x32_bf16 v[160:163], v[34:37], v[200:203], v[160:163]
	v_mfma_f32_16x16x32_bf16 v[164:167], v[152:155], v[200:203], v[164:167]
	v_mfma_f32_16x16x32_bf16 v[168:171], v[34:37], v[208:211], v[168:171]
	v_mfma_f32_16x16x32_bf16 v[172:175], v[152:155], v[208:211], v[172:175]
	v_mfma_f32_16x16x32_bf16 v[176:179], v[34:37], v[216:219], v[176:179]
	v_mfma_f32_16x16x32_bf16 v[180:183], v[152:155], v[216:219], v[180:183]
	s_setprio 1
	s_setprio 0
	v_mfma_f32_16x16x32_bf16 v[18:21], v[156:159], v[196:199], v[18:21]
	v_mfma_f32_16x16x32_bf16 v[30:33], v[188:191], v[196:199], v[60:63]
	v_mfma_f32_16x16x32_bf16 v[34:37], v[156:159], v[204:207], v[108:111]
	v_mfma_f32_16x16x32_bf16 v[58:61], v[188:191], v[204:207], v[112:115]
	v_mfma_f32_16x16x32_bf16 v[108:111], v[156:159], v[212:215], v[116:119]
	v_mfma_f32_16x16x32_bf16 v[112:115], v[188:191], v[212:215], v[120:123]
	v_mfma_f32_16x16x32_bf16 v[22:25], v[156:159], v[220:223], v[22:25]
	v_mfma_f32_16x16x32_bf16 v[26:29], v[188:191], v[220:223], v[26:29]
	v_mfma_f32_16x16x32_bf16 v[18:21], v[184:187], v[200:203], v[18:21]
	v_mfma_f32_16x16x32_bf16 v[30:33], v[192:195], v[200:203], v[30:33]
	v_mfma_f32_16x16x32_bf16 v[34:37], v[184:187], v[208:211], v[34:37]
	v_mfma_f32_16x16x32_bf16 v[58:61], v[192:195], v[208:211], v[58:61]
	v_mfma_f32_16x16x32_bf16 v[108:111], v[184:187], v[216:219], v[108:111]
	v_mfma_f32_16x16x32_bf16 v[112:115], v[192:195], v[216:219], v[112:115]
	v_mfma_f32_16x16x32_bf16 v[22:25], v[184:187], v[224:227], v[22:25]
	v_mfma_f32_16x16x32_bf16 v[26:29], v[192:195], v[224:227], v[26:29]
	s_setprio 1
	s_barrier
	ds_read_b128 v[116:119], v149
	ds_read_b128 v[120:123], v149 offset:1024
	ds_read_b128 v[124:127], v149 offset:2048
	ds_read_b128 v[152:155], v149 offset:3072
	ds_read_b128 v[156:159], v150
	ds_read_b128 v[184:187], v150 offset:1024
	ds_read_b128 v[188:191], v150 offset:2048
	ds_read_b128 v[192:195], v150 offset:3072
	s_add_u32 s76, s36, 0x18180
	s_addc_u32 s77, s37, 0
	s_mov_b32 m0, s61
	v_lshl_add_u64 v[62:63], s[76:77], 0, v[128:129]
	ds_read_b128 v[196:199], v140
	ds_read_b128 v[200:203], v140 offset:1024
	ds_read_b128 v[204:207], v140 offset:2048
	ds_read_b128 v[208:211], v140 offset:3072
	ds_read_b128 v[212:215], v140 offset:4096
	ds_read_b128 v[216:219], v140 offset:5120
	ds_read_b128 v[220:223], v140 offset:6144
	ds_read_b128 v[224:227], v140 offset:7168
	global_load_lds_dwordx4 v[62:63], off
	v_lshl_add_u64 v[62:63], s[76:77], 0, v[132:133]
	s_mov_b32 m0, s62
	s_nop 0
	global_load_lds_dwordx4 v[62:63], off
	s_waitcnt vmcnt(8)
	s_waitcnt lgkmcnt(0)
	s_barrier
	s_setprio 0
	s_waitcnt lgkmcnt(0)
	v_mfma_f32_16x16x32_bf16 v[62:65], v[116:119], v[196:199], v[64:67]
	v_mfma_f32_16x16x32_bf16 v[66:69], v[124:127], v[196:199], v[68:71]
	v_mfma_f32_16x16x32_bf16 v[70:73], v[116:119], v[204:207], v[72:75]
	v_mfma_f32_16x16x32_bf16 v[74:77], v[124:127], v[204:207], v[76:79]
	v_mfma_f32_16x16x32_bf16 v[78:81], v[116:119], v[212:215], v[80:83]
	v_mfma_f32_16x16x32_bf16 v[82:85], v[124:127], v[212:215], v[84:87]
	v_mfma_f32_16x16x32_bf16 v[86:89], v[116:119], v[220:223], v[88:91]
	v_mfma_f32_16x16x32_bf16 v[90:93], v[124:127], v[220:223], v[92:95]
	v_mfma_f32_16x16x32_bf16 v[62:65], v[120:123], v[200:203], v[62:65]
	v_mfma_f32_16x16x32_bf16 v[66:69], v[152:155], v[200:203], v[66:69]
	v_mfma_f32_16x16x32_bf16 v[70:73], v[120:123], v[208:211], v[70:73]
	v_mfma_f32_16x16x32_bf16 v[74:77], v[152:155], v[208:211], v[74:77]
	v_mfma_f32_16x16x32_bf16 v[78:81], v[120:123], v[216:219], v[78:81]
	v_mfma_f32_16x16x32_bf16 v[82:85], v[152:155], v[216:219], v[82:85]
	v_mfma_f32_16x16x32_bf16 v[86:89], v[120:123], v[224:227], v[86:89]
	v_mfma_f32_16x16x32_bf16 v[90:93], v[152:155], v[224:227], v[90:93]
	s_setprio 1
	s_setprio 0
	v_mfma_f32_16x16x32_bf16 v[94:97], v[156:159], v[196:199], v[96:99]
	v_mfma_f32_16x16x32_bf16 v[98:101], v[188:191], v[196:199], v[100:103]
	v_mfma_f32_16x16x32_bf16 v[102:105], v[156:159], v[204:207], v[104:107]
	v_mfma_f32_16x16x32_bf16 v[38:41], v[188:191], v[204:207], v[38:41]
	v_mfma_f32_16x16x32_bf16 v[42:45], v[156:159], v[212:215], v[42:45]
	v_mfma_f32_16x16x32_bf16 v[46:49], v[188:191], v[212:215], v[46:49]
	v_mfma_f32_16x16x32_bf16 v[50:53], v[156:159], v[220:223], v[50:53]
	v_mfma_f32_16x16x32_bf16 v[54:57], v[188:191], v[220:223], v[54:57]
	v_mfma_f32_16x16x32_bf16 v[94:97], v[184:187], v[200:203], v[94:97]
	v_mfma_f32_16x16x32_bf16 v[98:101], v[192:195], v[200:203], v[98:101]
	v_mfma_f32_16x16x32_bf16 v[102:105], v[184:187], v[208:211], v[102:105]
	v_mfma_f32_16x16x32_bf16 v[38:41], v[192:195], v[208:211], v[38:41]
	v_mfma_f32_16x16x32_bf16 v[42:45], v[184:187], v[216:219], v[42:45]
	v_mfma_f32_16x16x32_bf16 v[46:49], v[192:195], v[216:219], v[46:49]
	v_mfma_f32_16x16x32_bf16 v[50:53], v[184:187], v[224:227], v[50:53]
	v_mfma_f32_16x16x32_bf16 v[54:57], v[192:195], v[224:227], v[54:57]
	s_setprio 1
	s_barrier
	s_mov_b32 m0, s70
	v_lshl_add_u64 v[106:107], v[0:1], 0, s[22:23]
	s_add_u32 s76, s38, 0x1a00
	ds_read_b128 v[196:199], v140 offset:16384
	ds_read_b128 v[200:203], v140 offset:17408
	ds_read_b128 v[204:207], v140 offset:18432
	ds_read_b128 v[208:211], v140 offset:19456
	ds_read_b128 v[212:215], v140 offset:20480
	ds_read_b128 v[216:219], v140 offset:21504
	ds_read_b128 v[220:223], v140 offset:22528
	ds_read_b128 v[224:227], v140 offset:23552
	global_load_lds_dwordx4 v[106:107], off
	v_lshl_add_u64 v[106:107], v[2:3], 0, s[22:23]
	s_mov_b32 m0, s67
	s_addc_u32 s77, s39, 0
	global_load_lds_dwordx4 v[106:107], off
	v_lshl_add_u64 v[106:107], s[76:77], 0, v[130:131]
	s_mov_b32 m0, s68
	s_nop 0
	global_load_lds_dwordx4 v[106:107], off
	v_lshl_add_u64 v[106:107], s[76:77], 0, v[134:135]
	s_mov_b32 m0, s69
	s_nop 0
	global_load_lds_dwordx4 v[106:107], off
	v_lshl_add_u64 v[106:107], v[4:5], 0, s[22:23]
	s_mov_b32 m0, s46
	s_nop 0
	global_load_lds_dwordx4 v[106:107], off
	v_lshl_add_u64 v[106:107], v[6:7], 0, s[22:23]
	s_mov_b32 m0, s47
	s_nop 0
	global_load_lds_dwordx4 v[106:107], off
	s_waitcnt vmcnt(8)
	s_waitcnt lgkmcnt(0)
	s_barrier
	s_setprio 0
	s_waitcnt lgkmcnt(0)
	v_mfma_f32_16x16x32_bf16 v[10:13], v[116:119], v[220:223], v[10:13]
	v_mfma_f32_16x16x32_bf16 v[14:17], v[124:127], v[220:223], v[14:17]
	v_mfma_f32_16x16x32_bf16 v[160:163], v[116:119], v[196:199], v[160:163]
	v_mfma_f32_16x16x32_bf16 v[164:167], v[124:127], v[196:199], v[164:167]
	v_mfma_f32_16x16x32_bf16 v[168:171], v[116:119], v[204:207], v[168:171]
	v_mfma_f32_16x16x32_bf16 v[172:175], v[124:127], v[204:207], v[172:175]
	v_mfma_f32_16x16x32_bf16 v[176:179], v[116:119], v[212:215], v[176:179]
	v_mfma_f32_16x16x32_bf16 v[180:183], v[124:127], v[212:215], v[180:183]
	v_mfma_f32_16x16x32_bf16 v[10:13], v[120:123], v[224:227], v[10:13]
	v_mfma_f32_16x16x32_bf16 v[14:17], v[152:155], v[224:227], v[14:17]
	v_mfma_f32_16x16x32_bf16 v[160:163], v[120:123], v[200:203], v[160:163]
	v_mfma_f32_16x16x32_bf16 v[164:167], v[152:155], v[200:203], v[164:167]
	v_mfma_f32_16x16x32_bf16 v[168:171], v[120:123], v[208:211], v[168:171]
	v_mfma_f32_16x16x32_bf16 v[172:175], v[152:155], v[208:211], v[172:175]
	v_mfma_f32_16x16x32_bf16 v[176:179], v[120:123], v[216:219], v[176:179]
	v_mfma_f32_16x16x32_bf16 v[180:183], v[152:155], v[216:219], v[180:183]
	s_setprio 1
	s_setprio 0
	v_mfma_f32_16x16x32_bf16 v[18:21], v[156:159], v[196:199], v[18:21]
	v_mfma_f32_16x16x32_bf16 v[30:33], v[188:191], v[196:199], v[30:33]
	v_mfma_f32_16x16x32_bf16 v[34:37], v[156:159], v[204:207], v[34:37]
	v_mfma_f32_16x16x32_bf16 v[58:61], v[188:191], v[204:207], v[58:61]
	v_mfma_f32_16x16x32_bf16 v[106:109], v[156:159], v[212:215], v[108:111]
	v_mfma_f32_16x16x32_bf16 v[110:113], v[188:191], v[212:215], v[112:115]
	v_mfma_f32_16x16x32_bf16 v[22:25], v[156:159], v[220:223], v[22:25]
	v_mfma_f32_16x16x32_bf16 v[26:29], v[188:191], v[220:223], v[26:29]
	v_mfma_f32_16x16x32_bf16 v[18:21], v[184:187], v[200:203], v[18:21]
	v_mfma_f32_16x16x32_bf16 v[30:33], v[192:195], v[200:203], v[30:33]
	v_mfma_f32_16x16x32_bf16 v[34:37], v[184:187], v[208:211], v[34:37]
	v_mfma_f32_16x16x32_bf16 v[58:61], v[192:195], v[208:211], v[58:61]
	v_mfma_f32_16x16x32_bf16 v[106:109], v[184:187], v[216:219], v[106:109]
	v_mfma_f32_16x16x32_bf16 v[110:113], v[192:195], v[216:219], v[110:113]
	v_mfma_f32_16x16x32_bf16 v[22:25], v[184:187], v[224:227], v[22:25]
	v_mfma_f32_16x16x32_bf16 v[26:29], v[192:195], v[224:227], v[26:29]
	s_setprio 1
	s_barrier
	ds_read_b128 v[114:117], v8
	ds_read_b128 v[118:121], v8 offset:1024
	ds_read_b128 v[122:125], v8 offset:2048
	ds_read_b128 v[152:155], v8 offset:3072
	ds_read_b128 v[156:159], v9
	ds_read_b128 v[184:187], v9 offset:1024
	ds_read_b128 v[188:191], v9 offset:2048
	ds_read_b128 v[192:195], v9 offset:3072
	s_add_u32 s76, s36, 0x18200
	s_addc_u32 s77, s37, 0
	s_mov_b32 m0, s49
	v_lshl_add_u64 v[126:127], s[76:77], 0, v[128:129]
	ds_read_b128 v[196:199], v140 offset:32768
	ds_read_b128 v[200:203], v140 offset:33792
	ds_read_b128 v[204:207], v140 offset:34816
	ds_read_b128 v[208:211], v140 offset:35840
	ds_read_b128 v[212:215], v140 offset:36864
	ds_read_b128 v[216:219], v140 offset:37888
	ds_read_b128 v[220:223], v140 offset:38912
	ds_read_b128 v[224:227], v140 offset:39936
	global_load_lds_dwordx4 v[126:127], off
	v_lshl_add_u64 v[126:127], s[76:77], 0, v[132:133]
	s_mov_b32 m0, s50
	s_nop 0
	global_load_lds_dwordx4 v[126:127], off
	s_waitcnt vmcnt(8)
	s_waitcnt lgkmcnt(0)
	s_barrier
	s_setprio 0
	s_waitcnt lgkmcnt(0)
	v_mfma_f32_16x16x32_bf16 v[62:65], v[114:117], v[196:199], v[62:65]
	v_mfma_f32_16x16x32_bf16 v[66:69], v[122:125], v[196:199], v[66:69]
	v_mfma_f32_16x16x32_bf16 v[70:73], v[114:117], v[204:207], v[70:73]
	v_mfma_f32_16x16x32_bf16 v[74:77], v[122:125], v[204:207], v[74:77]
	v_mfma_f32_16x16x32_bf16 v[78:81], v[114:117], v[212:215], v[78:81]
	v_mfma_f32_16x16x32_bf16 v[82:85], v[122:125], v[212:215], v[82:85]
	v_mfma_f32_16x16x32_bf16 v[86:89], v[114:117], v[220:223], v[86:89]
	v_mfma_f32_16x16x32_bf16 v[90:93], v[122:125], v[220:223], v[90:93]
	v_mfma_f32_16x16x32_bf16 v[62:65], v[118:121], v[200:203], v[62:65]
	v_mfma_f32_16x16x32_bf16 v[66:69], v[152:155], v[200:203], v[66:69]
	v_mfma_f32_16x16x32_bf16 v[70:73], v[118:121], v[208:211], v[70:73]
	v_mfma_f32_16x16x32_bf16 v[74:77], v[152:155], v[208:211], v[74:77]
	v_mfma_f32_16x16x32_bf16 v[78:81], v[118:121], v[216:219], v[78:81]
	v_mfma_f32_16x16x32_bf16 v[82:85], v[152:155], v[216:219], v[82:85]
	v_mfma_f32_16x16x32_bf16 v[86:89], v[118:121], v[224:227], v[86:89]
	v_mfma_f32_16x16x32_bf16 v[90:93], v[152:155], v[224:227], v[90:93]
	s_setprio 1
	s_setprio 0
	v_mfma_f32_16x16x32_bf16 v[94:97], v[156:159], v[196:199], v[94:97]
	v_mfma_f32_16x16x32_bf16 v[98:101], v[188:191], v[196:199], v[98:101]
	v_mfma_f32_16x16x32_bf16 v[102:105], v[156:159], v[204:207], v[102:105]
	v_mfma_f32_16x16x32_bf16 v[38:41], v[188:191], v[204:207], v[38:41]
	v_mfma_f32_16x16x32_bf16 v[42:45], v[156:159], v[212:215], v[42:45]
	v_mfma_f32_16x16x32_bf16 v[46:49], v[188:191], v[212:215], v[46:49]
	v_mfma_f32_16x16x32_bf16 v[50:53], v[156:159], v[220:223], v[50:53]
	v_mfma_f32_16x16x32_bf16 v[54:57], v[188:191], v[220:223], v[54:57]
	v_mfma_f32_16x16x32_bf16 v[94:97], v[184:187], v[200:203], v[94:97]
	v_mfma_f32_16x16x32_bf16 v[98:101], v[192:195], v[200:203], v[98:101]
	v_mfma_f32_16x16x32_bf16 v[102:105], v[184:187], v[208:211], v[102:105]
	v_mfma_f32_16x16x32_bf16 v[38:41], v[192:195], v[208:211], v[38:41]
	v_mfma_f32_16x16x32_bf16 v[42:45], v[184:187], v[216:219], v[42:45]
	v_mfma_f32_16x16x32_bf16 v[46:49], v[192:195], v[216:219], v[46:49]
	v_mfma_f32_16x16x32_bf16 v[50:53], v[184:187], v[224:227], v[50:53]
	v_mfma_f32_16x16x32_bf16 v[54:57], v[192:195], v[224:227], v[54:57]
	s_setprio 1
	s_barrier
	s_mov_b32 m0, s74
	v_lshl_add_u64 v[0:1], v[0:1], 0, s[24:25]
	s_add_u32 s38, s38, 0x1a80
	ds_read_b128 v[196:199], v140 offset:49152
	ds_read_b128 v[200:203], v140 offset:50176
	ds_read_b128 v[204:207], v140 offset:51200
	ds_read_b128 v[208:211], v140 offset:52224
	ds_read_b128 v[212:215], v140 offset:53248
	ds_read_b128 v[216:219], v140 offset:54272
	ds_read_b128 v[220:223], v140 offset:55296
	ds_read_b128 v[224:227], v140 offset:56320
	global_load_lds_dwordx4 v[0:1], off
	v_lshl_add_u64 v[0:1], v[2:3], 0, s[24:25]
	s_mov_b32 m0, s71
	s_addc_u32 s39, s39, 0
	global_load_lds_dwordx4 v[0:1], off
	v_lshl_add_u64 v[0:1], s[38:39], 0, v[130:131]
	s_mov_b32 m0, s72
	s_nop 0
	global_load_lds_dwordx4 v[0:1], off
	v_lshl_add_u64 v[0:1], s[38:39], 0, v[134:135]
	s_mov_b32 m0, s73
	s_nop 0
	global_load_lds_dwordx4 v[0:1], off
	v_lshl_add_u64 v[0:1], v[4:5], 0, s[24:25]
	s_mov_b32 m0, s52
	s_nop 0
	global_load_lds_dwordx4 v[0:1], off
	v_lshl_add_u64 v[0:1], v[6:7], 0, s[24:25]
	s_mov_b32 m0, s53
	s_nop 0
	global_load_lds_dwordx4 v[0:1], off
	s_waitcnt vmcnt(8)
	s_waitcnt lgkmcnt(0)
	s_barrier
	s_setprio 0
	s_waitcnt lgkmcnt(0)
	v_mfma_f32_16x16x32_bf16 v[0:3], v[114:117], v[196:199], v[160:163]
	v_mfma_f32_16x16x32_bf16 v[4:7], v[122:125], v[196:199], v[164:167]
	v_mfma_f32_16x16x32_bf16 v[10:13], v[114:117], v[220:223], v[10:13]
	v_mfma_f32_16x16x32_bf16 v[14:17], v[122:125], v[220:223], v[14:17]
	v_mfma_f32_16x16x32_bf16 v[0:3], v[118:121], v[200:203], v[0:3]
	v_mfma_f32_16x16x32_bf16 v[4:7], v[152:155], v[200:203], v[4:7]
	v_mfma_f32_16x16x32_bf16 v[160:163], v[114:117], v[204:207], v[168:171]
	v_mfma_f32_16x16x32_bf16 v[164:167], v[122:125], v[204:207], v[172:175]
	v_mfma_f32_16x16x32_bf16 v[168:171], v[114:117], v[212:215], v[176:179]
	v_mfma_f32_16x16x32_bf16 v[172:175], v[122:125], v[212:215], v[180:183]
	v_mfma_f32_16x16x32_bf16 v[10:13], v[118:121], v[224:227], v[10:13]
	v_mfma_f32_16x16x32_bf16 v[14:17], v[152:155], v[224:227], v[14:17]
	v_mfma_f32_16x16x32_bf16 v[160:163], v[118:121], v[208:211], v[160:163]
	v_mfma_f32_16x16x32_bf16 v[164:167], v[152:155], v[208:211], v[164:167]
	v_mfma_f32_16x16x32_bf16 v[168:171], v[118:121], v[216:219], v[168:171]
	v_mfma_f32_16x16x32_bf16 v[172:175], v[152:155], v[216:219], v[172:175]
	s_setprio 1
	s_setprio 0
	v_mfma_f32_16x16x32_bf16 v[18:21], v[156:159], v[196:199], v[18:21]
	v_mfma_f32_16x16x32_bf16 v[30:33], v[188:191], v[196:199], v[30:33]
	v_mfma_f32_16x16x32_bf16 v[34:37], v[156:159], v[204:207], v[34:37]
	v_mfma_f32_16x16x32_bf16 v[58:61], v[188:191], v[204:207], v[58:61]
	v_mfma_f32_16x16x32_bf16 v[106:109], v[156:159], v[212:215], v[106:109]
	v_mfma_f32_16x16x32_bf16 v[110:113], v[188:191], v[212:215], v[110:113]
	v_mfma_f32_16x16x32_bf16 v[22:25], v[156:159], v[220:223], v[22:25]
	v_mfma_f32_16x16x32_bf16 v[26:29], v[188:191], v[220:223], v[26:29]
	v_mfma_f32_16x16x32_bf16 v[18:21], v[184:187], v[200:203], v[18:21]
	v_mfma_f32_16x16x32_bf16 v[30:33], v[192:195], v[200:203], v[30:33]
	v_mfma_f32_16x16x32_bf16 v[34:37], v[184:187], v[208:211], v[34:37]
	v_mfma_f32_16x16x32_bf16 v[58:61], v[192:195], v[208:211], v[58:61]
	v_mfma_f32_16x16x32_bf16 v[106:109], v[184:187], v[216:219], v[106:109]
	v_mfma_f32_16x16x32_bf16 v[110:113], v[192:195], v[216:219], v[110:113]
	v_mfma_f32_16x16x32_bf16 v[22:25], v[184:187], v[224:227], v[22:25]
	v_mfma_f32_16x16x32_bf16 v[26:29], v[192:195], v[224:227], v[26:29]
	s_setprio 1
	s_barrier
	ds_read_b128 v[114:117], v149
	ds_read_b128 v[118:121], v149 offset:1024
	ds_read_b128 v[122:125], v149 offset:2048
	ds_read_b128 v[152:155], v149 offset:3072
	ds_read_b128 v[156:159], v150
	ds_read_b128 v[176:179], v150 offset:1024
	ds_read_b128 v[180:183], v150 offset:2048
	ds_read_b128 v[184:187], v150 offset:3072
	s_add_u32 s36, s36, 0x18280
	s_addc_u32 s37, s37, 0
	s_mov_b32 m0, s61
	v_lshl_add_u64 v[126:127], s[36:37], 0, v[128:129]
	ds_read_b128 v[188:191], v140
	ds_read_b128 v[192:195], v140 offset:1024
	ds_read_b128 v[196:199], v140 offset:2048
	ds_read_b128 v[200:203], v140 offset:3072
	ds_read_b128 v[204:207], v140 offset:4096
	ds_read_b128 v[208:211], v140 offset:5120
	ds_read_b128 v[212:215], v140 offset:6144
	ds_read_b128 v[216:219], v140 offset:7168
	global_load_lds_dwordx4 v[126:127], off
	v_lshl_add_u64 v[126:127], s[36:37], 0, v[132:133]
	s_mov_b32 m0, s62
	s_nop 0
	global_load_lds_dwordx4 v[126:127], off
	s_waitcnt vmcnt(8)
	s_waitcnt lgkmcnt(0)
	s_barrier
	s_setprio 0
	s_waitcnt lgkmcnt(0)
	v_mfma_f32_16x16x32_bf16 v[82:85], v[122:125], v[204:207], v[82:85]
	v_mfma_f32_16x16x32_bf16 v[220:223], v[152:155], v[208:211], v[82:85]
	v_mfma_f32_16x16x32_bf16 v[82:85], v[114:117], v[212:215], v[86:89]
	v_mfma_f32_16x16x32_bf16 v[62:65], v[114:117], v[188:191], v[62:65]
	v_mfma_f32_16x16x32_bf16 v[66:69], v[122:125], v[188:191], v[66:69]
	v_mfma_f32_16x16x32_bf16 v[70:73], v[114:117], v[196:199], v[70:73]
	v_mfma_f32_16x16x32_bf16 v[74:77], v[122:125], v[196:199], v[74:77]
	v_mfma_f32_16x16x32_bf16 v[78:81], v[114:117], v[204:207], v[78:81]
	v_mfma_f32_16x16x32_bf16 v[224:227], v[118:121], v[216:219], v[82:85]
	v_mfma_f32_16x16x32_bf16 v[82:85], v[122:125], v[212:215], v[90:93]
	v_mfma_f32_16x16x32_bf16 v[62:65], v[118:121], v[192:195], v[62:65]
	v_mfma_f32_16x16x32_bf16 v[66:69], v[152:155], v[192:195], v[66:69]
	v_mfma_f32_16x16x32_bf16 v[70:73], v[118:121], v[200:203], v[70:73]
	v_mfma_f32_16x16x32_bf16 v[74:77], v[152:155], v[200:203], v[74:77]
	v_mfma_f32_16x16x32_bf16 v[78:81], v[118:121], v[208:211], v[78:81]
	v_mfma_f32_16x16x32_bf16 v[88:91], v[152:155], v[216:219], v[82:85]
	s_setprio 1
	s_setprio 0
	v_mfma_f32_16x16x32_bf16 v[82:85], v[156:159], v[188:191], v[94:97]
	v_mfma_f32_16x16x32_bf16 v[92:95], v[176:179], v[192:195], v[82:85]
	v_mfma_f32_16x16x32_bf16 v[82:85], v[180:183], v[188:191], v[98:101]
	v_mfma_f32_16x16x32_bf16 v[38:41], v[180:183], v[196:199], v[38:41]
	v_mfma_f32_16x16x32_bf16 v[42:45], v[156:159], v[204:207], v[42:45]
	v_mfma_f32_16x16x32_bf16 v[46:49], v[180:183], v[204:207], v[46:49]
	v_mfma_f32_16x16x32_bf16 v[50:53], v[156:159], v[212:215], v[50:53]
	v_mfma_f32_16x16x32_bf16 v[54:57], v[180:183], v[212:215], v[54:57]
	v_mfma_f32_16x16x32_bf16 v[188:191], v[184:187], v[192:195], v[82:85]
	v_mfma_f32_16x16x32_bf16 v[82:85], v[156:159], v[196:199], v[102:105]
	v_mfma_f32_16x16x32_bf16 v[38:41], v[184:187], v[200:203], v[38:41]
	v_mfma_f32_16x16x32_bf16 v[42:45], v[176:179], v[208:211], v[42:45]
	v_mfma_f32_16x16x32_bf16 v[46:49], v[184:187], v[208:211], v[46:49]
	v_mfma_f32_16x16x32_bf16 v[50:53], v[176:179], v[216:219], v[50:53]
	v_mfma_f32_16x16x32_bf16 v[54:57], v[184:187], v[216:219], v[54:57]
	v_mfma_f32_16x16x32_bf16 v[192:195], v[176:179], v[200:203], v[82:85]
	s_setprio 1
	s_barrier
	s_mov_b32 m0, s70
	v_lshl_add_u64 v[136:137], s[28:29], 0, v[130:131]
	s_add_u32 s36, s28, 0x1800
	ds_read_b128 v[82:85], v140 offset:16384
	ds_read_b128 v[96:99], v140 offset:17408
	ds_read_b128 v[100:103], v140 offset:18432
	ds_read_b128 v[196:199], v140 offset:19456
	ds_read_b128 v[200:203], v140 offset:20480
	ds_read_b128 v[204:207], v140 offset:21504
	ds_read_b128 v[208:211], v140 offset:22528
	ds_read_b128 v[212:215], v140 offset:23552
	global_load_lds_dwordx4 v[136:137], off
	v_lshl_add_u64 v[142:143], s[28:29], 0, v[134:135]
	s_mov_b32 m0, s67
	s_addc_u32 s37, s29, 0
	global_load_lds_dwordx4 v[142:143], off
	v_lshl_add_u64 v[86:87], s[36:37], 0, v[130:131]
	s_mov_b32 m0, s68
	v_lshl_add_u64 v[144:145], s[26:27], 0, v[128:129]
	global_load_lds_dwordx4 v[86:87], off
	v_lshl_add_u64 v[86:87], s[36:37], 0, v[134:135]
	s_mov_b32 m0, s69
	v_lshl_add_u64 v[146:147], s[26:27], 0, v[132:133]
	global_load_lds_dwordx4 v[86:87], off
	s_mov_b32 m0, s46
	s_nop 0
	global_load_lds_dwordx4 v[144:145], off
	s_mov_b32 m0, s47
	s_nop 0
	global_load_lds_dwordx4 v[146:147], off
	s_waitcnt vmcnt(8)
	s_waitcnt lgkmcnt(0)
	s_barrier
	s_setprio 0
	s_waitcnt lgkmcnt(0)
	v_mfma_f32_16x16x32_bf16 v[0:3], v[114:117], v[82:85], v[0:3]
	v_mfma_f32_16x16x32_bf16 v[4:7], v[122:125], v[82:85], v[4:7]
	v_mfma_f32_16x16x32_bf16 v[10:13], v[114:117], v[208:211], v[10:13]
	v_mfma_f32_16x16x32_bf16 v[0:3], v[118:121], v[96:99], v[0:3]
	v_mfma_f32_16x16x32_bf16 v[4:7], v[152:155], v[96:99], v[4:7]
	v_mfma_f32_16x16x32_bf16 v[160:163], v[114:117], v[100:103], v[160:163]
	v_mfma_f32_16x16x32_bf16 v[164:167], v[122:125], v[100:103], v[164:167]
	v_mfma_f32_16x16x32_bf16 v[168:171], v[114:117], v[200:203], v[168:171]
	v_mfma_f32_16x16x32_bf16 v[172:175], v[122:125], v[200:203], v[172:175]
	v_mfma_f32_16x16x32_bf16 v[10:13], v[118:121], v[212:215], v[10:13]
	v_mfma_f32_16x16x32_bf16 v[14:17], v[122:125], v[208:211], v[14:17]
	v_mfma_f32_16x16x32_bf16 v[160:163], v[118:121], v[196:199], v[160:163]
	v_mfma_f32_16x16x32_bf16 v[164:167], v[152:155], v[196:199], v[164:167]
	v_mfma_f32_16x16x32_bf16 v[168:171], v[118:121], v[204:207], v[168:171]
	v_mfma_f32_16x16x32_bf16 v[172:175], v[152:155], v[204:207], v[172:175]
	v_mfma_f32_16x16x32_bf16 v[152:155], v[152:155], v[212:215], v[14:17]
	s_setprio 1
	s_setprio 0
	v_mfma_f32_16x16x32_bf16 v[14:17], v[156:159], v[82:85], v[18:21]
	v_mfma_f32_16x16x32_bf16 v[216:219], v[176:179], v[96:99], v[14:17]
	v_mfma_f32_16x16x32_bf16 v[14:17], v[180:183], v[82:85], v[30:33]
	v_mfma_f32_16x16x32_bf16 v[228:231], v[184:187], v[96:99], v[14:17]
	v_mfma_f32_16x16x32_bf16 v[14:17], v[156:159], v[100:103], v[34:37]
	v_mfma_f32_16x16x32_bf16 v[232:235], v[176:179], v[196:199], v[14:17]
	v_mfma_f32_16x16x32_bf16 v[14:17], v[180:183], v[100:103], v[58:61]
	v_mfma_f32_16x16x32_bf16 v[196:199], v[184:187], v[196:199], v[14:17]
	v_mfma_f32_16x16x32_bf16 v[14:17], v[156:159], v[200:203], v[106:109]
	v_mfma_f32_16x16x32_bf16 v[236:239], v[176:179], v[204:207], v[14:17]
	v_mfma_f32_16x16x32_bf16 v[14:17], v[180:183], v[200:203], v[110:113]
	v_mfma_f32_16x16x32_bf16 v[200:203], v[184:187], v[204:207], v[14:17]
	v_mfma_f32_16x16x32_bf16 v[14:17], v[156:159], v[208:211], v[22:25]
	v_mfma_f32_16x16x32_bf16 v[156:159], v[176:179], v[212:215], v[14:17]
	v_mfma_f32_16x16x32_bf16 v[14:17], v[180:183], v[208:211], v[26:29]
	v_mfma_f32_16x16x32_bf16 v[176:179], v[184:187], v[212:215], v[14:17]
	s_setprio 1
	s_barrier
	ds_read_b128 v[24:27], v8
	ds_read_b128 v[28:31], v8 offset:1024
	ds_read_b128 v[58:61], v8 offset:2048
	ds_read_b128 v[180:183], v8 offset:3072
	ds_read_b128 v[184:187], v9
	ds_read_b128 v[204:207], v9 offset:1024
	ds_read_b128 v[208:211], v9 offset:2048
	ds_read_b128 v[212:215], v9 offset:3072
	s_add_u32 s36, s26, 0x18000
	s_addc_u32 s37, s27, 0
	s_mov_b32 m0, s49
	v_lshl_add_u64 v[8:9], s[36:37], 0, v[128:129]
	ds_read_b128 v[14:17], v140 offset:32768
	ds_read_b128 v[18:21], v140 offset:33792
	ds_read_b128 v[32:35], v140 offset:34816
	ds_read_b128 v[108:111], v140 offset:35840
	ds_read_b128 v[240:243], v140 offset:36864
	ds_read_b128 v[244:247], v140 offset:37888
	ds_read_b128 v[248:251], v140 offset:38912
	ds_read_b128 v[252:255], v140 offset:39936
	global_load_lds_dwordx4 v[8:9], off
	v_lshl_add_u64 v[8:9], s[36:37], 0, v[132:133]
	s_mov_b32 m0, s50
	s_nop 0
	global_load_lds_dwordx4 v[8:9], off
	s_waitcnt vmcnt(8)
	s_waitcnt lgkmcnt(0)
	s_barrier
	s_setprio 0
	s_waitcnt lgkmcnt(0)
	v_mfma_f32_16x16x32_bf16 v[62:65], v[24:27], v[14:17], v[62:65]
	v_mfma_f32_16x16x32_bf16 v[112:115], v[28:31], v[18:21], v[62:65]
	v_mfma_f32_16x16x32_bf16 v[62:65], v[58:61], v[14:17], v[66:69]
	v_mfma_f32_16x16x32_bf16 v[116:119], v[180:183], v[18:21], v[62:65]
	v_mfma_f32_16x16x32_bf16 v[62:65], v[24:27], v[32:35], v[70:73]
	v_mfma_f32_16x16x32_bf16 v[96:99], v[28:31], v[108:111], v[62:65]
	v_mfma_f32_16x16x32_bf16 v[62:65], v[58:61], v[32:35], v[74:77]
	v_mfma_f32_16x16x32_bf16 v[100:103], v[180:183], v[108:111], v[62:65]
	v_mfma_f32_16x16x32_bf16 v[62:65], v[24:27], v[240:243], v[78:81]
	v_mfma_f32_16x16x32_bf16 v[80:83], v[28:31], v[244:247], v[62:65]
	v_mfma_f32_16x16x32_bf16 v[62:65], v[58:61], v[240:243], v[220:223]
	v_mfma_f32_16x16x32_bf16 v[84:87], v[180:183], v[244:247], v[62:65]
	v_mfma_f32_16x16x32_bf16 v[62:65], v[24:27], v[248:251], v[224:227]
	v_mfma_f32_16x16x32_bf16 v[68:71], v[58:61], v[248:251], v[88:91]
	v_mfma_f32_16x16x32_bf16 v[64:67], v[28:31], v[252:255], v[62:65]
	v_mfma_f32_16x16x32_bf16 v[68:71], v[180:183], v[252:255], v[68:71]
	s_setprio 1
	s_setprio 0
	v_mfma_f32_16x16x32_bf16 v[72:75], v[184:187], v[14:17], v[92:95]
	v_mfma_f32_16x16x32_bf16 v[14:17], v[208:211], v[14:17], v[188:191]
	v_mfma_f32_16x16x32_bf16 v[124:127], v[212:215], v[18:21], v[14:17]
	v_mfma_f32_16x16x32_bf16 v[14:17], v[184:187], v[32:35], v[192:195]
	v_mfma_f32_16x16x32_bf16 v[104:107], v[204:207], v[108:111], v[14:17]
	v_mfma_f32_16x16x32_bf16 v[14:17], v[208:211], v[32:35], v[38:41]
	v_mfma_f32_16x16x32_bf16 v[108:111], v[212:215], v[108:111], v[14:17]
	v_mfma_f32_16x16x32_bf16 v[14:17], v[184:187], v[240:243], v[42:45]
	v_mfma_f32_16x16x32_bf16 v[88:91], v[204:207], v[244:247], v[14:17]
	v_mfma_f32_16x16x32_bf16 v[14:17], v[208:211], v[240:243], v[46:49]
	v_mfma_f32_16x16x32_bf16 v[92:95], v[212:215], v[244:247], v[14:17]
	v_mfma_f32_16x16x32_bf16 v[14:17], v[184:187], v[248:251], v[50:53]
	v_mfma_f32_16x16x32_bf16 v[120:123], v[204:207], v[18:21], v[72:75]
	v_mfma_f32_16x16x32_bf16 v[72:75], v[204:207], v[252:255], v[14:17]
	v_mfma_f32_16x16x32_bf16 v[14:17], v[208:211], v[248:251], v[54:57]
	v_mfma_f32_16x16x32_bf16 v[76:79], v[212:215], v[252:255], v[14:17]
	s_setprio 1
	s_barrier
	s_mov_b32 m0, s74
	v_lshl_add_u64 v[8:9], v[136:137], 0, s[14:15]
	s_add_u32 s36, s28, 0x1880
	ds_read_b128 v[40:43], v140 offset:49152
	ds_read_b128 v[44:47], v140 offset:50176
	ds_read_b128 v[188:191], v140 offset:51200
	ds_read_b128 v[192:195], v140 offset:52224
	ds_read_b128 v[220:223], v140 offset:53248
	ds_read_b128 v[224:227], v140 offset:54272
	ds_read_b128 v[240:243], v140 offset:55296
	ds_read_b128 v[244:247], v140 offset:56320
	global_load_lds_dwordx4 v[8:9], off
	v_lshl_add_u64 v[8:9], v[142:143], 0, s[14:15]
	s_mov_b32 m0, s71
	s_addc_u32 s37, s29, 0
	global_load_lds_dwordx4 v[8:9], off
	v_lshl_add_u64 v[8:9], s[36:37], 0, v[130:131]
	s_mov_b32 m0, s72
	s_nop 0
	global_load_lds_dwordx4 v[8:9], off
	v_lshl_add_u64 v[8:9], s[36:37], 0, v[134:135]
	s_mov_b32 m0, s73
	s_nop 0
	global_load_lds_dwordx4 v[8:9], off
	v_lshl_add_u64 v[8:9], v[144:145], 0, s[14:15]
	s_mov_b32 m0, s52
	s_nop 0
	global_load_lds_dwordx4 v[8:9], off
	v_lshl_add_u64 v[8:9], v[146:147], 0, s[14:15]
	s_mov_b32 m0, s53
	s_nop 0
	global_load_lds_dwordx4 v[8:9], off
	s_waitcnt vmcnt(8)
	s_waitcnt lgkmcnt(0)
	s_barrier
	s_setprio 0
	s_waitcnt lgkmcnt(0)
	v_mfma_f32_16x16x32_bf16 v[0:3], v[24:27], v[40:43], v[0:3]
	v_mfma_f32_16x16x32_bf16 v[48:51], v[28:31], v[44:47], v[0:3]
	v_mfma_f32_16x16x32_bf16 v[0:3], v[58:61], v[40:43], v[4:7]
	v_mfma_f32_16x16x32_bf16 v[52:55], v[180:183], v[44:47], v[0:3]
	v_mfma_f32_16x16x32_bf16 v[0:3], v[24:27], v[188:191], v[160:163]
	v_mfma_f32_16x16x32_bf16 v[32:35], v[28:31], v[192:195], v[0:3]
	v_mfma_f32_16x16x32_bf16 v[0:3], v[58:61], v[188:191], v[164:167]
	v_mfma_f32_16x16x32_bf16 v[36:39], v[180:183], v[192:195], v[0:3]
	v_mfma_f32_16x16x32_bf16 v[0:3], v[24:27], v[220:223], v[168:171]
	v_mfma_f32_16x16x32_bf16 v[16:19], v[28:31], v[224:227], v[0:3]
	v_mfma_f32_16x16x32_bf16 v[0:3], v[58:61], v[220:223], v[172:175]
	v_mfma_f32_16x16x32_bf16 v[20:23], v[180:183], v[224:227], v[0:3]
	v_mfma_f32_16x16x32_bf16 v[0:3], v[24:27], v[240:243], v[10:13]
	v_mfma_f32_16x16x32_bf16 v[4:7], v[58:61], v[240:243], v[152:155]
	v_mfma_f32_16x16x32_bf16 v[0:3], v[28:31], v[244:247], v[0:3]
	v_mfma_f32_16x16x32_bf16 v[4:7], v[180:183], v[244:247], v[4:7]
	s_setprio 1
	s_setprio 0
	v_mfma_f32_16x16x32_bf16 v[8:11], v[184:187], v[40:43], v[216:219]
	v_mfma_f32_16x16x32_bf16 v[56:59], v[204:207], v[44:47], v[8:11]
	v_mfma_f32_16x16x32_bf16 v[8:11], v[208:211], v[40:43], v[228:231]
	v_mfma_f32_16x16x32_bf16 v[60:63], v[212:215], v[44:47], v[8:11]
	v_mfma_f32_16x16x32_bf16 v[8:11], v[184:187], v[188:191], v[232:235]
	v_mfma_f32_16x16x32_bf16 v[40:43], v[204:207], v[192:195], v[8:11]
	v_mfma_f32_16x16x32_bf16 v[8:11], v[208:211], v[188:191], v[196:199]
	v_mfma_f32_16x16x32_bf16 v[44:47], v[212:215], v[192:195], v[8:11]
	v_mfma_f32_16x16x32_bf16 v[8:11], v[184:187], v[220:223], v[236:239]
	v_mfma_f32_16x16x32_bf16 v[24:27], v[204:207], v[224:227], v[8:11]
	v_mfma_f32_16x16x32_bf16 v[8:11], v[208:211], v[220:223], v[200:203]
	v_mfma_f32_16x16x32_bf16 v[28:31], v[212:215], v[224:227], v[8:11]
	v_mfma_f32_16x16x32_bf16 v[8:11], v[184:187], v[240:243], v[156:159]
	v_mfma_f32_16x16x32_bf16 v[12:15], v[208:211], v[240:243], v[176:179]
	v_mfma_f32_16x16x32_bf16 v[8:11], v[204:207], v[244:247], v[8:11]
	v_mfma_f32_16x16x32_bf16 v[12:15], v[212:215], v[244:247], v[12:15]
	s_setprio 1
	s_barrier
	s_andn2_b64 vcc, exec, s[16:17]
	s_cbranch_vccnz .LBB0_4461
	s_barrier
